# DPP/permlane butterflies also in norm1, final combine and fused epilogue reductions
# speedup vs baseline: 1.0067x; 1.0067x over previous
; __device__ __forceinline__ unsigned pk2(float lo, float hi) { unsigned r; asm("v_cvt_pk_bf16_f32 %0, %1, %2" : "=v"(r) : "v"(lo), "v"(hi)); return r; }
; __device__ __forceinline__ float bflo(unsigned u) { return __uint_as_float(u << 16); }
; __device__ __forceinline__ float bfhi(unsigned u) { return __uint_as_float(u & 0xffff0000u); }
; __device__ __forceinline__ float wave_sum(float v) {
; #pragma unroll
;     for (int o = 1; o < 64; o <<= 1) v += __shfl_xor(v, o);
;     return v;
; }
; __device__ __forceinline__ void ph_norm1(const Params& p, int mode, LAS unsigned char* lds) {
;     ...
;             f32x4 v[8];
; #pragma unroll
;             for (int j = 0; j < 8; ++j) { const f32x4 g = gfv[j];
;                 v[j] = (f32x4){bflo(xw[q][j].x), bfhi(xw[q][j].x), bflo(xw[q][j].y), bfhi(xw[q][j].y)} + g * macc[j]; }
;             if (mode == 1) {
;                 bf16_t* xo = (bf16_t*)(p.ws + WS_X) + (size_t)t * DM;
; #pragma unroll
;                 for (int j = 0; j < 8; ++j) { u32x2 w; w.x = pk2(v[j][0], v[j][1]); w.y = pk2(v[j][2], v[j][3]); *(u32x2*)(xo + 4 * lane + 256 * j) = w;
;                     v[j] = (f32x4){bflo(w.x), bfhi(w.x), bflo(w.y), bfhi(w.y)}; }
;             }
;             float ss = 0.f;
; #pragma unroll
;             for (int j = 0; j < 8; ++j) ss += v[j][0] * v[j][0] + v[j][1] * v[j][1] + v[j][2] * v[j][2] + v[j][3] * v[j][3];
;             const float r = 1.0f / sqrtf(wave_sum(ss) * (1.f / DM) + EPS);
.LBB0_343:
	v_lshlrev_b32_e32 v16, 16, v68
	v_and_b32_e32 v17, 0xffff0000, v68
	v_pk_fma_f32 v[16:17], v[34:35], v[96:97], v[16:17]
	v_lshlrev_b32_e32 v34, 16, v66
	v_and_b32_e32 v35, 0xffff0000, v66
	v_pk_fma_f32 v[30:31], v[30:31], v[92:93], v[34:35]
	v_lshlrev_b32_e32 v34, 16, v64
	v_and_b32_e32 v35, 0xffff0000, v64
	v_pk_fma_f32 v[26:27], v[26:27], v[88:89], v[34:35]
	v_lshlrev_b32_e32 v34, 16, v62
	v_and_b32_e32 v35, 0xffff0000, v62
	v_lshlrev_b32_e32 v64, 16, v65
	v_and_b32_e32 v65, 0xffff0000, v65
	v_lshlrev_b32_e32 v62, 16, v63
	v_and_b32_e32 v63, 0xffff0000, v63
	v_pk_fma_f32 v[34:35], v[22:23], v[84:85], v[34:35]
	v_lshlrev_b32_e32 v22, 16, v60
	v_and_b32_e32 v23, 0xffff0000, v60
	v_lshlrev_b32_e32 v66, 16, v67
	v_and_b32_e32 v67, 0xffff0000, v67
	v_pk_fma_f32 v[28:29], v[28:29], v[90:91], v[64:65]
	v_pk_fma_f32 v[62:63], v[24:25], v[86:87], v[62:63]
	v_lshlrev_b32_e32 v24, 16, v61
	v_and_b32_e32 v25, 0xffff0000, v61
	v_pk_fma_f32 v[64:65], v[18:19], v[80:81], v[22:23]
	v_lshlrev_b32_e32 v18, 16, v58
	v_and_b32_e32 v19, 0xffff0000, v58
	v_lshlrev_b32_e32 v68, 16, v69
	v_and_b32_e32 v69, 0xffff0000, v69
	v_pk_fma_f32 v[32:33], v[32:33], v[94:95], v[66:67]
	v_pk_fma_f32 v[60:61], v[20:21], v[82:83], v[24:25]
	v_lshlrev_b32_e32 v20, 16, v59
	v_and_b32_e32 v21, 0xffff0000, v59
	v_pk_fma_f32 v[66:67], v[10:11], v[76:77], v[18:19]
	v_lshlrev_b32_e32 v10, 16, v56
	v_and_b32_e32 v11, 0xffff0000, v56
	v_pk_fma_f32 v[36:37], v[36:37], v[98:99], v[68:69]
	v_pk_fma_f32 v[58:59], v[12:13], v[78:79], v[20:21]
	v_lshlrev_b32_e32 v12, 16, v57
	v_and_b32_e32 v13, 0xffff0000, v57
	v_pk_fma_f32 v[6:7], v[6:7], v[72:73], v[10:11]
	v_lshlrev_b32_e32 v10, 16, v54
	v_and_b32_e32 v11, 0xffff0000, v54
	v_pk_fma_f32 v[8:9], v[8:9], v[74:75], v[12:13]
	v_lshlrev_b32_e32 v12, 16, v55
	v_and_b32_e32 v13, 0xffff0000, v55
	v_pk_fma_f32 v[54:55], v[2:3], v[70:71], v[10:11]
	v_cvt_pk_bf16_f32 v56, v16, v17
	v_cvt_pk_bf16_f32 v57, v36, v37
	v_cvt_pk_bf16_f32 v30, v30, v31
	v_cvt_pk_bf16_f32 v26, v26, v27
	v_cvt_pk_bf16_f32 v27, v28, v29
	v_cvt_pk_bf16_f32 v28, v34, v35
	s_nop 0
	v_and_b32_e32 v37, 0xffff0000, v56
	v_and_b32_e32 v71, 0xffff0000, v30
	v_lshlrev_b32_e32 v36, 16, v56
	v_lshlrev_b32_e32 v70, 16, v30
	v_cvt_pk_bf16_f32 v35, v58, v59
	v_cvt_pk_bf16_f32 v58, v6, v7
	v_mul_f32_e32 v6, v37, v37
	v_mul_f32_e32 v7, v71, v71
	v_lshlrev_b32_e32 v68, 16, v57
	v_cvt_pk_bf16_f32 v31, v32, v33
	v_fmac_f32_e32 v6, v36, v36
	v_lshlrev_b32_e32 v72, 16, v31
	v_fmac_f32_e32 v7, v70, v70
	v_and_b32_e32 v69, 0xffff0000, v57
	v_and_b32_e32 v73, 0xffff0000, v31
	v_fmac_f32_e32 v6, v68, v68
	v_fmac_f32_e32 v7, v72, v72
	v_and_b32_e32 v23, 0xffff0000, v26
	v_fmac_f32_e32 v6, v69, v69
	v_fmac_f32_e32 v7, v73, v73
	v_lshlrev_b32_e32 v22, 16, v26
	v_add_f32_e32 v6, v6, v7
	v_mul_f32_e32 v7, v23, v23
	v_lshlrev_b32_e32 v24, 16, v27
	v_fmac_f32_e32 v7, v22, v22
	v_and_b32_e32 v25, 0xffff0000, v27
	v_fmac_f32_e32 v7, v24, v24
	v_and_b32_e32 v19, 0xffff0000, v28
	v_fmac_f32_e32 v7, v25, v25
	v_lshlrev_b32_e32 v18, 16, v28
	v_add_f32_e32 v6, v6, v7
	v_mul_f32_e32 v7, v19, v19
	v_cvt_pk_bf16_f32 v29, v62, v63
	v_fmac_f32_e32 v7, v18, v18
	v_lshlrev_b32_e32 v20, 16, v29
	v_and_b32_e32 v21, 0xffff0000, v29
	v_fmac_f32_e32 v7, v20, v20
	v_cvt_pk_bf16_f32 v32, v64, v65
	v_fmac_f32_e32 v7, v21, v21
	v_and_b32_e32 v11, 0xffff0000, v32
	v_lshlrev_b32_e32 v10, 16, v32
	v_add_f32_e32 v6, v6, v7
	v_mul_f32_e32 v7, v11, v11
	v_pk_fma_f32 v[14:15], v[4:5], v[14:15], v[12:13]
	v_cvt_pk_bf16_f32 v33, v60, v61
	v_fmac_f32_e32 v7, v10, v10
	v_lshlrev_b32_e32 v12, 16, v33
	v_and_b32_e32 v13, 0xffff0000, v33
	v_fmac_f32_e32 v7, v12, v12
	v_cvt_pk_bf16_f32 v34, v66, v67
	v_fmac_f32_e32 v7, v13, v13
	v_and_b32_e32 v3, 0xffff0000, v34
	v_lshlrev_b32_e32 v2, 16, v34
	v_add_f32_e32 v6, v6, v7
	v_mul_f32_e32 v7, v3, v3
	v_lshlrev_b32_e32 v4, 16, v35
	v_fmac_f32_e32 v7, v2, v2
	v_and_b32_e32 v5, 0xffff0000, v35
	v_fmac_f32_e32 v7, v4, v4
	v_cvt_pk_bf16_f32 v59, v8, v9
	v_cvt_pk_bf16_f32 v54, v54, v55
	v_fmac_f32_e32 v7, v5, v5
	v_and_b32_e32 v9, 0xffff0000, v54
	v_and_b32_e32 v8, 0xffff0000, v58
	v_add_f32_e32 v62, v6, v7
	v_lshlrev_b32_e32 v6, 16, v58
	v_lshlrev_b32_e32 v7, 16, v54
	v_pk_mul_f32 v[60:61], v[8:9], v[8:9]
	v_cvt_pk_bf16_f32 v55, v14, v15
	v_lshlrev_b32_e32 v14, 16, v59
	v_lshlrev_b32_e32 v15, 16, v55
	v_pk_fma_f32 v[60:61], v[6:7], v[6:7], v[60:61]
	v_and_b32_e32 v17, 0xffff0000, v55
	v_and_b32_e32 v16, 0xffff0000, v59
	v_pk_fma_f32 v[60:61], v[14:15], v[14:15], v[60:61]
	s_movk_i32 s0, 0x1fff
	v_pk_fma_f32 v[60:61], v[16:17], v[16:17], v[60:61]
	s_nop 0
	v_add_f32_e32 v60, v62, v60
	v_add_f32_e32 v60, v60, v61
	s_waitcnt lgkmcnt(0)
	s_nop 1
	v_add_f32_dpp v39, v60, v60 quad_perm:[1,0,3,2] row_mask:0xf bank_mask:0xf
	s_waitcnt lgkmcnt(0)
	s_nop 1
	v_add_f32_dpp v39, v39, v39 quad_perm:[2,3,0,1] row_mask:0xf bank_mask:0xf
	s_waitcnt lgkmcnt(0)
	s_nop 1
	v_add_f32_dpp v39, v39, v39 row_half_mirror row_mask:0xf bank_mask:0xf
	s_waitcnt lgkmcnt(0)
	s_nop 1
	v_add_f32_dpp v39, v39, v39 row_mirror row_mask:0xf bank_mask:0xf
	v_mov_b32_e32 v62, v39
	s_nop 1
	v_permlane16_swap_b32_e32 v39, v62
	v_or_b32_e32 v60, 3, v38
	v_ashrrev_i32_e32 v61, 31, v60
	v_lshlrev_b64 v[60:61], 12, v[60:61]
	v_add_u32_e32 v38, s20, v38
	s_waitcnt lgkmcnt(0)
; #define LAS __attribute__((address_space(3)))
; __device__ __forceinline__ unsigned pk2(float lo, float hi) { unsigned r; asm("v_cvt_pk_bf16_f32 %0, %1, %2" : "=v"(r) : "v"(lo), "v"(hi)); return r; }
; __device__ __forceinline__ float bflo(unsigned u) { return __uint_as_float(u << 16); }
; __device__ __forceinline__ float bfhi(unsigned u) { return __uint_as_float(u & 0xffff0000u); }
; __device__ __forceinline__ float wave_sum(float v) {
; #pragma unroll
;     for (int o = 1; o < 64; o <<= 1) v += __shfl_xor(v, o);
;     return v;
; }
; __device__ __forceinline__ void ph_norm1(const Params& p, int mode, LAS unsigned char* lds) {
;     ...
;                 bf16_t* xo = (bf16_t*)(p.ws + WS_X) + (size_t)t * DM;
; #pragma unroll
;                 for (int j = 0; j < 8; ++j) { u32x2 w; w.x = pk2(v[j][0], v[j][1]); w.y = pk2(v[j][2], v[j][3]); *(u32x2*)(xo + 4 * lane + 256 * j) = w;
;                     v[j] = (f32x4){bflo(w.x), bfhi(w.x), bflo(w.y), bfhi(w.y)}; }
;             }
;             float ss = 0.f;
; #pragma unroll
;             for (int j = 0; j < 8; ++j) ss += v[j][0] * v[j][0] + v[j][1] * v[j][1] + v[j][2] * v[j][2] + v[j][3] * v[j][3];
;             const float r = 1.0f / sqrtf(wave_sum(ss) * (1.f / DM) + EPS);
;             asm volatile("" ::: "memory");
;             if (mode == 2) {
;                 float* o = p.out + (size_t)t * DM;
; #pragma unroll
;                 for (int j = 0; j < 8; ++j) { const f32x4 g = fgv[j]; __builtin_nontemporal_store(v[j] * r * g, (f32x4*)(o + 4 * lane + 256 * j)); }
;             } else {
;                 const float* g1 = p.in[5] + (size_t)DM;
;                 const float* sh = mod + ((size_t)4 + b) * 12288;
;                 const float* sc = sh + 2048;
;                 bf16_t* ho = (bf16_t*)(p.ws + WS_H) + (size_t)t * DM;
; #pragma unroll
;                 for (int j = 0; j < 8; ++j) {
;                     const f32x4 h = (v[j] * r) * *(const LAS f32x4*)(T1 + 4 * lane + 256 * j) + *(const LAS f32x4*)(T2 + 4 * lane + 256 * j);
;                     u32x2 w; w.x = pk2(h[0], h[1]); w.y = pk2(h[2], h[3]);
;                     *(u32x2*)(ho + 4 * lane + 256 * j) = w;
;                 }
	v_add_f32_e32 v39, v39, v62
	ds_bpermute_b32 v64, v142, v39
	v_lshl_add_u64 v[62:63], v[48:49], 0, v[60:61]
	global_store_dwordx2 v[62:63], v[56:57], off
	global_store_dwordx2 v[62:63], v[30:31], off offset:512
	global_store_dwordx2 v[62:63], v[26:27], off offset:1024
	global_store_dwordx2 v[62:63], v[28:29], off offset:1536
	global_store_dwordx2 v[62:63], v[32:33], off offset:2048
	global_store_dwordx2 v[62:63], v[34:35], off offset:2560
	global_store_dwordx2 v[62:63], v[58:59], off offset:3072
	global_store_dwordx2 v[62:63], v[54:55], off offset:3584
	s_waitcnt lgkmcnt(0)
	v_add_f32_e32 v30, v39, v64
	v_fmamk_f32 v30, v30, 0x3a000000, v217
	v_mul_f32_e32 v31, 0x4f800000, v30
	v_cmp_gt_f32_e32 vcc, s5, v30
	v_lshl_add_u64 v[60:61], v[50:51], 0, v[60:61]
	s_nop 0
	v_cndmask_b32_e32 v30, v30, v31, vcc
	v_sqrt_f32_e32 v31, v30
	s_nop 0
	v_add_u32_e32 v26, -1, v31
	v_fma_f32 v27, -v26, v31, v30
	v_cmp_ge_f32_e64 s[34:35], 0, v27
	v_add_u32_e32 v27, 1, v31
	v_fma_f32 v28, -v27, v31, v30
	v_cndmask_b32_e64 v26, v31, v26, s[34:35]
	v_cmp_lt_f32_e64 s[34:35], 0, v28
	s_nop 1
	v_cndmask_b32_e64 v26, v26, v27, s[34:35]
	v_mul_f32_e32 v27, 0x37800000, v26
	v_cndmask_b32_e32 v26, v26, v27, vcc
	v_cmp_class_f32_e32 vcc, v30, v219
	s_nop 1
	v_cndmask_b32_e32 v26, v26, v30, vcc
	v_div_scale_f32 v27, s[8:9], v26, v26, 1.0
	v_rcp_f32_e32 v28, v27
	s_nop 0
	v_fma_f32 v29, -v27, v28, 1.0
	v_fmac_f32_e32 v28, v29, v28
	v_div_scale_f32 v29, vcc, 1.0, v26, 1.0
	v_mul_f32_e32 v30, v29, v28
	v_fma_f32 v31, -v27, v30, v29
	v_fmac_f32_e32 v30, v31, v28
	v_fma_f32 v27, -v27, v30, v29
	v_div_fmas_f32 v27, v27, v28, v30
	v_div_fixup_f32 v58, v27, v26, 1.0
	ds_read_b128 v[26:29], v153
	ds_read_b128 v[30:33], v153 offset:8192
	v_pk_mul_f32 v[62:63], v[58:59], v[36:37] op_sel_hi:[0,1]
	ds_read_b128 v[34:37], v153 offset:1024
	ds_read_b128 v[54:57], v153 offset:9216
	v_pk_mul_f32 v[64:65], v[58:59], v[68:69] op_sel_hi:[0,1]
	v_pk_mul_f32 v[18:19], v[58:59], v[18:19] op_sel_hi:[0,1]
	s_waitcnt lgkmcnt(2)
	v_pk_fma_f32 v[26:27], v[26:27], v[62:63], v[30:31]
	v_pk_fma_f32 v[28:29], v[28:29], v[64:65], v[32:33]
	v_cvt_pk_bf16_f32 v26, v26, v27
	v_pk_mul_f32 v[20:21], v[58:59], v[20:21] op_sel_hi:[0,1]
	v_cvt_pk_bf16_f32 v27, v28, v29
	global_store_dwordx2 v[60:61], v[26:27], off
	v_pk_mul_f32 v[26:27], v[58:59], v[70:71] op_sel_hi:[0,1]
	v_pk_mul_f32 v[28:29], v[58:59], v[72:73] op_sel_hi:[0,1]
	s_waitcnt lgkmcnt(0)
	v_pk_fma_f32 v[26:27], v[34:35], v[26:27], v[54:55]
	v_pk_fma_f32 v[28:29], v[36:37], v[28:29], v[56:57]
	v_cvt_pk_bf16_f32 v26, v26, v27
	v_pk_mul_f32 v[54:55], v[58:59], v[22:23] op_sel_hi:[0,1]
	v_cvt_pk_bf16_f32 v27, v28, v29
	global_store_dwordx2 v[60:61], v[26:27], off offset:512
	ds_read_b128 v[26:29], v153 offset:2048
	ds_read_b128 v[30:33], v153 offset:10240
	v_pk_mul_f32 v[56:57], v[58:59], v[24:25] op_sel_hi:[0,1]
	ds_read_b128 v[22:25], v153 offset:3072
	ds_read_b128 v[34:37], v153 offset:11264
	v_pk_mul_f32 v[2:3], v[58:59], v[2:3] op_sel_hi:[0,1]
	v_pk_mul_f32 v[4:5], v[58:59], v[4:5] op_sel_hi:[0,1]
	s_waitcnt lgkmcnt(2)
	v_pk_fma_f32 v[26:27], v[54:55], v[26:27], v[30:31]
	v_pk_fma_f32 v[28:29], v[56:57], v[28:29], v[32:33]
	s_waitcnt lgkmcnt(0)
	v_pk_fma_f32 v[18:19], v[18:19], v[22:23], v[34:35]
	v_cvt_pk_bf16_f32 v26, v26, v27
	v_cvt_pk_bf16_f32 v27, v28, v29
	global_store_dwordx2 v[60:61], v[26:27], off offset:1024
	v_pk_fma_f32 v[20:21], v[20:21], v[24:25], v[36:37]
	v_cvt_pk_bf16_f32 v18, v18, v19
	v_pk_mul_f32 v[30:31], v[58:59], v[10:11] op_sel_hi:[0,1]
	v_cvt_pk_bf16_f32 v19, v20, v21
	global_store_dwordx2 v[60:61], v[18:19], off offset:1536
	ds_read_b128 v[18:21], v153 offset:4096
	ds_read_b128 v[22:25], v153 offset:12288
	v_pk_mul_f32 v[32:33], v[58:59], v[12:13] op_sel_hi:[0,1]
	ds_read_b128 v[10:13], v153 offset:5120
	ds_read_b128 v[26:29], v153 offset:13312
	v_cmp_lt_i32_e32 vcc, s0, v38
	s_or_b64 s[38:39], vcc, s[38:39]
	s_waitcnt lgkmcnt(2)
	v_pk_fma_f32 v[18:19], v[30:31], v[18:19], v[22:23]
	v_pk_fma_f32 v[20:21], v[32:33], v[20:21], v[24:25]
	s_waitcnt lgkmcnt(0)
	v_pk_fma_f32 v[2:3], v[2:3], v[10:11], v[26:27]
	v_pk_fma_f32 v[4:5], v[4:5], v[12:13], v[28:29]
	v_cvt_pk_bf16_f32 v2, v2, v3
	v_cvt_pk_bf16_f32 v18, v18, v19
	v_cvt_pk_bf16_f32 v19, v20, v21
	global_store_dwordx2 v[60:61], v[18:19], off offset:2048
	v_cvt_pk_bf16_f32 v3, v4, v5
	global_store_dwordx2 v[60:61], v[2:3], off offset:2560
	v_mov_b32_e32 v2, v6
	v_mov_b32_e32 v3, v8
	v_pk_mul_f32 v[26:27], v[58:59], v[2:3] op_sel_hi:[0,1]
	ds_read_b128 v[2:5], v153 offset:6144
	ds_read_b128 v[10:13], v153 offset:14336
	v_mov_b32_e32 v18, v14
	v_mov_b32_e32 v19, v16
	v_pk_mul_f32 v[28:29], v[58:59], v[18:19] op_sel_hi:[0,1]
	ds_read_b128 v[18:21], v153 offset:7168
	ds_read_b128 v[22:25], v153 offset:15360
	s_waitcnt lgkmcnt(2)
	v_pk_fma_f32 v[2:3], v[26:27], v[2:3], v[10:11]
	v_pk_fma_f32 v[4:5], v[28:29], v[4:5], v[12:13]
	v_cvt_pk_bf16_f32 v2, v2, v3
	v_mov_b32_e32 v8, v7
	v_cvt_pk_bf16_f32 v3, v4, v5
	global_store_dwordx2 v[60:61], v[2:3], off offset:3072
	v_pk_mul_f32 v[2:3], v[58:59], v[8:9] op_sel_hi:[0,1]
	v_mov_b32_e32 v16, v15
	v_pk_mul_f32 v[4:5], v[58:59], v[16:17] op_sel_hi:[0,1]
	s_waitcnt lgkmcnt(0)
	v_pk_fma_f32 v[2:3], v[2:3], v[18:19], v[22:23]
	v_pk_fma_f32 v[4:5], v[4:5], v[20:21], v[24:25]
	v_cvt_pk_bf16_f32 v2, v2, v3
	s_nop 0
	v_cvt_pk_bf16_f32 v3, v4, v5
	global_store_dwordx2 v[60:61], v[2:3], off offset:3584
	s_andn2_b64 exec, exec, s[38:39]
	s_cbranch_execz .LBB0_359

; __device__ __forceinline__ unsigned pk2(float lo, float hi) { unsigned r; asm("v_cvt_pk_bf16_f32 %0, %1, %2" : "=v"(r) : "v"(lo), "v"(hi)); return r; }
; __device__ __forceinline__ float bflo(unsigned u) { return __uint_as_float(u << 16); }
; __device__ __forceinline__ float bfhi(unsigned u) { return __uint_as_float(u & 0xffff0000u); }
; __device__ __forceinline__ void ph_norm1(const Params& p, int mode, LAS unsigned char* lds) {
;     ...
;             f32x4 v[8];
; #pragma unroll
;             for (int j = 0; j < 8; ++j) { const f32x4 g = gfv[j];
;                 v[j] = (f32x4){bflo(xw[q][j].x), bfhi(xw[q][j].x), bflo(xw[q][j].y), bfhi(xw[q][j].y)} + g * macc[j]; }
;             if (mode == 1) {
;                 bf16_t* xo = (bf16_t*)(p.ws + WS_X) + (size_t)t * DM;
; #pragma unroll
;                 for (int j = 0; j < 8; ++j) { u32x2 w; w.x = pk2(v[j][0], v[j][1]); w.y = pk2(v[j][2], v[j][3]); *(u32x2*)(xo + 4 * lane + 256 * j) = w;
;                     v[j] = (f32x4){bflo(w.x), bfhi(w.x), bflo(w.y), bfhi(w.y)}; }
;             }
;             float ss = 0.f;
; #pragma unroll
;             for (int j = 0; j < 8; ++j) ss += v[j][0] * v[j][0] + v[j][1] * v[j][1] + v[j][2] * v[j][2] + v[j][3] * v[j][3];
;             const float r = 1.0f / sqrtf(wave_sum(ss) * (1.f / DM) + EPS);
.LBB0_350:
	s_waitcnt vmcnt(39)
	v_lshlrev_b32_e32 v156, 16, v118
	v_and_b32_e32 v157, 0xffff0000, v118
	v_lshlrev_b32_e32 v118, 16, v119
	v_and_b32_e32 v119, 0xffff0000, v119
	s_waitcnt vmcnt(5)
	v_pk_fma_f32 v[118:119], v[36:37], v[150:151], v[118:119]
	v_lshlrev_b32_e32 v150, 16, v116
	v_and_b32_e32 v151, 0xffff0000, v116
	v_lshlrev_b32_e32 v116, 16, v117
	v_and_b32_e32 v117, 0xffff0000, v117
	v_pk_fma_f32 v[116:117], v[32:33], v[146:147], v[116:117]
	v_lshlrev_b32_e32 v146, 16, v114
	v_and_b32_e32 v147, 0xffff0000, v114
	v_lshlrev_b32_e32 v114, 16, v115
	v_and_b32_e32 v115, 0xffff0000, v115
	v_pk_fma_f32 v[114:115], v[28:29], v[142:143], v[114:115]
	v_lshlrev_b32_e32 v142, 16, v112
	v_and_b32_e32 v143, 0xffff0000, v112
	v_lshlrev_b32_e32 v112, 16, v113
	v_and_b32_e32 v113, 0xffff0000, v113
	s_waitcnt vmcnt(4)
	v_pk_fma_f32 v[112:113], v[24:25], v[138:139], v[112:113]
	v_pk_fma_f32 v[138:139], v[22:23], v[136:137], v[142:143]
	v_lshlrev_b32_e32 v136, 16, v110
	v_and_b32_e32 v137, 0xffff0000, v110
	s_waitcnt vmcnt(3)
	v_pk_fma_f32 v[142:143], v[18:19], v[132:133], v[136:137]
	v_lshlrev_b32_e32 v132, 16, v108
	v_and_b32_e32 v133, 0xffff0000, v108
	v_pk_fma_f32 v[140:141], v[26:27], v[140:141], v[146:147]
	s_waitcnt vmcnt(2)
	v_pk_fma_f32 v[146:147], v[10:11], v[128:129], v[132:133]
	v_lshlrev_b32_e32 v128, 16, v106
	v_and_b32_e32 v129, 0xffff0000, v106
	v_pk_fma_f32 v[144:145], v[30:31], v[144:145], v[150:151]
	v_lshlrev_b32_e32 v110, 16, v111
	v_and_b32_e32 v111, 0xffff0000, v111
	v_lshlrev_b32_e32 v108, 16, v109
	v_and_b32_e32 v109, 0xffff0000, v109
	s_waitcnt vmcnt(1)
	v_pk_fma_f32 v[150:151], v[6:7], v[124:125], v[128:129]
	v_lshlrev_b32_e32 v124, 16, v102
	v_and_b32_e32 v125, 0xffff0000, v102
	v_lshlrev_b32_e32 v102, 16, v103
	v_and_b32_e32 v103, 0xffff0000, v103
	v_pk_fma_f32 v[148:149], v[34:35], v[148:149], v[156:157]
	v_pk_fma_f32 v[110:111], v[20:21], v[134:135], v[110:111]
	v_pk_fma_f32 v[108:109], v[12:13], v[130:131], v[108:109]
	s_waitcnt vmcnt(0)
	v_pk_fma_f32 v[102:103], v[4:5], v[120:121], v[102:103]
	v_cvt_pk_bf16_f32 v120, v148, v149
	v_cvt_pk_bf16_f32 v121, v118, v119
	v_cvt_pk_bf16_f32 v118, v144, v145
	v_cvt_pk_bf16_f32 v119, v116, v117
	v_lshlrev_b32_e32 v106, 16, v107
	v_and_b32_e32 v135, 0xffff0000, v120
	v_and_b32_e32 v131, 0xffff0000, v118
	v_lshlrev_b32_e32 v134, 16, v120
	v_lshlrev_b32_e32 v130, 16, v118
	v_mul_f32_e32 v14, v135, v135
	v_mul_f32_e32 v39, v131, v131
	v_lshlrev_b32_e32 v136, 16, v121
	v_lshlrev_b32_e32 v132, 16, v119
	v_fmac_f32_e32 v14, v134, v134
	v_fmac_f32_e32 v39, v130, v130
	v_and_b32_e32 v107, 0xffff0000, v107
	v_and_b32_e32 v137, 0xffff0000, v121
	v_and_b32_e32 v133, 0xffff0000, v119
	v_fmac_f32_e32 v14, v136, v136
	v_fmac_f32_e32 v39, v132, v132
	v_pk_fma_f32 v[106:107], v[8:9], v[126:127], v[106:107]
	v_cvt_pk_bf16_f32 v116, v140, v141
	v_fmac_f32_e32 v14, v137, v137
	v_and_b32_e32 v127, 0xffff0000, v116
	v_fmac_f32_e32 v39, v133, v133
	v_lshlrev_b32_e32 v126, 16, v116
	v_add_f32_e32 v14, v14, v39
	v_mul_f32_e32 v39, v127, v127
	v_cvt_pk_bf16_f32 v117, v114, v115
	v_fmac_f32_e32 v39, v126, v126
	v_lshlrev_b32_e32 v128, 16, v117
	v_and_b32_e32 v129, 0xffff0000, v117
	v_fmac_f32_e32 v39, v128, v128
	v_pk_fma_f32 v[156:157], v[2:3], v[122:123], v[124:125]
	v_cvt_pk_bf16_f32 v114, v138, v139
	v_fmac_f32_e32 v39, v129, v129
	v_and_b32_e32 v123, 0xffff0000, v114
	v_lshlrev_b32_e32 v122, 16, v114
	v_add_f32_e32 v14, v14, v39
	v_mul_f32_e32 v39, v123, v123
	v_cvt_pk_bf16_f32 v115, v112, v113
	v_fmac_f32_e32 v39, v122, v122
	v_lshlrev_b32_e32 v124, 16, v115
	v_lshl_add_u64 v[158:159], v[48:49], 0, v[104:105]
	v_and_b32_e32 v125, 0xffff0000, v115
	v_fmac_f32_e32 v39, v124, v124
	global_store_dwordx2 v[158:159], v[118:119], off offset:512
	v_cvt_pk_bf16_f32 v112, v142, v143
	v_fmac_f32_e32 v39, v125, v125
	v_and_b32_e32 v119, 0xffff0000, v112
	v_lshlrev_b32_e32 v118, 16, v112
	v_add_f32_e32 v14, v14, v39
	v_mul_f32_e32 v39, v119, v119
	global_store_dwordx2 v[158:159], v[120:121], off
	v_cvt_pk_bf16_f32 v113, v110, v111
	v_fmac_f32_e32 v39, v118, v118
	v_lshlrev_b32_e32 v120, 16, v113
	v_and_b32_e32 v121, 0xffff0000, v113
	v_fmac_f32_e32 v39, v120, v120
	global_store_dwordx2 v[158:159], v[114:115], off offset:1536
	v_cvt_pk_bf16_f32 v110, v146, v147
	v_fmac_f32_e32 v39, v121, v121
	v_and_b32_e32 v115, 0xffff0000, v110
	global_store_dwordx2 v[158:159], v[112:113], off offset:2048
	v_cvt_pk_bf16_f32 v111, v108, v109
	v_lshlrev_b32_e32 v114, 16, v110
	v_cvt_pk_bf16_f32 v138, v150, v151
	v_cvt_pk_bf16_f32 v112, v156, v157
	v_add_f32_e32 v14, v14, v39
	v_mul_f32_e32 v39, v115, v115
	v_and_b32_e32 v109, 0xffff0000, v112
	v_and_b32_e32 v108, 0xffff0000, v138
	global_store_dwordx2 v[158:159], v[116:117], off offset:1024
	v_lshlrev_b32_e32 v116, 16, v111
	v_cvt_pk_bf16_f32 v139, v106, v107
	v_cvt_pk_bf16_f32 v113, v102, v103
	v_fmac_f32_e32 v39, v114, v114
	v_lshlrev_b32_e32 v106, 16, v138
	v_lshlrev_b32_e32 v107, 16, v112
	v_pk_mul_f32 v[102:103], v[108:109], v[108:109]
	global_store_dwordx2 v[158:159], v[110:111], off offset:2560
	v_and_b32_e32 v117, 0xffff0000, v111
	v_fmac_f32_e32 v39, v116, v116
	v_lshlrev_b32_e32 v110, 16, v139
	v_lshlrev_b32_e32 v111, 16, v113
	v_pk_fma_f32 v[102:103], v[106:107], v[106:107], v[102:103]
	global_store_dwordx2 v[158:159], v[112:113], off offset:3584
	v_fmac_f32_e32 v39, v117, v117
	v_and_b32_e32 v113, 0xffff0000, v113
	v_and_b32_e32 v112, 0xffff0000, v139
	v_pk_fma_f32 v[102:103], v[110:111], v[110:111], v[102:103]
	v_add_f32_e32 v14, v14, v39
	v_pk_fma_f32 v[102:103], v[112:113], v[112:113], v[102:103]
	v_cmp_lt_i32_e32 vcc, v220, v213
	v_add_f32_e32 v14, v14, v102
	v_add_f32_e32 v14, v14, v103
	v_cndmask_b32_e32 v39, v212, v220, vcc
	v_lshlrev_b32_e32 v39, 2, v39
	global_store_dwordx2 v[158:159], v[138:139], off offset:3072
	v_lshl_add_u64 v[104:105], v[50:51], 0, v[104:105]
	v_mov_b32_e32 v103, 0
	s_waitcnt lgkmcnt(0)
; #define LAS __attribute__((address_space(3)))
; __device__ __forceinline__ unsigned pk2(float lo, float hi) { unsigned r; asm("v_cvt_pk_bf16_f32 %0, %1, %2" : "=v"(r) : "v"(lo), "v"(hi)); return r; }
; __device__ __forceinline__ void ph_norm1(const Params& p, int mode, LAS unsigned char* lds) {
;     ...
;             unsigned m = (unsigned)(__ballot(myslot[q] >= 0) & 0xffffull);
;             while (m) {
;                 const int e0 = __builtin_ctz(m); m &= m - 1u;
;                 const bool two = m != 0u; const int e1 = two ? __builtin_ctz(m) : e0; if (two) m &= m - 1u;
;     ...
;             const float r = 1.0f / sqrtf(wave_sum(ss) * (1.f / DM) + EPS);
;             asm volatile("" ::: "memory");
;             if (mode == 2) {
;                 float* o = p.out + (size_t)t * DM;
; #pragma unroll
;                 for (int j = 0; j < 8; ++j) { const f32x4 g = fgv[j]; __builtin_nontemporal_store(v[j] * r * g, (f32x4*)(o + 4 * lane + 256 * j)); }
;             } else {
;                 const float* g1 = p.in[5] + (size_t)DM;
;                 const float* sh = mod + ((size_t)4 + b) * 12288;
;                 const float* sc = sh + 2048;
;                 bf16_t* ho = (bf16_t*)(p.ws + WS_H) + (size_t)t * DM;
; #pragma unroll
;                 for (int j = 0; j < 8; ++j) {
;                     const f32x4 h = (v[j] * r) * *(const LAS f32x4*)(T1 + 4 * lane + 256 * j) + *(const LAS f32x4*)(T2 + 4 * lane + 256 * j);
;                     u32x2 w; w.x = pk2(h[0], h[1]); w.y = pk2(h[2], h[3]);
;                     *(u32x2*)(ho + 4 * lane + 256 * j) = w;
;                 }
	s_nop 1
	v_add_f32_dpp v14, v14, v14 quad_perm:[1,0,3,2] row_mask:0xf bank_mask:0xf
	v_xor_b32_e32 v102, 2, v212
	v_cmp_lt_i32_e32 vcc, v102, v213
	s_nop 1
	v_cndmask_b32_e32 v102, v212, v102, vcc
	v_lshlrev_b32_e32 v138, 2, v102
	s_waitcnt lgkmcnt(0)
	s_nop 1
	v_add_f32_dpp v14, v14, v14 quad_perm:[2,3,0,1] row_mask:0xf bank_mask:0xf
	v_xor_b32_e32 v102, 4, v212
	v_cmp_lt_i32_e32 vcc, v102, v213
	s_nop 1
	v_cndmask_b32_e32 v102, v212, v102, vcc
	v_lshlrev_b32_e32 v139, 2, v102
	s_waitcnt lgkmcnt(0)
	s_nop 1
	v_add_f32_dpp v14, v14, v14 row_half_mirror row_mask:0xf bank_mask:0xf
	v_xor_b32_e32 v102, 8, v212
	v_cmp_lt_i32_e32 vcc, v102, v213
	s_nop 1
	v_cndmask_b32_e32 v102, v212, v102, vcc
	v_lshlrev_b32_e32 v140, 2, v102
	v_cmp_lt_i32_e32 vcc, v216, v213
	s_waitcnt lgkmcnt(0)
	s_nop 1
	v_add_f32_dpp v14, v14, v14 row_mirror row_mask:0xf bank_mask:0xf
	v_cndmask_b32_e32 v102, v212, v216, vcc
	v_lshlrev_b32_e32 v141, 2, v102
	v_mov_b32_e32 v102, v14
	s_nop 1
	v_permlane16_swap_b32_e32 v14, v102
	s_waitcnt lgkmcnt(0)
	v_add_f32_e32 v14, v14, v102
	v_xor_b32_e32 v102, 32, v212
	v_cmp_lt_i32_e32 vcc, v102, v213
	s_nop 1
	v_cndmask_b32_e32 v102, v212, v102, vcc
	v_lshlrev_b32_e32 v142, 2, v102
	v_mov_b32_e32 v102, v14
	s_nop 1
	v_permlane32_swap_b32_e32 v14, v102
	s_waitcnt lgkmcnt(0)
	v_add_f32_e32 v14, v14, v102
	v_fmamk_f32 v14, v14, 0x3a000000, v217
	v_cmp_gt_f32_e32 vcc, s5, v14
	v_mul_f32_e32 v102, 0x4f800000, v14
	s_nop 0
	v_cndmask_b32_e32 v14, v14, v102, vcc
	v_sqrt_f32_e32 v102, v14
	s_nop 0
	v_add_u32_e32 v143, -1, v102
	v_fma_f32 v144, -v143, v102, v14
	v_cmp_ge_f32_e64 s[34:35], 0, v144
	v_add_u32_e32 v144, 1, v102
	s_nop 0
	v_cndmask_b32_e64 v143, v102, v143, s[34:35]
	v_fma_f32 v102, -v144, v102, v14
	v_cmp_lt_f32_e64 s[34:35], 0, v102
	s_nop 1
	v_cndmask_b32_e64 v102, v143, v144, s[34:35]
	v_mul_f32_e32 v143, 0x37800000, v102
	v_cndmask_b32_e32 v102, v102, v143, vcc
	v_cmp_class_f32_e32 vcc, v14, v219
	s_nop 1
	v_cndmask_b32_e32 v14, v102, v14, vcc
	v_div_scale_f32 v102, s[8:9], v14, v14, 1.0
	v_rcp_f32_e32 v143, v102
	s_nop 0
	v_fma_f32 v144, -v102, v143, 1.0
	v_fmac_f32_e32 v143, v144, v143
	v_div_scale_f32 v144, vcc, 1.0, v14, 1.0
	v_mul_f32_e32 v145, v144, v143
	v_fma_f32 v146, -v102, v145, v144
	v_fmac_f32_e32 v145, v146, v143
	v_fma_f32 v102, -v102, v145, v144
	v_div_fmas_f32 v102, v102, v143, v145
	v_div_fixup_f32 v14, v102, v14, 1.0
	v_pk_mul_f32 v[148:149], v[14:15], v[134:135] op_sel_hi:[0,1]
	v_pk_mul_f32 v[150:151], v[14:15], v[136:137] op_sel_hi:[0,1]
	ds_read_b128 v[134:137], v153
	ds_read_b128 v[144:147], v153 offset:8192
	v_cmp_lt_i32_e32 vcc, -1, v15
	s_and_b32 s4, vcc_lo, 0xffff
	s_cmp_eq_u32 s4, 0
	v_mov_b32_e32 v102, v103
	s_waitcnt lgkmcnt(0)
	v_pk_fma_f32 v[134:135], v[134:135], v[148:149], v[144:145]
	v_pk_fma_f32 v[136:137], v[136:137], v[150:151], v[146:147]
	v_cvt_pk_bf16_f32 v134, v134, v135
	v_pk_mul_f32 v[144:145], v[14:15], v[130:131] op_sel_hi:[0,1]
	v_cvt_pk_bf16_f32 v135, v136, v137
	global_store_dwordx2 v[104:105], v[134:135], off
	v_pk_mul_f32 v[146:147], v[14:15], v[132:133] op_sel_hi:[0,1]
	ds_read_b128 v[130:133], v153 offset:1024
	ds_read_b128 v[134:137], v153 offset:9216
	s_waitcnt lgkmcnt(0)
	v_pk_fma_f32 v[130:131], v[130:131], v[144:145], v[134:135]
	v_pk_fma_f32 v[132:133], v[132:133], v[146:147], v[136:137]
	v_cvt_pk_bf16_f32 v130, v130, v131
	v_pk_mul_f32 v[134:135], v[14:15], v[126:127] op_sel_hi:[0,1]
	v_cvt_pk_bf16_f32 v131, v132, v133
	global_store_dwordx2 v[104:105], v[130:131], off offset:512
	v_pk_mul_f32 v[136:137], v[14:15], v[128:129] op_sel_hi:[0,1]
	ds_read_b128 v[126:129], v153 offset:2048
	ds_read_b128 v[130:133], v153 offset:10240
	s_waitcnt lgkmcnt(0)
	v_pk_fma_f32 v[126:127], v[134:135], v[126:127], v[130:131]
	v_pk_fma_f32 v[128:129], v[136:137], v[128:129], v[132:133]
	v_cvt_pk_bf16_f32 v126, v126, v127
	v_pk_mul_f32 v[130:131], v[14:15], v[122:123] op_sel_hi:[0,1]
	v_cvt_pk_bf16_f32 v127, v128, v129
	global_store_dwordx2 v[104:105], v[126:127], off offset:1024
	v_pk_mul_f32 v[132:133], v[14:15], v[124:125] op_sel_hi:[0,1]
	ds_read_b128 v[122:125], v153 offset:3072
	ds_read_b128 v[126:129], v153 offset:11264
	s_waitcnt lgkmcnt(0)
; #define LAS __attribute__((address_space(3)))
; __device__ __forceinline__ unsigned pk2(float lo, float hi) { unsigned r; asm("v_cvt_pk_bf16_f32 %0, %1, %2" : "=v"(r) : "v"(lo), "v"(hi)); return r; }
; __device__ __forceinline__ void ph_norm1(const Params& p, int mode, LAS unsigned char* lds) {
;     ...
;             f32x4 macc[8];
; #pragma unroll
;             for (int j = 0; j < 8; ++j) macc[j] = (f32x4){0.f, 0.f, 0.f, 0.f};
;             unsigned m = (unsigned)(__ballot(myslot[q] >= 0) & 0xffffull);
;             while (m) {
;                 const int e0 = __builtin_ctz(m); m &= m - 1u;
;                 const bool two = m != 0u; const int e1 = two ? __builtin_ctz(m) : e0; if (two) m &= m - 1u;
;     ...
;                 bf16_t* ho = (bf16_t*)(p.ws + WS_H) + (size_t)t * DM;
; #pragma unroll
;                 for (int j = 0; j < 8; ++j) {
;                     const f32x4 h = (v[j] * r) * *(const LAS f32x4*)(T1 + 4 * lane + 256 * j) + *(const LAS f32x4*)(T2 + 4 * lane + 256 * j);
;                     u32x2 w; w.x = pk2(h[0], h[1]); w.y = pk2(h[2], h[3]);
;                     *(u32x2*)(ho + 4 * lane + 256 * j) = w;
;                 }
	v_pk_fma_f32 v[122:123], v[130:131], v[122:123], v[126:127]
	v_pk_fma_f32 v[124:125], v[132:133], v[124:125], v[128:129]
	v_cvt_pk_bf16_f32 v122, v122, v123
	v_pk_mul_f32 v[126:127], v[14:15], v[118:119] op_sel_hi:[0,1]
	v_cvt_pk_bf16_f32 v123, v124, v125
	global_store_dwordx2 v[104:105], v[122:123], off offset:1536
	v_pk_mul_f32 v[128:129], v[14:15], v[120:121] op_sel_hi:[0,1]
	ds_read_b128 v[118:121], v153 offset:4096
	ds_read_b128 v[122:125], v153 offset:12288
	v_mov_b32_e32 v133, v103
	v_mov_b32_e32 v132, v103
	v_mov_b32_e32 v131, v103
	v_mov_b32_e32 v130, v103
	s_waitcnt lgkmcnt(0)
	v_pk_fma_f32 v[118:119], v[126:127], v[118:119], v[122:123]
	v_pk_fma_f32 v[120:121], v[128:129], v[120:121], v[124:125]
	v_cvt_pk_bf16_f32 v118, v118, v119
	v_pk_mul_f32 v[122:123], v[14:15], v[114:115] op_sel_hi:[0,1]
	v_cvt_pk_bf16_f32 v119, v120, v121
	global_store_dwordx2 v[104:105], v[118:119], off offset:2048
	v_pk_mul_f32 v[124:125], v[14:15], v[116:117] op_sel_hi:[0,1]
	ds_read_b128 v[114:117], v153 offset:5120
	ds_read_b128 v[118:121], v153 offset:13312
	v_mov_b32_e32 v129, v103
	v_mov_b32_e32 v128, v103
	v_mov_b32_e32 v127, v103
	v_mov_b32_e32 v126, v103
	s_waitcnt lgkmcnt(0)
	v_pk_fma_f32 v[114:115], v[122:123], v[114:115], v[118:119]
	v_pk_fma_f32 v[116:117], v[124:125], v[116:117], v[120:121]
	v_cvt_pk_bf16_f32 v114, v114, v115
	s_nop 0
	v_cvt_pk_bf16_f32 v115, v116, v117
	global_store_dwordx2 v[104:105], v[114:115], off offset:2560
	v_mov_b32_e32 v114, v106
	v_mov_b32_e32 v115, v108
	v_pk_mul_f32 v[122:123], v[14:15], v[114:115] op_sel_hi:[0,1]
	v_mov_b32_e32 v114, v110
	v_mov_b32_e32 v115, v112
	v_pk_mul_f32 v[124:125], v[14:15], v[114:115] op_sel_hi:[0,1]
	ds_read_b128 v[114:117], v153 offset:6144
	ds_read_b128 v[118:121], v153 offset:14336
	v_mov_b32_e32 v108, v107
	v_mov_b32_e32 v112, v111
	s_waitcnt lgkmcnt(0)
	v_pk_fma_f32 v[114:115], v[122:123], v[114:115], v[118:119]
	v_pk_fma_f32 v[116:117], v[124:125], v[116:117], v[120:121]
	v_cvt_pk_bf16_f32 v114, v114, v115
	v_mov_b32_e32 v121, v103
	v_cvt_pk_bf16_f32 v115, v116, v117
	global_store_dwordx2 v[104:105], v[114:115], off offset:3072
	v_pk_mul_f32 v[114:115], v[14:15], v[108:109] op_sel_hi:[0,1]
	v_pk_mul_f32 v[116:117], v[14:15], v[112:113] op_sel_hi:[0,1]
	ds_read_b128 v[106:109], v153 offset:7168
	ds_read_b128 v[110:113], v153 offset:15360
	v_mov_b32_e32 v120, v103
	v_mov_b32_e32 v119, v103
	v_mov_b32_e32 v118, v103
	v_mov_b32_e32 v125, v103
	s_waitcnt lgkmcnt(0)
	v_pk_fma_f32 v[106:107], v[114:115], v[106:107], v[110:111]
	v_pk_fma_f32 v[108:109], v[116:117], v[108:109], v[112:113]
	v_cvt_pk_bf16_f32 v106, v106, v107
	v_mov_b32_e32 v113, v103
	v_cvt_pk_bf16_f32 v107, v108, v109
	global_store_dwordx2 v[104:105], v[106:107], off offset:3584
	v_mov_b32_e32 v105, v103
	v_mov_b32_e32 v104, v103
	v_mov_b32_e32 v109, v103
	v_mov_b32_e32 v108, v103
	v_mov_b32_e32 v107, v103
	v_mov_b32_e32 v106, v103
	v_mov_b32_e32 v112, v103
	v_mov_b32_e32 v111, v103
	v_mov_b32_e32 v110, v103
	v_mov_b32_e32 v117, v103
	v_mov_b32_e32 v116, v103
	v_mov_b32_e32 v115, v103
	v_mov_b32_e32 v114, v103
	v_mov_b32_e32 v124, v103
	v_mov_b32_e32 v123, v103
	v_mov_b32_e32 v122, v103
	s_cbranch_scc1 .LBB0_353
	v_mov_b32_e32 v102, 0
	v_mov_b32_e32 v103, v102
	v_mov_b32_e32 v130, v102
	v_mov_b32_e32 v131, v102
	v_mov_b32_e32 v132, v102
	v_mov_b32_e32 v133, v102
	v_mov_b32_e32 v126, v102
	v_mov_b32_e32 v127, v102
	v_mov_b32_e32 v128, v102
	v_mov_b32_e32 v129, v102
	v_mov_b32_e32 v122, v102
	v_mov_b32_e32 v123, v102
	v_mov_b32_e32 v124, v102
	v_mov_b32_e32 v125, v102
	v_mov_b32_e32 v118, v102
	v_mov_b32_e32 v119, v102
	v_mov_b32_e32 v120, v102
	v_mov_b32_e32 v121, v102
	v_mov_b32_e32 v114, v102
	v_mov_b32_e32 v115, v102
	v_mov_b32_e32 v116, v102
	v_mov_b32_e32 v117, v102
	v_mov_b32_e32 v110, v102
	v_mov_b32_e32 v111, v102
	v_mov_b32_e32 v112, v102
	v_mov_b32_e32 v113, v102
	v_mov_b32_e32 v106, v102
	v_mov_b32_e32 v107, v102
	v_mov_b32_e32 v108, v102
	v_mov_b32_e32 v109, v102
	v_mov_b32_e32 v104, v102
	v_mov_b32_e32 v105, v102

; __device__ __forceinline__ unsigned pk2(float lo, float hi) { unsigned r; asm("v_cvt_pk_bf16_f32 %0, %1, %2" : "=v"(r) : "v"(lo), "v"(hi)); return r; }
; __device__ __forceinline__ float bflo(unsigned u) { return __uint_as_float(u << 16); }
; __device__ __forceinline__ float bfhi(unsigned u) { return __uint_as_float(u & 0xffff0000u); }
; __device__ __forceinline__ void ph_norm1(const Params& p, int mode, LAS unsigned char* lds) {
;     ...
;             f32x4 v[8];
; #pragma unroll
;             for (int j = 0; j < 8; ++j) { const f32x4 g = gfv[j];
;                 v[j] = (f32x4){bflo(xw[q][j].x), bfhi(xw[q][j].x), bflo(xw[q][j].y), bfhi(xw[q][j].y)} + g * macc[j]; }
;             if (mode == 1) {
;                 bf16_t* xo = (bf16_t*)(p.ws + WS_X) + (size_t)t * DM;
; #pragma unroll
;                 for (int j = 0; j < 8; ++j) { u32x2 w; w.x = pk2(v[j][0], v[j][1]); w.y = pk2(v[j][2], v[j][3]); *(u32x2*)(xo + 4 * lane + 256 * j) = w;
;                     v[j] = (f32x4){bflo(w.x), bfhi(w.x), bflo(w.y), bfhi(w.y)}; }
;             }
;             float ss = 0.f;
; #pragma unroll
;             for (int j = 0; j < 8; ++j) ss += v[j][0] * v[j][0] + v[j][1] * v[j][1] + v[j][2] * v[j][2] + v[j][3] * v[j][3];
;             const float r = 1.0f / sqrtf(wave_sum(ss) * (1.f / DM) + EPS);
.LBB0_353:
	v_lshlrev_b32_e32 v14, 16, v100
	v_and_b32_e32 v15, 0xffff0000, v100
	v_pk_fma_f32 v[14:15], v[34:35], v[130:131], v[14:15]
	v_lshlrev_b32_e32 v130, 16, v98
	v_and_b32_e32 v131, 0xffff0000, v98
	v_lshlrev_b32_e32 v98, 16, v99
	v_and_b32_e32 v99, 0xffff0000, v99
	v_pk_fma_f32 v[98:99], v[32:33], v[128:129], v[98:99]
	v_lshlrev_b32_e32 v128, 16, v96
	v_and_b32_e32 v129, 0xffff0000, v96
	v_lshlrev_b32_e32 v96, 16, v97
	v_and_b32_e32 v97, 0xffff0000, v97
	v_pk_fma_f32 v[96:97], v[28:29], v[124:125], v[96:97]
	v_lshlrev_b32_e32 v124, 16, v94
	v_and_b32_e32 v125, 0xffff0000, v94
	v_lshlrev_b32_e32 v94, 16, v95
	v_and_b32_e32 v95, 0xffff0000, v95
	v_pk_fma_f32 v[94:95], v[24:25], v[120:121], v[94:95]
	v_pk_fma_f32 v[120:121], v[22:23], v[118:119], v[124:125]
	v_lshlrev_b32_e32 v118, 16, v92
	v_and_b32_e32 v119, 0xffff0000, v92
	v_pk_fma_f32 v[124:125], v[18:19], v[114:115], v[118:119]
	v_lshlrev_b32_e32 v114, 16, v90
	v_and_b32_e32 v115, 0xffff0000, v90
	v_pk_fma_f32 v[122:123], v[26:27], v[122:123], v[128:129]
	v_pk_fma_f32 v[128:129], v[10:11], v[110:111], v[114:115]
	v_lshlrev_b32_e32 v110, 16, v88
	v_and_b32_e32 v111, 0xffff0000, v88
	v_lshlrev_b32_e32 v88, 16, v89
	v_and_b32_e32 v89, 0xffff0000, v89
	v_pk_fma_f32 v[126:127], v[30:31], v[126:127], v[130:131]
	v_lshlrev_b32_e32 v92, 16, v93
	v_and_b32_e32 v93, 0xffff0000, v93
	v_lshlrev_b32_e32 v90, 16, v91
	v_and_b32_e32 v91, 0xffff0000, v91
	v_pk_fma_f32 v[88:89], v[8:9], v[108:109], v[88:89]
	v_lshlrev_b32_e32 v108, 16, v86
	v_and_b32_e32 v109, 0xffff0000, v86
	v_lshlrev_b32_e32 v86, 16, v87
	v_and_b32_e32 v87, 0xffff0000, v87
	v_pk_fma_f32 v[92:93], v[20:21], v[116:117], v[92:93]
	v_pk_fma_f32 v[90:91], v[12:13], v[112:113], v[90:91]
	v_pk_fma_f32 v[86:87], v[4:5], v[102:103], v[86:87]
	v_pk_fma_f32 v[130:131], v[2:3], v[104:105], v[108:109]
	v_cvt_pk_bf16_f32 v14, v14, v15
	v_cvt_pk_bf16_f32 v126, v126, v127
	v_lshlrev_b32_e32 v100, 16, v101
	v_and_b32_e32 v117, 0xffff0000, v14
	v_and_b32_e32 v113, 0xffff0000, v126
	v_and_b32_e32 v101, 0xffff0000, v101
	v_lshlrev_b32_e32 v116, 16, v14
	v_lshlrev_b32_e32 v112, 16, v126
	v_cvt_pk_bf16_f32 v130, v130, v131
	v_cvt_pk_bf16_f32 v131, v86, v87
	v_mul_f32_e32 v86, v117, v117
	v_mul_f32_e32 v87, v113, v113
	v_pk_fma_f32 v[100:101], v[36:37], v[132:133], v[100:101]
	v_cvt_pk_bf16_f32 v127, v98, v99
	v_fmac_f32_e32 v86, v116, v116
	v_cvt_pk_bf16_f32 v15, v100, v101
	v_lshlrev_b32_e32 v114, 16, v127
	v_lshlrev_b32_e32 v118, 16, v15
	v_fmac_f32_e32 v87, v112, v112
	v_and_b32_e32 v119, 0xffff0000, v15
	v_and_b32_e32 v115, 0xffff0000, v127
	v_fmac_f32_e32 v86, v118, v118
	v_fmac_f32_e32 v87, v114, v114
	v_cvt_pk_bf16_f32 v122, v122, v123
	v_fmac_f32_e32 v86, v119, v119
	v_and_b32_e32 v109, 0xffff0000, v122
	v_fmac_f32_e32 v87, v115, v115
	v_lshlrev_b32_e32 v108, 16, v122
	v_add_f32_e32 v86, v86, v87
	v_mul_f32_e32 v87, v109, v109
	v_pk_fma_f32 v[106:107], v[6:7], v[106:107], v[110:111]
	v_cvt_pk_bf16_f32 v123, v96, v97
	v_fmac_f32_e32 v87, v108, v108
	v_lshlrev_b32_e32 v110, 16, v123
	v_and_b32_e32 v111, 0xffff0000, v123
	v_fmac_f32_e32 v87, v110, v110
	v_cvt_pk_bf16_f32 v120, v120, v121
	v_fmac_f32_e32 v87, v111, v111
	v_and_b32_e32 v103, 0xffff0000, v120
	v_lshlrev_b32_e32 v102, 16, v120
	v_add_f32_e32 v86, v86, v87
	v_mul_f32_e32 v87, v103, v103
	v_cvt_pk_bf16_f32 v121, v94, v95
	v_fmac_f32_e32 v87, v102, v102
	v_lshlrev_b32_e32 v104, 16, v121
	v_and_b32_e32 v105, 0xffff0000, v121
	v_fmac_f32_e32 v87, v104, v104
	v_cvt_pk_bf16_f32 v124, v124, v125
	v_fmac_f32_e32 v87, v105, v105
	v_and_b32_e32 v99, 0xffff0000, v124
	v_lshlrev_b32_e32 v98, 16, v124
	v_add_f32_e32 v86, v86, v87
	v_mul_f32_e32 v87, v99, v99
	v_cvt_pk_bf16_f32 v125, v92, v93
	v_fmac_f32_e32 v87, v98, v98
	v_lshlrev_b32_e32 v100, 16, v125
	v_and_b32_e32 v101, 0xffff0000, v125
	v_fmac_f32_e32 v87, v100, v100
	v_cvt_pk_bf16_f32 v128, v128, v129
	v_fmac_f32_e32 v87, v101, v101
	v_and_b32_e32 v95, 0xffff0000, v128
	v_lshlrev_b32_e32 v94, 16, v128
	v_add_f32_e32 v86, v86, v87
	v_mul_f32_e32 v87, v95, v95
	v_cvt_pk_bf16_f32 v129, v90, v91
	v_fmac_f32_e32 v87, v94, v94
	v_lshlrev_b32_e32 v96, 16, v129
	v_and_b32_e32 v97, 0xffff0000, v129
	v_fmac_f32_e32 v87, v96, v96
	v_cvt_pk_bf16_f32 v106, v106, v107
	v_cvt_pk_bf16_f32 v107, v88, v89
	v_fmac_f32_e32 v87, v97, v97
	v_and_b32_e32 v89, 0xffff0000, v130
	v_and_b32_e32 v88, 0xffff0000, v106
	v_add_f32_e32 v134, v86, v87
	v_lshlrev_b32_e32 v86, 16, v106
	v_lshlrev_b32_e32 v87, 16, v130
	v_pk_mul_f32 v[132:133], v[88:89], v[88:89]
	v_lshlrev_b32_e32 v90, 16, v107
	v_lshlrev_b32_e32 v91, 16, v131
	v_pk_fma_f32 v[132:133], v[86:87], v[86:87], v[132:133]
	v_and_b32_e32 v93, 0xffff0000, v131
	v_and_b32_e32 v92, 0xffff0000, v107
	v_pk_fma_f32 v[132:133], v[90:91], v[90:91], v[132:133]
	s_nop 0
	v_pk_fma_f32 v[132:133], v[92:93], v[92:93], v[132:133]
	s_nop 0
	v_add_f32_e32 v132, v134, v132
	v_add_f32_e32 v132, v132, v133
	s_waitcnt lgkmcnt(0)
	s_nop 1
	v_add_f32_dpp v132, v132, v132 quad_perm:[1,0,3,2] row_mask:0xf bank_mask:0xf
	s_waitcnt lgkmcnt(0)
	s_nop 1
	v_add_f32_dpp v132, v132, v132 quad_perm:[2,3,0,1] row_mask:0xf bank_mask:0xf
	s_waitcnt lgkmcnt(0)
	s_nop 1
	v_add_f32_dpp v132, v132, v132 row_half_mirror row_mask:0xf bank_mask:0xf
	s_waitcnt lgkmcnt(0)
	s_nop 1
	v_add_f32_dpp v134, v132, v132 row_mirror row_mask:0xf bank_mask:0xf
	v_mov_b32_e32 v135, v134
	s_nop 1
	v_permlane16_swap_b32_e32 v134, v135
	v_or_b32_e32 v132, 1, v38
	v_ashrrev_i32_e32 v133, 31, v132
	v_lshlrev_b64 v[132:133], 12, v[132:133]
	s_waitcnt lgkmcnt(0)
; #define LAS __attribute__((address_space(3)))
; __device__ __forceinline__ unsigned pk2(float lo, float hi) { unsigned r; asm("v_cvt_pk_bf16_f32 %0, %1, %2" : "=v"(r) : "v"(lo), "v"(hi)); return r; }
; __device__ __forceinline__ float bflo(unsigned u) { return __uint_as_float(u << 16); }
; __device__ __forceinline__ float bfhi(unsigned u) { return __uint_as_float(u & 0xffff0000u); }
; __device__ __forceinline__ void ph_norm1(const Params& p, int mode, LAS unsigned char* lds) {
;     ...
;             unsigned m = (unsigned)(__ballot(myslot[q] >= 0) & 0xffffull);
;             while (m) {
;                 const int e0 = __builtin_ctz(m); m &= m - 1u;
;                 const bool two = m != 0u; const int e1 = two ? __builtin_ctz(m) : e0; if (two) m &= m - 1u;
;     ...
;                 bf16_t* xo = (bf16_t*)(p.ws + WS_X) + (size_t)t * DM;
; #pragma unroll
;                 for (int j = 0; j < 8; ++j) { u32x2 w; w.x = pk2(v[j][0], v[j][1]); w.y = pk2(v[j][2], v[j][3]); *(u32x2*)(xo + 4 * lane + 256 * j) = w;
;                     v[j] = (f32x4){bflo(w.x), bfhi(w.x), bflo(w.y), bfhi(w.y)}; }
;             }
;             float ss = 0.f;
; #pragma unroll
;             for (int j = 0; j < 8; ++j) ss += v[j][0] * v[j][0] + v[j][1] * v[j][1] + v[j][2] * v[j][2] + v[j][3] * v[j][3];
;             const float r = 1.0f / sqrtf(wave_sum(ss) * (1.f / DM) + EPS);
;             asm volatile("" ::: "memory");
;             if (mode == 2) {
;                 float* o = p.out + (size_t)t * DM;
; #pragma unroll
;                 for (int j = 0; j < 8; ++j) { const f32x4 g = fgv[j]; __builtin_nontemporal_store(v[j] * r * g, (f32x4*)(o + 4 * lane + 256 * j)); }
;             } else {
;                 const float* g1 = p.in[5] + (size_t)DM;
;                 const float* sh = mod + ((size_t)4 + b) * 12288;
;                 const float* sc = sh + 2048;
;                 bf16_t* ho = (bf16_t*)(p.ws + WS_H) + (size_t)t * DM;
; #pragma unroll
;                 for (int j = 0; j < 8; ++j) {
;                     const f32x4 h = (v[j] * r) * *(const LAS f32x4*)(T1 + 4 * lane + 256 * j) + *(const LAS f32x4*)(T2 + 4 * lane + 256 * j);
;                     u32x2 w; w.x = pk2(h[0], h[1]); w.y = pk2(h[2], h[3]);
;                     *(u32x2*)(ho + 4 * lane + 256 * j) = w;
;                 }
	v_add_f32_e32 v136, v134, v135
	ds_bpermute_b32 v137, v142, v136
	v_lshl_add_u64 v[134:135], v[48:49], 0, v[132:133]
	global_store_dwordx2 v[134:135], v[14:15], off
	global_store_dwordx2 v[134:135], v[126:127], off offset:512
	global_store_dwordx2 v[134:135], v[122:123], off offset:1024
	global_store_dwordx2 v[134:135], v[120:121], off offset:1536
	global_store_dwordx2 v[134:135], v[124:125], off offset:2048
	global_store_dwordx2 v[134:135], v[128:129], off offset:2560
	global_store_dwordx2 v[134:135], v[106:107], off offset:3072
	global_store_dwordx2 v[134:135], v[130:131], off offset:3584
	s_waitcnt lgkmcnt(0)
	v_add_f32_e32 v14, v136, v137
	v_fmamk_f32 v14, v14, 0x3a000000, v217
	v_cmp_gt_f32_e32 vcc, s5, v14
	v_mul_f32_e32 v15, 0x4f800000, v14
	s_nop 0
	v_cndmask_b32_e32 v14, v14, v15, vcc
	v_sqrt_f32_e32 v15, v14
	s_nop 0
	v_add_u32_e32 v120, -1, v15
	v_fma_f32 v121, -v120, v15, v14
	v_cmp_ge_f32_e64 s[34:35], 0, v121
	v_add_u32_e32 v121, 1, v15
	s_nop 0
	v_cndmask_b32_e64 v120, v15, v120, s[34:35]
	v_fma_f32 v15, -v121, v15, v14
	v_cmp_lt_f32_e64 s[34:35], 0, v15
	s_nop 1
	v_cndmask_b32_e64 v15, v120, v121, s[34:35]
	v_mul_f32_e32 v120, 0x37800000, v15
	v_cndmask_b32_e32 v15, v15, v120, vcc
	v_cmp_class_f32_e32 vcc, v14, v219
	s_nop 1
	v_cndmask_b32_e32 v14, v15, v14, vcc
	v_div_scale_f32 v120, s[8:9], v14, v14, 1.0
	v_rcp_f32_e32 v121, v120
	v_mov_b32_e32 v15, 0
	v_fma_f32 v106, -v120, v121, 1.0
	v_fmac_f32_e32 v121, v106, v121
	v_div_scale_f32 v106, vcc, 1.0, v14, 1.0
	v_mul_f32_e32 v107, v106, v121
	v_fma_f32 v122, -v120, v107, v106
	v_fmac_f32_e32 v107, v122, v121
	v_fma_f32 v106, -v120, v107, v106
	v_div_fmas_f32 v106, v106, v121, v107
	ds_read_b128 v[120:123], v153
	ds_read_b128 v[124:127], v153 offset:8192
	v_div_fixup_f32 v14, v106, v14, 1.0
	v_pk_mul_f32 v[116:117], v[14:15], v[116:117] op_sel_hi:[0,1]
	v_pk_mul_f32 v[118:119], v[14:15], v[118:119] op_sel_hi:[0,1]
	v_lshl_add_u64 v[106:107], v[50:51], 0, v[132:133]
	s_waitcnt lgkmcnt(0)
	v_pk_fma_f32 v[116:117], v[120:121], v[116:117], v[124:125]
	v_pk_fma_f32 v[126:127], v[122:123], v[118:119], v[126:127]
	v_cvt_pk_bf16_f32 v124, v116, v117
	ds_read_b128 v[116:119], v153 offset:1024
	ds_read_b128 v[120:123], v153 offset:9216
	v_pk_mul_f32 v[112:113], v[14:15], v[112:113] op_sel_hi:[0,1]
	v_cvt_pk_bf16_f32 v125, v126, v127
	global_store_dwordx2 v[106:107], v[124:125], off
	v_pk_mul_f32 v[114:115], v[14:15], v[114:115] op_sel_hi:[0,1]
	s_waitcnt lgkmcnt(0)
	v_pk_fma_f32 v[112:113], v[116:117], v[112:113], v[120:121]
	v_pk_fma_f32 v[122:123], v[118:119], v[114:115], v[122:123]
	v_cvt_pk_bf16_f32 v120, v112, v113
	ds_read_b128 v[112:115], v153 offset:2048
	ds_read_b128 v[116:119], v153 offset:10240
	v_pk_mul_f32 v[108:109], v[14:15], v[108:109] op_sel_hi:[0,1]
	v_cvt_pk_bf16_f32 v121, v122, v123
	global_store_dwordx2 v[106:107], v[120:121], off offset:512
	v_pk_mul_f32 v[110:111], v[14:15], v[110:111] op_sel_hi:[0,1]
	s_waitcnt lgkmcnt(0)
	v_pk_fma_f32 v[108:109], v[108:109], v[112:113], v[116:117]
	v_pk_fma_f32 v[118:119], v[110:111], v[114:115], v[118:119]
	v_cvt_pk_bf16_f32 v116, v108, v109
	ds_read_b128 v[108:111], v153 offset:3072
	ds_read_b128 v[112:115], v153 offset:11264
	v_pk_mul_f32 v[102:103], v[14:15], v[102:103] op_sel_hi:[0,1]
	v_cvt_pk_bf16_f32 v117, v118, v119
	global_store_dwordx2 v[106:107], v[116:117], off offset:1024
	v_pk_mul_f32 v[104:105], v[14:15], v[104:105] op_sel_hi:[0,1]
	s_waitcnt lgkmcnt(0)
	v_pk_fma_f32 v[102:103], v[102:103], v[108:109], v[112:113]
	v_pk_fma_f32 v[114:115], v[104:105], v[110:111], v[114:115]
	v_cvt_pk_bf16_f32 v112, v102, v103
	ds_read_b128 v[102:105], v153 offset:4096
	ds_read_b128 v[108:111], v153 offset:12288
	v_pk_mul_f32 v[98:99], v[14:15], v[98:99] op_sel_hi:[0,1]
	v_cvt_pk_bf16_f32 v113, v114, v115
	global_store_dwordx2 v[106:107], v[112:113], off offset:1536
	v_pk_mul_f32 v[100:101], v[14:15], v[100:101] op_sel_hi:[0,1]
	s_waitcnt lgkmcnt(0)
	v_pk_fma_f32 v[98:99], v[98:99], v[102:103], v[108:109]
	v_pk_fma_f32 v[110:111], v[100:101], v[104:105], v[110:111]
	v_cvt_pk_bf16_f32 v108, v98, v99
	ds_read_b128 v[98:101], v153 offset:5120
	ds_read_b128 v[102:105], v153 offset:13312
	v_pk_mul_f32 v[94:95], v[14:15], v[94:95] op_sel_hi:[0,1]
	v_pk_mul_f32 v[96:97], v[14:15], v[96:97] op_sel_hi:[0,1]
	v_cvt_pk_bf16_f32 v109, v110, v111
	global_store_dwordx2 v[106:107], v[108:109], off offset:2048
	s_waitcnt lgkmcnt(0)
	v_pk_fma_f32 v[94:95], v[94:95], v[98:99], v[102:103]
	v_pk_fma_f32 v[96:97], v[96:97], v[100:101], v[104:105]
	v_cvt_pk_bf16_f32 v94, v94, v95
	v_mov_b32_e32 v102, v86
	v_cvt_pk_bf16_f32 v95, v96, v97
	global_store_dwordx2 v[106:107], v[94:95], off offset:2560
	ds_read_b128 v[94:97], v153 offset:6144
	ds_read_b128 v[98:101], v153 offset:14336
	v_mov_b32_e32 v103, v88
	v_pk_mul_f32 v[102:103], v[14:15], v[102:103] op_sel_hi:[0,1]
	v_mov_b32_e32 v104, v90
	v_mov_b32_e32 v105, v92
	v_pk_mul_f32 v[104:105], v[14:15], v[104:105] op_sel_hi:[0,1]
	s_waitcnt lgkmcnt(0)
	v_pk_fma_f32 v[94:95], v[102:103], v[94:95], v[98:99]
	v_pk_fma_f32 v[96:97], v[104:105], v[96:97], v[100:101]
	v_cvt_pk_bf16_f32 v94, v94, v95
	v_mov_b32_e32 v88, v87
	v_cvt_pk_bf16_f32 v95, v96, v97
	global_store_dwordx2 v[106:107], v[94:95], off offset:3072
	ds_read_b128 v[94:97], v153 offset:7168
	ds_read_b128 v[98:101], v153 offset:15360
	v_pk_mul_f32 v[86:87], v[14:15], v[88:89] op_sel_hi:[0,1]
	v_mov_b32_e32 v92, v91
	v_pk_mul_f32 v[88:89], v[14:15], v[92:93] op_sel_hi:[0,1]
	v_cmp_lt_i32_e32 vcc, -1, v16
	s_waitcnt lgkmcnt(0)
	v_pk_fma_f32 v[86:87], v[86:87], v[94:95], v[98:99]
	v_pk_fma_f32 v[88:89], v[88:89], v[96:97], v[100:101]
	v_cvt_pk_bf16_f32 v86, v86, v87
	s_and_b32 s4, vcc_lo, 0xffff
	v_cvt_pk_bf16_f32 v87, v88, v89
	global_store_dwordx2 v[106:107], v[86:87], off offset:3584
	s_cmp_eq_u32 s4, 0
	v_mov_b32_e32 v14, v15
	v_mov_b32_e32 v87, v15
	v_mov_b32_e32 v86, v15
	v_mov_b32_e32 v91, v15
	v_mov_b32_e32 v90, v15
	v_mov_b32_e32 v89, v15
	v_mov_b32_e32 v88, v15
	v_mov_b32_e32 v95, v15
	v_mov_b32_e32 v94, v15
	v_mov_b32_e32 v93, v15
	v_mov_b32_e32 v92, v15
	v_mov_b32_e32 v99, v15
	v_mov_b32_e32 v98, v15
	v_mov_b32_e32 v97, v15
	v_mov_b32_e32 v96, v15
	v_mov_b32_e32 v103, v15
	v_mov_b32_e32 v102, v15
	v_mov_b32_e32 v101, v15
	v_mov_b32_e32 v100, v15
	v_mov_b32_e32 v107, v15
	v_mov_b32_e32 v106, v15
	v_mov_b32_e32 v105, v15
	v_mov_b32_e32 v104, v15
	v_mov_b32_e32 v111, v15
	v_mov_b32_e32 v110, v15
	v_mov_b32_e32 v109, v15
	v_mov_b32_e32 v108, v15
	v_mov_b32_e32 v115, v15
	v_mov_b32_e32 v114, v15
	v_mov_b32_e32 v113, v15
	v_mov_b32_e32 v112, v15
	s_cbranch_scc1 .LBB0_356
; __device__ __forceinline__ void ph_norm1(const Params& p, int mode, LAS unsigned char* lds) {
;     ...
;             f32x4 macc[8];
; #pragma unroll
;             for (int j = 0; j < 8; ++j) macc[j] = (f32x4){0.f, 0.f, 0.f, 0.f};
	v_mov_b32_e32 v14, 0
	v_mov_b32_e32 v15, v14
	v_mov_b32_e32 v112, v14
	v_mov_b32_e32 v113, v14
	v_mov_b32_e32 v114, v14
	v_mov_b32_e32 v115, v14
	v_mov_b32_e32 v108, v14
	v_mov_b32_e32 v109, v14
	v_mov_b32_e32 v110, v14
	v_mov_b32_e32 v111, v14
	v_mov_b32_e32 v104, v14
	v_mov_b32_e32 v105, v14
	v_mov_b32_e32 v106, v14
	v_mov_b32_e32 v107, v14
	v_mov_b32_e32 v100, v14
	v_mov_b32_e32 v101, v14
	v_mov_b32_e32 v102, v14
	v_mov_b32_e32 v103, v14
	v_mov_b32_e32 v96, v14
	v_mov_b32_e32 v97, v14
	v_mov_b32_e32 v98, v14
	v_mov_b32_e32 v99, v14
	v_mov_b32_e32 v92, v14
	v_mov_b32_e32 v93, v14
	v_mov_b32_e32 v94, v14
	v_mov_b32_e32 v95, v14
	v_mov_b32_e32 v88, v14
	v_mov_b32_e32 v89, v14
	v_mov_b32_e32 v90, v14
	v_mov_b32_e32 v91, v14
	v_mov_b32_e32 v86, v14
	v_mov_b32_e32 v87, v14

; __device__ __forceinline__ unsigned pk2(float lo, float hi) { unsigned r; asm("v_cvt_pk_bf16_f32 %0, %1, %2" : "=v"(r) : "v"(lo), "v"(hi)); return r; }
; __device__ __forceinline__ float bflo(unsigned u) { return __uint_as_float(u << 16); }
; __device__ __forceinline__ float bfhi(unsigned u) { return __uint_as_float(u & 0xffff0000u); }
; __device__ __forceinline__ void ph_norm1(const Params& p, int mode, LAS unsigned char* lds) {
;     ...
;             f32x4 v[8];
; #pragma unroll
;             for (int j = 0; j < 8; ++j) { const f32x4 g = gfv[j];
;                 v[j] = (f32x4){bflo(xw[q][j].x), bfhi(xw[q][j].x), bflo(xw[q][j].y), bfhi(xw[q][j].y)} + g * macc[j]; }
;             if (mode == 1) {
;                 bf16_t* xo = (bf16_t*)(p.ws + WS_X) + (size_t)t * DM;
; #pragma unroll
;                 for (int j = 0; j < 8; ++j) { u32x2 w; w.x = pk2(v[j][0], v[j][1]); w.y = pk2(v[j][2], v[j][3]); *(u32x2*)(xo + 4 * lane + 256 * j) = w;
;                     v[j] = (f32x4){bflo(w.x), bfhi(w.x), bflo(w.y), bfhi(w.y)}; }
;             }
;             float ss = 0.f;
; #pragma unroll
;             for (int j = 0; j < 8; ++j) ss += v[j][0] * v[j][0] + v[j][1] * v[j][1] + v[j][2] * v[j][2] + v[j][3] * v[j][3];
;             const float r = 1.0f / sqrtf(wave_sum(ss) * (1.f / DM) + EPS);
.LBB0_356:
	v_lshlrev_b32_e32 v116, 16, v84
	v_and_b32_e32 v117, 0xffff0000, v84
	v_lshlrev_b32_e32 v84, 16, v85
	v_and_b32_e32 v85, 0xffff0000, v85
	v_pk_fma_f32 v[84:85], v[36:37], v[114:115], v[84:85]
	v_lshlrev_b32_e32 v114, 16, v82
	v_and_b32_e32 v115, 0xffff0000, v82
	v_lshlrev_b32_e32 v82, 16, v83
	v_and_b32_e32 v83, 0xffff0000, v83
	v_pk_fma_f32 v[82:83], v[32:33], v[110:111], v[82:83]
	v_lshlrev_b32_e32 v110, 16, v80
	v_and_b32_e32 v111, 0xffff0000, v80
	v_lshlrev_b32_e32 v80, 16, v81
	v_and_b32_e32 v81, 0xffff0000, v81
	v_pk_fma_f32 v[80:81], v[28:29], v[106:107], v[80:81]
	v_lshlrev_b32_e32 v106, 16, v78
	v_and_b32_e32 v107, 0xffff0000, v78
	v_pk_fma_f32 v[106:107], v[22:23], v[100:101], v[106:107]
	v_lshlrev_b32_e32 v100, 16, v76
	v_and_b32_e32 v101, 0xffff0000, v76
	v_pk_fma_f32 v[104:105], v[26:27], v[104:105], v[110:111]
	v_pk_fma_f32 v[110:111], v[18:19], v[96:97], v[100:101]
	v_lshlrev_b32_e32 v96, 16, v74
	v_and_b32_e32 v97, 0xffff0000, v74
	v_pk_fma_f32 v[108:109], v[30:31], v[108:109], v[114:115]
	v_pk_fma_f32 v[114:115], v[10:11], v[92:93], v[96:97]
	v_lshlrev_b32_e32 v92, 16, v72
	v_and_b32_e32 v93, 0xffff0000, v72
	v_lshlrev_b32_e32 v72, 16, v73
	v_and_b32_e32 v73, 0xffff0000, v73
	v_pk_fma_f32 v[112:113], v[34:35], v[112:113], v[116:117]
	v_pk_fma_f32 v[72:73], v[8:9], v[90:91], v[72:73]
	v_pk_fma_f32 v[90:91], v[6:7], v[88:89], v[92:93]
	v_lshlrev_b32_e32 v88, 16, v70
	v_and_b32_e32 v89, 0xffff0000, v70
	v_lshlrev_b32_e32 v70, 16, v71
	v_and_b32_e32 v71, 0xffff0000, v71
	v_pk_fma_f32 v[14:15], v[4:5], v[14:15], v[70:71]
	v_cvt_pk_bf16_f32 v112, v112, v113
	v_cvt_pk_bf16_f32 v108, v108, v109
	v_lshlrev_b32_e32 v78, 16, v79
	v_and_b32_e32 v101, 0xffff0000, v112
	v_and_b32_e32 v97, 0xffff0000, v108
	v_and_b32_e32 v79, 0xffff0000, v79
	v_lshlrev_b32_e32 v76, 16, v77
	v_and_b32_e32 v77, 0xffff0000, v77
	v_lshlrev_b32_e32 v100, 16, v112
	v_lshlrev_b32_e32 v96, 16, v108
	v_cvt_pk_bf16_f32 v117, v14, v15
	v_mul_f32_e32 v14, v101, v101
	v_mul_f32_e32 v15, v97, v97
	v_pk_fma_f32 v[78:79], v[24:25], v[102:103], v[78:79]
	v_pk_fma_f32 v[76:77], v[20:21], v[98:99], v[76:77]
	v_cvt_pk_bf16_f32 v113, v84, v85
	v_cvt_pk_bf16_f32 v109, v82, v83
	v_fmac_f32_e32 v14, v100, v100
	v_lshlrev_b32_e32 v102, 16, v113
	v_lshlrev_b32_e32 v98, 16, v109
	v_fmac_f32_e32 v15, v96, v96
	v_and_b32_e32 v103, 0xffff0000, v113
	v_and_b32_e32 v99, 0xffff0000, v109
	v_fmac_f32_e32 v14, v102, v102
	v_fmac_f32_e32 v15, v98, v98
	v_cvt_pk_bf16_f32 v104, v104, v105
	v_fmac_f32_e32 v14, v103, v103
	v_and_b32_e32 v93, 0xffff0000, v104
	v_fmac_f32_e32 v15, v99, v99
	v_lshlrev_b32_e32 v74, 16, v75
	v_and_b32_e32 v75, 0xffff0000, v75
	v_lshlrev_b32_e32 v92, 16, v104
	v_add_f32_e32 v14, v14, v15
	v_mul_f32_e32 v15, v93, v93
	v_pk_fma_f32 v[74:75], v[12:13], v[94:95], v[74:75]
	v_cvt_pk_bf16_f32 v105, v80, v81
	v_fmac_f32_e32 v15, v92, v92
	v_lshlrev_b32_e32 v94, 16, v105
	v_and_b32_e32 v95, 0xffff0000, v105
	v_fmac_f32_e32 v15, v94, v94
	v_pk_fma_f32 v[70:71], v[2:3], v[86:87], v[88:89]
	v_cvt_pk_bf16_f32 v106, v106, v107
	v_fmac_f32_e32 v15, v95, v95
	v_and_b32_e32 v87, 0xffff0000, v106
	v_lshlrev_b32_e32 v86, 16, v106
	v_add_f32_e32 v14, v14, v15
	v_mul_f32_e32 v15, v87, v87
	v_cvt_pk_bf16_f32 v107, v78, v79
	v_fmac_f32_e32 v15, v86, v86
	v_lshlrev_b32_e32 v88, 16, v107
	v_and_b32_e32 v89, 0xffff0000, v107
	v_fmac_f32_e32 v15, v88, v88
	v_cvt_pk_bf16_f32 v110, v110, v111
	v_fmac_f32_e32 v15, v89, v89
	v_and_b32_e32 v83, 0xffff0000, v110
	v_lshlrev_b32_e32 v82, 16, v110
	v_add_f32_e32 v14, v14, v15
	v_mul_f32_e32 v15, v83, v83
	v_cvt_pk_bf16_f32 v111, v76, v77
	v_fmac_f32_e32 v15, v82, v82
	v_lshlrev_b32_e32 v84, 16, v111
	v_and_b32_e32 v85, 0xffff0000, v111
	v_fmac_f32_e32 v15, v84, v84
	v_cvt_pk_bf16_f32 v114, v114, v115
	v_fmac_f32_e32 v15, v85, v85
	v_and_b32_e32 v79, 0xffff0000, v114
	v_lshlrev_b32_e32 v78, 16, v114
	v_add_f32_e32 v14, v14, v15
	v_mul_f32_e32 v15, v79, v79
	v_cvt_pk_bf16_f32 v115, v74, v75
	v_fmac_f32_e32 v15, v78, v78
	v_lshlrev_b32_e32 v80, 16, v115
	v_and_b32_e32 v81, 0xffff0000, v115
	v_fmac_f32_e32 v15, v80, v80
	v_cvt_pk_bf16_f32 v90, v90, v91
	v_cvt_pk_bf16_f32 v91, v72, v73
	v_cvt_pk_bf16_f32 v116, v70, v71
	v_fmac_f32_e32 v15, v81, v81
	v_and_b32_e32 v73, 0xffff0000, v116
	v_and_b32_e32 v72, 0xffff0000, v90
	v_add_f32_e32 v16, v14, v15
	v_lshlrev_b32_e32 v70, 16, v90
	v_lshlrev_b32_e32 v71, 16, v116
	v_pk_mul_f32 v[14:15], v[72:73], v[72:73]
	v_lshlrev_b32_e32 v74, 16, v91
	v_lshlrev_b32_e32 v75, 16, v117
	v_pk_fma_f32 v[14:15], v[70:71], v[70:71], v[14:15]
	v_and_b32_e32 v77, 0xffff0000, v117
	v_and_b32_e32 v76, 0xffff0000, v91
	v_pk_fma_f32 v[14:15], v[74:75], v[74:75], v[14:15]
	s_nop 0
	v_pk_fma_f32 v[14:15], v[76:77], v[76:77], v[14:15]
	s_nop 0
	v_add_f32_e32 v14, v16, v14
	v_add_f32_e32 v14, v14, v15
	s_waitcnt lgkmcnt(0)
	s_nop 1
	v_add_f32_dpp v14, v14, v14 quad_perm:[1,0,3,2] row_mask:0xf bank_mask:0xf
	s_waitcnt lgkmcnt(0)
	s_nop 1
	v_add_f32_dpp v14, v14, v14 quad_perm:[2,3,0,1] row_mask:0xf bank_mask:0xf
	s_waitcnt lgkmcnt(0)
	s_nop 1
	v_add_f32_dpp v14, v14, v14 row_half_mirror row_mask:0xf bank_mask:0xf
	s_waitcnt lgkmcnt(0)
	s_nop 1
	v_add_f32_dpp v16, v14, v14 row_mirror row_mask:0xf bank_mask:0xf
	v_mov_b32_e32 v120, v16
	s_nop 1
	v_permlane16_swap_b32_e32 v16, v120
	v_or_b32_e32 v14, 2, v38
	v_ashrrev_i32_e32 v15, 31, v14
	v_lshlrev_b64 v[118:119], 12, v[14:15]
	v_lshl_add_u64 v[14:15], v[48:49], 0, v[118:119]
	s_waitcnt lgkmcnt(0)
; #define LAS __attribute__((address_space(3)))
; __device__ __forceinline__ unsigned pk2(float lo, float hi) { unsigned r; asm("v_cvt_pk_bf16_f32 %0, %1, %2" : "=v"(r) : "v"(lo), "v"(hi)); return r; }
; __device__ __forceinline__ float bflo(unsigned u) { return __uint_as_float(u << 16); }
; __device__ __forceinline__ float bfhi(unsigned u) { return __uint_as_float(u & 0xffff0000u); }
; __device__ __forceinline__ void ph_norm1(const Params& p, int mode, LAS unsigned char* lds) {
;     ...
;             unsigned m = (unsigned)(__ballot(myslot[q] >= 0) & 0xffffull);
;             while (m) {
;                 const int e0 = __builtin_ctz(m); m &= m - 1u;
;                 const bool two = m != 0u; const int e1 = two ? __builtin_ctz(m) : e0; if (two) m &= m - 1u;
;     ...
;                 bf16_t* xo = (bf16_t*)(p.ws + WS_X) + (size_t)t * DM;
; #pragma unroll
;                 for (int j = 0; j < 8; ++j) { u32x2 w; w.x = pk2(v[j][0], v[j][1]); w.y = pk2(v[j][2], v[j][3]); *(u32x2*)(xo + 4 * lane + 256 * j) = w;
;                     v[j] = (f32x4){bflo(w.x), bfhi(w.x), bflo(w.y), bfhi(w.y)}; }
;             }
;             float ss = 0.f;
; #pragma unroll
;             for (int j = 0; j < 8; ++j) ss += v[j][0] * v[j][0] + v[j][1] * v[j][1] + v[j][2] * v[j][2] + v[j][3] * v[j][3];
;             const float r = 1.0f / sqrtf(wave_sum(ss) * (1.f / DM) + EPS);
;             asm volatile("" ::: "memory");
;             if (mode == 2) {
;                 float* o = p.out + (size_t)t * DM;
; #pragma unroll
;                 for (int j = 0; j < 8; ++j) { const f32x4 g = fgv[j]; __builtin_nontemporal_store(v[j] * r * g, (f32x4*)(o + 4 * lane + 256 * j)); }
;             } else {
;                 const float* g1 = p.in[5] + (size_t)DM;
;                 const float* sh = mod + ((size_t)4 + b) * 12288;
;                 const float* sc = sh + 2048;
;                 bf16_t* ho = (bf16_t*)(p.ws + WS_H) + (size_t)t * DM;
; #pragma unroll
;                 for (int j = 0; j < 8; ++j) {
;                     const f32x4 h = (v[j] * r) * *(const LAS f32x4*)(T1 + 4 * lane + 256 * j) + *(const LAS f32x4*)(T2 + 4 * lane + 256 * j);
;                     u32x2 w; w.x = pk2(h[0], h[1]); w.y = pk2(h[2], h[3]);
;                     *(u32x2*)(ho + 4 * lane + 256 * j) = w;
;                 }
	v_add_f32_e32 v16, v16, v120
	ds_bpermute_b32 v120, v142, v16
	global_store_dwordx2 v[14:15], v[112:113], off
	global_store_dwordx2 v[14:15], v[108:109], off offset:512
	global_store_dwordx2 v[14:15], v[104:105], off offset:1024
	global_store_dwordx2 v[14:15], v[106:107], off offset:1536
	global_store_dwordx2 v[14:15], v[110:111], off offset:2048
	global_store_dwordx2 v[14:15], v[114:115], off offset:2560
	global_store_dwordx2 v[14:15], v[90:91], off offset:3072
	global_store_dwordx2 v[14:15], v[116:117], off offset:3584
	s_waitcnt lgkmcnt(0)
	v_add_f32_e32 v16, v16, v120
	v_fmamk_f32 v16, v16, 0x3a000000, v217
	v_cmp_gt_f32_e32 vcc, s5, v16
	v_mul_f32_e32 v104, 0x4f800000, v16
	v_mov_b32_e32 v15, 0
	v_cndmask_b32_e32 v16, v16, v104, vcc
	v_sqrt_f32_e32 v104, v16
	s_nop 0
	v_add_u32_e32 v105, -1, v104
	v_fma_f32 v106, -v105, v104, v16
	v_cmp_ge_f32_e64 s[34:35], 0, v106
	v_add_u32_e32 v106, 1, v104
	s_nop 0
	v_cndmask_b32_e64 v105, v104, v105, s[34:35]
	v_fma_f32 v104, -v106, v104, v16
	v_cmp_lt_f32_e64 s[34:35], 0, v104
	s_nop 1
	v_cndmask_b32_e64 v104, v105, v106, s[34:35]
	v_mul_f32_e32 v105, 0x37800000, v104
	v_cndmask_b32_e32 v104, v104, v105, vcc
	v_cmp_class_f32_e32 vcc, v16, v219
	s_nop 1
	v_cndmask_b32_e32 v16, v104, v16, vcc
	v_div_scale_f32 v104, s[8:9], v16, v16, 1.0
	v_rcp_f32_e32 v105, v104
	s_nop 0
	v_fma_f32 v14, -v104, v105, 1.0
	v_fmac_f32_e32 v105, v14, v105
	v_div_scale_f32 v14, vcc, 1.0, v16, 1.0
	v_mul_f32_e32 v90, v14, v105
	v_fma_f32 v91, -v104, v90, v14
	v_fmac_f32_e32 v90, v91, v105
	v_fma_f32 v14, -v104, v90, v14
	v_div_fmas_f32 v14, v14, v105, v90
	ds_read_b128 v[104:107], v153
	ds_read_b128 v[108:111], v153 offset:8192
	v_div_fixup_f32 v14, v14, v16, 1.0
	v_pk_mul_f32 v[100:101], v[14:15], v[100:101] op_sel_hi:[0,1]
	v_pk_mul_f32 v[102:103], v[14:15], v[102:103] op_sel_hi:[0,1]
	v_lshl_add_u64 v[90:91], v[50:51], 0, v[118:119]
	s_waitcnt lgkmcnt(0)
	v_pk_fma_f32 v[100:101], v[104:105], v[100:101], v[108:109]
	v_pk_fma_f32 v[110:111], v[106:107], v[102:103], v[110:111]
	v_cvt_pk_bf16_f32 v108, v100, v101
	ds_read_b128 v[100:103], v153 offset:1024
	ds_read_b128 v[104:107], v153 offset:9216
	v_pk_mul_f32 v[96:97], v[14:15], v[96:97] op_sel_hi:[0,1]
	v_cvt_pk_bf16_f32 v109, v110, v111
	global_store_dwordx2 v[90:91], v[108:109], off
	v_pk_mul_f32 v[98:99], v[14:15], v[98:99] op_sel_hi:[0,1]
	s_waitcnt lgkmcnt(0)
	v_pk_fma_f32 v[96:97], v[100:101], v[96:97], v[104:105]
	v_pk_fma_f32 v[106:107], v[102:103], v[98:99], v[106:107]
	v_cvt_pk_bf16_f32 v104, v96, v97
	ds_read_b128 v[96:99], v153 offset:2048
	ds_read_b128 v[100:103], v153 offset:10240
	v_pk_mul_f32 v[92:93], v[14:15], v[92:93] op_sel_hi:[0,1]
	v_cvt_pk_bf16_f32 v105, v106, v107
	global_store_dwordx2 v[90:91], v[104:105], off offset:512
	v_pk_mul_f32 v[94:95], v[14:15], v[94:95] op_sel_hi:[0,1]
	s_waitcnt lgkmcnt(0)
	v_pk_fma_f32 v[92:93], v[92:93], v[96:97], v[100:101]
	v_pk_fma_f32 v[102:103], v[94:95], v[98:99], v[102:103]
	v_cvt_pk_bf16_f32 v100, v92, v93
	ds_read_b128 v[92:95], v153 offset:3072
	ds_read_b128 v[96:99], v153 offset:11264
	v_pk_mul_f32 v[86:87], v[14:15], v[86:87] op_sel_hi:[0,1]
	v_cvt_pk_bf16_f32 v101, v102, v103
	global_store_dwordx2 v[90:91], v[100:101], off offset:1024
	v_pk_mul_f32 v[88:89], v[14:15], v[88:89] op_sel_hi:[0,1]
	s_waitcnt lgkmcnt(0)
	v_pk_fma_f32 v[86:87], v[86:87], v[92:93], v[96:97]
	v_pk_fma_f32 v[98:99], v[88:89], v[94:95], v[98:99]
	v_cvt_pk_bf16_f32 v96, v86, v87
	ds_read_b128 v[86:89], v153 offset:4096
	ds_read_b128 v[92:95], v153 offset:12288
	v_pk_mul_f32 v[82:83], v[14:15], v[82:83] op_sel_hi:[0,1]
	v_cvt_pk_bf16_f32 v97, v98, v99
	global_store_dwordx2 v[90:91], v[96:97], off offset:1536
	v_pk_mul_f32 v[84:85], v[14:15], v[84:85] op_sel_hi:[0,1]
	s_waitcnt lgkmcnt(0)
	v_pk_fma_f32 v[82:83], v[82:83], v[86:87], v[92:93]
	v_pk_fma_f32 v[94:95], v[84:85], v[88:89], v[94:95]
	v_cvt_pk_bf16_f32 v92, v82, v83
	ds_read_b128 v[82:85], v153 offset:5120
	ds_read_b128 v[86:89], v153 offset:13312
	v_pk_mul_f32 v[78:79], v[14:15], v[78:79] op_sel_hi:[0,1]
	v_pk_mul_f32 v[80:81], v[14:15], v[80:81] op_sel_hi:[0,1]
	v_cvt_pk_bf16_f32 v93, v94, v95
	global_store_dwordx2 v[90:91], v[92:93], off offset:2048
	s_waitcnt lgkmcnt(0)
	v_pk_fma_f32 v[78:79], v[78:79], v[82:83], v[86:87]
	v_pk_fma_f32 v[80:81], v[80:81], v[84:85], v[88:89]
	v_cvt_pk_bf16_f32 v78, v78, v79
	v_mov_b32_e32 v86, v70
	v_cvt_pk_bf16_f32 v79, v80, v81
	global_store_dwordx2 v[90:91], v[78:79], off offset:2560
	ds_read_b128 v[78:81], v153 offset:6144
	ds_read_b128 v[82:85], v153 offset:14336
	v_mov_b32_e32 v87, v72
	v_pk_mul_f32 v[86:87], v[14:15], v[86:87] op_sel_hi:[0,1]
	v_mov_b32_e32 v88, v74
	v_mov_b32_e32 v89, v76
	v_pk_mul_f32 v[88:89], v[14:15], v[88:89] op_sel_hi:[0,1]
	s_waitcnt lgkmcnt(0)
	v_pk_fma_f32 v[78:79], v[86:87], v[78:79], v[82:83]
	v_pk_fma_f32 v[80:81], v[88:89], v[80:81], v[84:85]
	v_cvt_pk_bf16_f32 v78, v78, v79
	v_mov_b32_e32 v72, v71
	v_cvt_pk_bf16_f32 v79, v80, v81
	global_store_dwordx2 v[90:91], v[78:79], off offset:3072
	ds_read_b128 v[78:81], v153 offset:7168
	ds_read_b128 v[82:85], v153 offset:15360
	v_pk_mul_f32 v[70:71], v[14:15], v[72:73] op_sel_hi:[0,1]
	v_mov_b32_e32 v76, v75
	v_pk_mul_f32 v[72:73], v[14:15], v[76:77] op_sel_hi:[0,1]
	v_cmp_lt_i32_e32 vcc, -1, v17
	s_waitcnt lgkmcnt(0)
	v_pk_fma_f32 v[70:71], v[70:71], v[78:79], v[82:83]
	v_pk_fma_f32 v[72:73], v[72:73], v[80:81], v[84:85]
	v_cvt_pk_bf16_f32 v70, v70, v71
	s_and_b32 s4, vcc_lo, 0xffff
	v_cvt_pk_bf16_f32 v71, v72, v73
	global_store_dwordx2 v[90:91], v[70:71], off offset:3584
	s_cmp_eq_u32 s4, 0
	v_mov_b32_e32 v14, v15
	v_mov_b32_e32 v71, v15
	v_mov_b32_e32 v70, v15
	v_mov_b32_e32 v75, v15
	v_mov_b32_e32 v74, v15
	v_mov_b32_e32 v73, v15
	v_mov_b32_e32 v72, v15
	v_mov_b32_e32 v79, v15
	v_mov_b32_e32 v78, v15
	v_mov_b32_e32 v77, v15
	v_mov_b32_e32 v76, v15
	v_mov_b32_e32 v83, v15
	v_mov_b32_e32 v82, v15
	v_mov_b32_e32 v81, v15
	v_mov_b32_e32 v80, v15
	v_mov_b32_e32 v87, v15
	v_mov_b32_e32 v86, v15
	v_mov_b32_e32 v85, v15
	v_mov_b32_e32 v84, v15
	v_mov_b32_e32 v91, v15
	v_mov_b32_e32 v90, v15
	v_mov_b32_e32 v89, v15
	v_mov_b32_e32 v88, v15
	v_mov_b32_e32 v95, v15
	v_mov_b32_e32 v94, v15
	v_mov_b32_e32 v93, v15
	v_mov_b32_e32 v92, v15
	v_mov_b32_e32 v99, v15
	v_mov_b32_e32 v98, v15
	v_mov_b32_e32 v97, v15
	v_mov_b32_e32 v96, v15
	s_cbranch_scc1 .LBB0_343
; __device__ __forceinline__ void ph_norm1(const Params& p, int mode, LAS unsigned char* lds) {
;     ...
;             f32x4 macc[8];
; #pragma unroll
;             for (int j = 0; j < 8; ++j) macc[j] = (f32x4){0.f, 0.f, 0.f, 0.f};
	v_mov_b32_e32 v14, 0
	v_mov_b32_e32 v15, v14
	v_mov_b32_e32 v96, v14
	v_mov_b32_e32 v97, v14
	v_mov_b32_e32 v98, v14
	v_mov_b32_e32 v99, v14
	v_mov_b32_e32 v92, v14
	v_mov_b32_e32 v93, v14
	v_mov_b32_e32 v94, v14
	v_mov_b32_e32 v95, v14
	v_mov_b32_e32 v88, v14
	v_mov_b32_e32 v89, v14
	v_mov_b32_e32 v90, v14
	v_mov_b32_e32 v91, v14
	v_mov_b32_e32 v84, v14
	v_mov_b32_e32 v85, v14
	v_mov_b32_e32 v86, v14
	v_mov_b32_e32 v87, v14
	v_mov_b32_e32 v80, v14
	v_mov_b32_e32 v81, v14
	v_mov_b32_e32 v82, v14
	v_mov_b32_e32 v83, v14
	v_mov_b32_e32 v76, v14
	v_mov_b32_e32 v77, v14
	v_mov_b32_e32 v78, v14
	v_mov_b32_e32 v79, v14
	v_mov_b32_e32 v72, v14
	v_mov_b32_e32 v73, v14
	v_mov_b32_e32 v74, v14
	v_mov_b32_e32 v75, v14
	v_mov_b32_e32 v70, v14
	v_mov_b32_e32 v71, v14

; __device__ __forceinline__ void ph_norm1_l0(const Params& p) {
;     ...
;     for (int t4 = (blockIdx.x * 8 + wv) * 4; t4 < NT; t4 += gridDim.x * 32) {
;         const int b = t4 >> 11;
;         const float* xr = p.in[0] + (size_t)t4 * DM;
;         f32x4 v[4][8];
; #pragma unroll
;         for (int q = 0; q < 4; ++q)
; #pragma unroll
;             for (int j = 0; j < 8; ++j) v[q][j] = __builtin_nontemporal_load((const f32x4*)(xr + (size_t)q * DM + 4 * lane + 256 * j));
;         float sq[4] = {0.f, 0.f, 0.f, 0.f};
; #pragma unroll
;         for (int q = 0; q < 4; ++q)
; #pragma unroll
;             for (int j = 0; j < 8; ++j) sq[q] += v[q][j][0] * v[q][j][0] + v[q][j][1] * v[q][j][1] + v[q][j][2] * v[q][j][2] + v[q][j][3] * v[q][j][3];
.LBB0_363:
	v_ashrrev_i32_e32 v143, 31, v142
	v_lshlrev_b64 v[2:3], 13, v[142:143]
	s_waitcnt vmcnt(0)
	v_lshl_add_u64 v[26:27], v[154:155], 0, v[2:3]
	global_load_dwordx4 v[106:109], v[26:27], off nt
	global_load_dwordx4 v[90:93], v[26:27], off offset:1024 nt
	global_load_dwordx4 v[74:77], v[26:27], off offset:2048 nt
	global_load_dwordx4 v[58:61], v[26:27], off offset:3072 nt
	v_add_co_u32_e32 v2, vcc, 0x1000, v26
	s_movk_i32 s4, 0x5000
	s_nop 0
	v_addc_co_u32_e32 v3, vcc, 0, v27, vcc
	global_load_dwordx4 v[50:53], v[2:3], off nt
	global_load_dwordx4 v[38:41], v[2:3], off offset:1024 nt
	global_load_dwordx4 v[18:21], v[2:3], off offset:2048 nt
	s_nop 0
	global_load_dwordx4 v[2:5], v[2:3], off offset:3072 nt
	v_add_co_u32_e32 v6, vcc, s0, v26
	s_waitcnt vmcnt(7)
	v_mul_f32_e32 v130, v107, v107
	v_addc_co_u32_e32 v7, vcc, 0, v27, vcc
	v_add_co_u32_e32 v8, vcc, s11, v26
	s_waitcnt vmcnt(6)
	v_mul_f32_e32 v131, v91, v91
	v_addc_co_u32_e32 v9, vcc, 0, v27, vcc
	global_load_dwordx4 v[114:117], v[8:9], off offset:-4096 nt
	global_load_dwordx4 v[94:97], v[6:7], off offset:1024 nt
	global_load_dwordx4 v[78:81], v[6:7], off offset:2048 nt
	global_load_dwordx4 v[62:65], v[6:7], off offset:3072 nt
	global_load_dwordx4 v[46:49], v[8:9], off nt
	global_load_dwordx4 v[34:37], v[8:9], off offset:1024 nt
	global_load_dwordx4 v[14:17], v[8:9], off offset:2048 nt
	s_nop 0
	global_load_dwordx4 v[6:9], v[8:9], off offset:3072 nt
	v_add_co_u32_e32 v10, vcc, s43, v26
	v_fmac_f32_e32 v130, v106, v106
	s_nop 0
	v_addc_co_u32_e32 v11, vcc, 0, v27, vcc
	v_add_co_u32_e32 v12, vcc, s4, v26
	s_movk_i32 s4, 0x6000
	s_nop 0
	v_addc_co_u32_e32 v13, vcc, 0, v27, vcc
	global_load_dwordx4 v[118:121], v[12:13], off offset:-4096 nt
	global_load_dwordx4 v[102:105], v[10:11], off offset:1024 nt
	global_load_dwordx4 v[86:89], v[10:11], off offset:2048 nt
	global_load_dwordx4 v[70:73], v[10:11], off offset:3072 nt
	global_load_dwordx4 v[54:57], v[12:13], off nt
	global_load_dwordx4 v[42:45], v[12:13], off offset:1024 nt
	global_load_dwordx4 v[22:25], v[12:13], off offset:2048 nt
	s_nop 0
	global_load_dwordx4 v[10:13], v[12:13], off offset:3072 nt
	v_add_co_u32_e32 v28, vcc, s4, v26
	s_movk_i32 s4, 0x7000
	s_nop 0
	v_addc_co_u32_e32 v29, vcc, 0, v27, vcc
	v_add_co_u32_e32 v26, vcc, s4, v26
	v_fmac_f32_e32 v131, v90, v90
	s_nop 0
	v_addc_co_u32_e32 v27, vcc, 0, v27, vcc
	global_load_dwordx4 v[126:129], v[26:27], off offset:-4096 nt
	global_load_dwordx4 v[122:125], v[28:29], off offset:1024 nt
	global_load_dwordx4 v[110:113], v[28:29], off offset:2048 nt
	global_load_dwordx4 v[98:101], v[28:29], off offset:3072 nt
	global_load_dwordx4 v[82:85], v[26:27], off nt
	global_load_dwordx4 v[66:69], v[26:27], off offset:1024 nt
	global_load_dwordx4 v[30:33], v[26:27], off offset:2048 nt
	s_nop 0
	global_load_dwordx4 v[26:29], v[26:27], off offset:3072 nt
	v_fmac_f32_e32 v130, v108, v108
	v_fmac_f32_e32 v131, v92, v92
	v_fmac_f32_e32 v130, v109, v109
	v_fmac_f32_e32 v131, v93, v93
	v_add_f32_e32 v130, v130, v131
	s_waitcnt vmcnt(29)
	v_mul_f32_e32 v131, v75, v75
	v_fmac_f32_e32 v131, v74, v74
	v_fmac_f32_e32 v131, v76, v76
	v_fmac_f32_e32 v131, v77, v77
	v_add_f32_e32 v130, v130, v131
	s_waitcnt vmcnt(28)
	v_mul_f32_e32 v131, v59, v59
	v_fmac_f32_e32 v131, v58, v58
	v_fmac_f32_e32 v131, v60, v60
	v_fmac_f32_e32 v131, v61, v61
	v_add_f32_e32 v130, v130, v131
	s_waitcnt vmcnt(27)
	v_mul_f32_e32 v131, v51, v51
	v_fmac_f32_e32 v131, v50, v50
	v_fmac_f32_e32 v131, v52, v52
	v_fmac_f32_e32 v131, v53, v53
	v_add_f32_e32 v130, v130, v131
	s_waitcnt vmcnt(26)
	v_mul_f32_e32 v131, v39, v39
	v_fmac_f32_e32 v131, v38, v38
	v_fmac_f32_e32 v131, v40, v40
	v_fmac_f32_e32 v131, v41, v41
	s_waitcnt vmcnt(25)
	v_mov_b32_e32 v132, v19
	s_waitcnt vmcnt(24)
	v_mov_b32_e32 v133, v3
	v_add_f32_e32 v134, v130, v131
	v_mov_b32_e32 v130, v18
	v_mov_b32_e32 v131, v2
	v_pk_mul_f32 v[132:133], v[132:133], v[132:133]
	s_nop 0
	v_pk_fma_f32 v[130:131], v[130:131], v[130:131], v[132:133]
	v_mov_b32_e32 v132, v20
	v_mov_b32_e32 v133, v4
	v_pk_fma_f32 v[130:131], v[132:133], v[132:133], v[130:131]
	v_mov_b32_e32 v132, v21
	v_mov_b32_e32 v133, v5
	v_pk_fma_f32 v[130:131], v[132:133], v[132:133], v[130:131]
	s_waitcnt vmcnt(17)
	v_mov_b32_e32 v132, v15
	v_add_f32_e32 v130, v134, v130
	v_add_f32_e32 v134, v130, v131
	v_mul_f32_e32 v130, v115, v115
	v_mul_f32_e32 v131, v95, v95
	v_fmac_f32_e32 v130, v114, v114
	v_fmac_f32_e32 v131, v94, v94
	v_fmac_f32_e32 v130, v116, v116
	v_fmac_f32_e32 v131, v96, v96
	v_fmac_f32_e32 v130, v117, v117
	v_fmac_f32_e32 v131, v97, v97
	v_add_f32_e32 v130, v130, v131
	v_mul_f32_e32 v131, v79, v79
	v_fmac_f32_e32 v131, v78, v78
	v_fmac_f32_e32 v131, v80, v80
	v_fmac_f32_e32 v131, v81, v81
	v_add_f32_e32 v130, v130, v131
	v_mul_f32_e32 v131, v63, v63
	v_fmac_f32_e32 v131, v62, v62
	v_fmac_f32_e32 v131, v64, v64
	v_fmac_f32_e32 v131, v65, v65
	v_add_f32_e32 v130, v130, v131
	v_mul_f32_e32 v131, v47, v47
	v_fmac_f32_e32 v131, v46, v46
	v_fmac_f32_e32 v131, v48, v48
	v_fmac_f32_e32 v131, v49, v49
	v_add_f32_e32 v130, v130, v131
	v_mul_f32_e32 v131, v35, v35
	v_fmac_f32_e32 v131, v34, v34
	v_fmac_f32_e32 v131, v36, v36
	v_fmac_f32_e32 v131, v37, v37
	s_waitcnt vmcnt(16)
	v_mov_b32_e32 v133, v7
	v_add_f32_e32 v135, v130, v131
	v_mov_b32_e32 v130, v14
	v_mov_b32_e32 v131, v6
	v_pk_mul_f32 v[132:133], v[132:133], v[132:133]
	s_nop 0
	v_pk_fma_f32 v[130:131], v[130:131], v[130:131], v[132:133]
	v_mov_b32_e32 v132, v16
	v_mov_b32_e32 v133, v8
	v_pk_fma_f32 v[130:131], v[132:133], v[132:133], v[130:131]
	v_mov_b32_e32 v132, v17
	v_mov_b32_e32 v133, v9
	v_pk_fma_f32 v[130:131], v[132:133], v[132:133], v[130:131]
	s_waitcnt vmcnt(9)
; __device__ __forceinline__ void ph_norm1_l0(const Params& p) {
;     ...
;         float sq[4] = {0.f, 0.f, 0.f, 0.f};
; #pragma unroll
;         for (int q = 0; q < 4; ++q)
; #pragma unroll
;             for (int j = 0; j < 8; ++j) sq[q] += v[q][j][0] * v[q][j][0] + v[q][j][1] * v[q][j][1] + v[q][j][2] * v[q][j][2] + v[q][j][3] * v[q][j][3];
; #pragma unroll
;         for (int o = 1; o < 64; o <<= 1)
; #pragma unroll
;             for (int q = 0; q < 4; ++q) sq[q] += __shfl_xor(sq[q], o);
	v_mov_b32_e32 v132, v23
	v_add_f32_e32 v130, v135, v130
	v_add_f32_e32 v135, v130, v131
	v_mul_f32_e32 v130, v119, v119
	v_mul_f32_e32 v131, v103, v103
	v_fmac_f32_e32 v130, v118, v118
	v_fmac_f32_e32 v131, v102, v102
	v_fmac_f32_e32 v130, v120, v120
	v_fmac_f32_e32 v131, v104, v104
	v_fmac_f32_e32 v130, v121, v121
	v_fmac_f32_e32 v131, v105, v105
	v_add_f32_e32 v130, v130, v131
	v_mul_f32_e32 v131, v87, v87
	v_fmac_f32_e32 v131, v86, v86
	v_fmac_f32_e32 v131, v88, v88
	v_fmac_f32_e32 v131, v89, v89
	v_add_f32_e32 v130, v130, v131
	v_mul_f32_e32 v131, v71, v71
	v_fmac_f32_e32 v131, v70, v70
	v_fmac_f32_e32 v131, v72, v72
	v_fmac_f32_e32 v131, v73, v73
	v_add_f32_e32 v130, v130, v131
	v_mul_f32_e32 v131, v55, v55
	v_fmac_f32_e32 v131, v54, v54
	v_fmac_f32_e32 v131, v56, v56
	v_fmac_f32_e32 v131, v57, v57
	v_add_f32_e32 v130, v130, v131
	v_mul_f32_e32 v131, v43, v43
	v_fmac_f32_e32 v131, v42, v42
	v_fmac_f32_e32 v131, v44, v44
	v_fmac_f32_e32 v131, v45, v45
	s_waitcnt vmcnt(8)
	v_mov_b32_e32 v133, v11
	v_add_f32_e32 v136, v130, v131
	v_mov_b32_e32 v130, v22
	v_mov_b32_e32 v131, v10
	v_pk_mul_f32 v[132:133], v[132:133], v[132:133]
	s_nop 0
	v_pk_fma_f32 v[130:131], v[130:131], v[130:131], v[132:133]
	v_mov_b32_e32 v132, v24
	v_mov_b32_e32 v133, v12
	v_pk_fma_f32 v[130:131], v[132:133], v[132:133], v[130:131]
	v_mov_b32_e32 v132, v25
	v_mov_b32_e32 v133, v13
	v_pk_fma_f32 v[130:131], v[132:133], v[132:133], v[130:131]
	s_waitcnt vmcnt(1)
	v_mov_b32_e32 v132, v31
	v_add_f32_e32 v130, v136, v130
	v_add_f32_e32 v136, v130, v131
	v_mul_f32_e32 v130, v127, v127
	v_mul_f32_e32 v131, v123, v123
	v_fmac_f32_e32 v130, v126, v126
	v_fmac_f32_e32 v131, v122, v122
	v_fmac_f32_e32 v130, v128, v128
	v_fmac_f32_e32 v131, v124, v124
	v_fmac_f32_e32 v130, v129, v129
	v_fmac_f32_e32 v131, v125, v125
	v_add_f32_e32 v130, v130, v131
	v_mul_f32_e32 v131, v111, v111
	v_fmac_f32_e32 v131, v110, v110
	v_fmac_f32_e32 v131, v112, v112
	v_fmac_f32_e32 v131, v113, v113
	v_add_f32_e32 v130, v130, v131
	v_mul_f32_e32 v131, v99, v99
	v_fmac_f32_e32 v131, v98, v98
	v_fmac_f32_e32 v131, v100, v100
	v_fmac_f32_e32 v131, v101, v101
	v_add_f32_e32 v130, v130, v131
	v_mul_f32_e32 v131, v83, v83
	v_fmac_f32_e32 v131, v82, v82
	v_fmac_f32_e32 v131, v84, v84
	v_fmac_f32_e32 v131, v85, v85
	v_add_f32_e32 v130, v130, v131
	v_mul_f32_e32 v131, v67, v67
	v_fmac_f32_e32 v131, v66, v66
	v_fmac_f32_e32 v131, v68, v68
	v_fmac_f32_e32 v131, v69, v69
	s_waitcnt vmcnt(0)
	v_mov_b32_e32 v133, v27
	v_add_f32_e32 v137, v130, v131
	v_mov_b32_e32 v130, v30
	v_mov_b32_e32 v131, v26
	v_pk_mul_f32 v[132:133], v[132:133], v[132:133]
	s_nop 0
	v_pk_fma_f32 v[130:131], v[130:131], v[130:131], v[132:133]
	v_mov_b32_e32 v132, v32
	v_mov_b32_e32 v133, v28
	v_pk_fma_f32 v[130:131], v[132:133], v[132:133], v[130:131]
	v_mov_b32_e32 v132, v33
	v_mov_b32_e32 v133, v29
	v_pk_fma_f32 v[130:131], v[132:133], v[132:133], v[130:131]
	v_add_f32_e32 v130, v137, v130
	v_add_f32_e32 v130, v130, v131
	s_waitcnt lgkmcnt(2)
	s_nop 1
	v_add_f32_dpp v132, v135, v135 quad_perm:[1,0,3,2] row_mask:0xf bank_mask:0xf
	s_waitcnt lgkmcnt(1)
	s_nop 1
	v_add_f32_dpp v131, v134, v134 quad_perm:[1,0,3,2] row_mask:0xf bank_mask:0xf
	s_waitcnt lgkmcnt(1)
	s_nop 1
	v_add_f32_dpp v133, v136, v136 quad_perm:[1,0,3,2] row_mask:0xf bank_mask:0xf
	s_waitcnt lgkmcnt(0)
	s_nop 1
	v_add_f32_dpp v130, v130, v130 quad_perm:[1,0,3,2] row_mask:0xf bank_mask:0xf
	s_waitcnt lgkmcnt(0)
	s_nop 1
	v_add_f32_dpp v131, v131, v131 quad_perm:[2,3,0,1] row_mask:0xf bank_mask:0xf
	s_waitcnt lgkmcnt(0)
	s_nop 1
	v_add_f32_dpp v132, v132, v132 quad_perm:[2,3,0,1] row_mask:0xf bank_mask:0xf
	s_waitcnt lgkmcnt(0)
	s_nop 1
	v_add_f32_dpp v133, v133, v133 quad_perm:[2,3,0,1] row_mask:0xf bank_mask:0xf
	s_waitcnt lgkmcnt(0)
	s_nop 1
	v_add_f32_dpp v130, v130, v130 quad_perm:[2,3,0,1] row_mask:0xf bank_mask:0xf
	s_waitcnt lgkmcnt(0)
	s_nop 1
	v_add_f32_dpp v131, v131, v131 row_half_mirror row_mask:0xf bank_mask:0xf
	s_waitcnt lgkmcnt(0)
	s_nop 1
	v_add_f32_dpp v132, v132, v132 row_half_mirror row_mask:0xf bank_mask:0xf
	s_waitcnt lgkmcnt(0)
	s_nop 1
	v_add_f32_dpp v133, v133, v133 row_half_mirror row_mask:0xf bank_mask:0xf
	s_waitcnt lgkmcnt(0)
	s_nop 1
	v_add_f32_dpp v130, v130, v130 row_half_mirror row_mask:0xf bank_mask:0xf
	s_waitcnt lgkmcnt(0)
	s_nop 1
	v_add_f32_dpp v131, v131, v131 row_mirror row_mask:0xf bank_mask:0xf
	s_waitcnt lgkmcnt(0)
	s_nop 1
	v_add_f32_dpp v132, v132, v132 row_mirror row_mask:0xf bank_mask:0xf
	s_waitcnt lgkmcnt(0)
	s_nop 1
	v_add_f32_dpp v133, v133, v133 row_mirror row_mask:0xf bank_mask:0xf
	s_waitcnt lgkmcnt(0)
	s_nop 1
	v_add_f32_dpp v130, v130, v130 row_mirror row_mask:0xf bank_mask:0xf
	v_mov_b32_e32 v134, v131
	s_nop 1
	v_permlane16_swap_b32_e32 v131, v134
	s_waitcnt lgkmcnt(0)
	v_add_f32_e32 v131, v131, v134
	v_mov_b32_e32 v134, v132
	s_nop 1
	v_permlane16_swap_b32_e32 v132, v134
	s_waitcnt lgkmcnt(0)
	v_add_f32_e32 v132, v132, v134
	v_mov_b32_e32 v134, v133
	s_nop 1
	v_permlane16_swap_b32_e32 v133, v134
	s_waitcnt lgkmcnt(0)
	v_add_f32_e32 v133, v133, v134
	v_mov_b32_e32 v134, v130
	s_nop 1
	v_permlane16_swap_b32_e32 v130, v134
	s_waitcnt lgkmcnt(0)
	v_add_f32_e32 v130, v130, v134
	v_mov_b32_e32 v134, v131
	s_nop 1
	v_permlane32_swap_b32_e32 v131, v134
	s_waitcnt lgkmcnt(0)
	v_add_f32_e32 v131, v131, v134
	v_mov_b32_e32 v134, v132
	s_nop 1
	v_permlane32_swap_b32_e32 v132, v134
	v_fmamk_f32 v131, v131, 0x3a000000, v217
	v_cmp_gt_f32_e32 vcc, s5, v131
	s_waitcnt lgkmcnt(0)
	v_add_f32_e32 v132, v132, v134
	v_mov_b32_e32 v134, v133
	s_nop 1
	v_permlane32_swap_b32_e32 v133, v134
	s_waitcnt lgkmcnt(0)
; __device__ __forceinline__ void ph_norm1_l0(const Params& p) {
;     ...
; #pragma unroll
;         for (int o = 1; o < 64; o <<= 1)
; #pragma unroll
;             for (int q = 0; q < 4; ++q) sq[q] += __shfl_xor(sq[q], o);
;         float rq[4];
; #pragma unroll
;         for (int q = 0; q < 4; ++q) rq[q] = 1.0f / sqrtf(sq[q] * (1.f / DM) + EPS);
;         const float* sh = mod + (size_t)b * 12288;
;         const float* sc = sh + 2048;
;         bf16_t* ho = (bf16_t*)(p.ws + WS_H) + (size_t)t4 * DM;
; #pragma unroll
;         for (int j = 0; j < 8; ++j) {
;             const f32x4 g = *(const f32x4*)(g1 + 4 * lane + 256 * j), s1 = *(const f32x4*)(sc + 4 * lane + 256 * j), s0 = *(const f32x4*)(sh + 4 * lane + 256 * j);
;             const f32x4 gg = g * (s1 + 1.f);
; #pragma unroll
;             for (int q = 0; q < 4; ++q) {
;                 const f32x4 hq = (v[q][j] * rq[q]) * gg + s0;
	v_add_f32_e32 v133, v133, v134
	v_mov_b32_e32 v134, v130
	s_nop 1
	v_permlane32_swap_b32_e32 v130, v134
	s_waitcnt lgkmcnt(0)
	v_add_f32_e32 v130, v130, v134
	v_mul_f32_e32 v134, 0x4f800000, v131
	v_cndmask_b32_e32 v131, v131, v134, vcc
	v_sqrt_f32_e32 v134, v131
	v_fmamk_f32 v130, v130, 0x3a000000, v217
	v_add_u32_e32 v135, -1, v134
	v_fma_f32 v136, -v135, v134, v131
	v_cmp_ge_f32_e64 s[34:35], 0, v136
	v_add_u32_e32 v136, 1, v134
	s_nop 0
	v_cndmask_b32_e64 v135, v134, v135, s[34:35]
	v_fma_f32 v134, -v136, v134, v131
	v_cmp_lt_f32_e64 s[34:35], 0, v134
	s_nop 1
	v_cndmask_b32_e64 v134, v135, v136, s[34:35]
	v_mul_f32_e32 v135, 0x37800000, v134
	v_cndmask_b32_e32 v134, v134, v135, vcc
	v_cmp_class_f32_e32 vcc, v131, v219
	s_nop 1
	v_cndmask_b32_e32 v131, v134, v131, vcc
	v_div_scale_f32 v134, s[8:9], v131, v131, 1.0
	v_rcp_f32_e32 v135, v134
	s_nop 0
	v_fma_f32 v136, -v134, v135, 1.0
	v_fmac_f32_e32 v135, v136, v135
	v_div_scale_f32 v136, vcc, 1.0, v131, 1.0
	v_mul_f32_e32 v137, v136, v135
	v_fma_f32 v138, -v134, v137, v136
	v_fmac_f32_e32 v137, v138, v135
	v_fma_f32 v134, -v134, v137, v136
	v_div_fmas_f32 v134, v134, v135, v137
	v_div_fixup_f32 v158, v134, v131, 1.0
	v_fmamk_f32 v131, v132, 0x3a000000, v217
	v_cmp_gt_f32_e32 vcc, s5, v131
	v_mul_f32_e32 v132, 0x4f800000, v131
	v_pk_mul_f32 v[106:107], v[106:107], v[158:159] op_sel_hi:[1,0]
	v_cndmask_b32_e32 v131, v131, v132, vcc
	v_sqrt_f32_e32 v132, v131
	v_pk_mul_f32 v[108:109], v[108:109], v[158:159] op_sel_hi:[1,0]
	v_pk_mul_f32 v[90:91], v[90:91], v[158:159] op_sel_hi:[1,0]
	v_pk_mul_f32 v[92:93], v[92:93], v[158:159] op_sel_hi:[1,0]
	v_add_u32_e32 v134, -1, v132
	v_fma_f32 v135, -v134, v132, v131
	v_cmp_ge_f32_e64 s[34:35], 0, v135
	v_add_u32_e32 v135, 1, v132
	v_pk_mul_f32 v[74:75], v[74:75], v[158:159] op_sel_hi:[1,0]
	v_cndmask_b32_e64 v134, v132, v134, s[34:35]
	v_fma_f32 v132, -v135, v132, v131
	v_cmp_lt_f32_e64 s[34:35], 0, v132
	v_pk_mul_f32 v[76:77], v[76:77], v[158:159] op_sel_hi:[1,0]
	v_pk_mul_f32 v[58:59], v[58:59], v[158:159] op_sel_hi:[1,0]
	v_cndmask_b32_e64 v132, v134, v135, s[34:35]
	v_mul_f32_e32 v134, 0x37800000, v132
	v_cndmask_b32_e32 v132, v132, v134, vcc
	v_cmp_class_f32_e32 vcc, v131, v219
	v_pk_mul_f32 v[60:61], v[60:61], v[158:159] op_sel_hi:[1,0]
	v_pk_mul_f32 v[50:51], v[50:51], v[158:159] op_sel_hi:[1,0]
	v_cndmask_b32_e32 v131, v132, v131, vcc
	v_div_scale_f32 v132, s[8:9], v131, v131, 1.0
	v_rcp_f32_e32 v134, v132
	v_pk_mul_f32 v[52:53], v[52:53], v[158:159] op_sel_hi:[1,0]
	v_pk_mul_f32 v[38:39], v[38:39], v[158:159] op_sel_hi:[1,0]
	v_pk_mul_f32 v[40:41], v[40:41], v[158:159] op_sel_hi:[1,0]
	v_fma_f32 v135, -v132, v134, 1.0
	v_fmac_f32_e32 v134, v135, v134
	v_div_scale_f32 v135, vcc, 1.0, v131, 1.0
	v_mul_f32_e32 v136, v135, v134
	v_fma_f32 v137, -v132, v136, v135
	v_fmac_f32_e32 v136, v137, v134
	v_fma_f32 v132, -v132, v136, v135
	v_div_fmas_f32 v132, v132, v134, v136
	v_div_fixup_f32 v160, v132, v131, 1.0
	v_fmamk_f32 v131, v133, 0x3a000000, v217
	v_cmp_gt_f32_e32 vcc, s5, v131
	v_mul_f32_e32 v132, 0x4f800000, v131
	v_pk_mul_f32 v[46:47], v[46:47], v[160:161] op_sel_hi:[1,0]
	v_cndmask_b32_e32 v131, v131, v132, vcc
	v_sqrt_f32_e32 v132, v131
	v_pk_mul_f32 v[48:49], v[48:49], v[160:161] op_sel_hi:[1,0]
	v_pk_mul_f32 v[34:35], v[34:35], v[160:161] op_sel_hi:[1,0]
	v_pk_mul_f32 v[36:37], v[36:37], v[160:161] op_sel_hi:[1,0]
	v_add_u32_e32 v133, -1, v132
	v_fma_f32 v134, -v133, v132, v131
	v_cmp_ge_f32_e64 s[34:35], 0, v134
	v_add_u32_e32 v134, 1, v132
	v_pk_mul_f32 v[14:15], v[14:15], v[160:161] op_sel_hi:[1,0]
	v_cndmask_b32_e64 v133, v132, v133, s[34:35]
	v_fma_f32 v132, -v134, v132, v131
	v_cmp_lt_f32_e64 s[34:35], 0, v132
	v_pk_mul_f32 v[16:17], v[16:17], v[160:161] op_sel_hi:[1,0]
	v_pk_mul_f32 v[18:19], v[18:19], v[158:159] op_sel_hi:[1,0]
	v_cndmask_b32_e64 v132, v133, v134, s[34:35]
	v_mul_f32_e32 v133, 0x37800000, v132
	v_cndmask_b32_e32 v132, v132, v133, vcc
	v_cmp_class_f32_e32 vcc, v131, v219
	v_pk_mul_f32 v[20:21], v[20:21], v[158:159] op_sel_hi:[1,0]
	v_pk_mul_f32 v[2:3], v[2:3], v[158:159] op_sel_hi:[1,0]
	v_cndmask_b32_e32 v131, v132, v131, vcc
	v_div_scale_f32 v132, s[8:9], v131, v131, 1.0
	v_rcp_f32_e32 v133, v132
	v_pk_mul_f32 v[4:5], v[4:5], v[158:159] op_sel_hi:[1,0]
	v_fma_f32 v134, -v132, v133, 1.0
	v_fmac_f32_e32 v133, v134, v133
	v_div_scale_f32 v134, vcc, 1.0, v131, 1.0
	v_mul_f32_e32 v135, v134, v133
	v_fma_f32 v136, -v132, v135, v134
	v_fmac_f32_e32 v135, v136, v133
	v_fma_f32 v132, -v132, v135, v134
	v_div_fmas_f32 v132, v132, v133, v135
	v_div_fixup_f32 v162, v132, v131, 1.0
	v_cmp_gt_f32_e32 vcc, s5, v130
	v_mul_f32_e32 v131, 0x4f800000, v130
	s_nop 0
	v_cndmask_b32_e32 v130, v130, v131, vcc
	v_sqrt_f32_e32 v131, v130
	s_nop 0
	v_add_u32_e32 v132, -1, v131
	v_fma_f32 v133, -v132, v131, v130
	v_cmp_ge_f32_e64 s[34:35], 0, v133
	v_add_u32_e32 v133, 1, v131
	s_nop 0
	v_cndmask_b32_e64 v132, v131, v132, s[34:35]
	v_fma_f32 v131, -v133, v131, v130
	v_cmp_lt_f32_e64 s[34:35], 0, v131
	s_nop 1
	v_cndmask_b32_e64 v131, v132, v133, s[34:35]
	v_mul_f32_e32 v132, 0x37800000, v131
	v_cndmask_b32_e32 v131, v131, v132, vcc
	v_cmp_class_f32_e32 vcc, v130, v219
	s_nop 1
	v_cndmask_b32_e32 v130, v131, v130, vcc
	v_div_scale_f32 v131, s[8:9], v130, v130, 1.0
	v_rcp_f32_e32 v132, v131
	s_nop 0
	v_fma_f32 v133, -v131, v132, 1.0
	v_fmac_f32_e32 v132, v133, v132
	v_div_scale_f32 v133, vcc, 1.0, v130, 1.0
	v_mul_f32_e32 v134, v133, v132
	v_fma_f32 v135, -v131, v134, v133
	v_fmac_f32_e32 v134, v135, v132
	v_fma_f32 v131, -v131, v134, v133
	v_div_fmas_f32 v131, v131, v132, v134
	v_div_fixup_f32 v164, v131, v130, 1.0
	v_ashrrev_i32_e32 v130, 11, v142
	v_mul_hi_i32_i24_e32 v131, 0xc000, v130
	v_mul_i32_i24_e32 v130, 0xc000, v130
	v_lshl_add_u64 v[130:131], s[52:53], 0, v[130:131]
	v_lshl_add_u64 v[170:171], v[130:131], 0, v[194:195]
	v_add_co_u32_e32 v168, vcc, s11, v170
	v_lshlrev_b64 v[130:131], 12, v[142:143]
	s_nop 0
	v_addc_co_u32_e32 v169, vcc, 0, v171, vcc
	v_lshl_add_u64 v[166:167], v[156:157], 0, v[130:131]
	global_load_dwordx4 v[134:137], v[144:145], off
	global_load_dwordx4 v[138:141], v[168:169], off offset:-4096
	global_load_dwordx4 v[130:133], v[170:171], off
	v_lshl_add_u64 v[172:173], v[170:171], 0, s[22:23]
	v_add_u32_e32 v142, s20, v142
	s_waitcnt vmcnt(1)
; __device__ __forceinline__ unsigned pk2(float lo, float hi) { unsigned r; asm("v_cvt_pk_bf16_f32 %0, %1, %2" : "=v"(r) : "v"(lo), "v"(hi)); return r; }
; __device__ __forceinline__ void ph_norm1_l0(const Params& p) {
;     ...
; #pragma unroll
;         for (int j = 0; j < 8; ++j) {
;             const f32x4 g = *(const f32x4*)(g1 + 4 * lane + 256 * j), s1 = *(const f32x4*)(sc + 4 * lane + 256 * j), s0 = *(const f32x4*)(sh + 4 * lane + 256 * j);
;             const f32x4 gg = g * (s1 + 1.f);
; #pragma unroll
;             for (int q = 0; q < 4; ++q) {
;                 const f32x4 hq = (v[q][j] * rq[q]) * gg + s0;
;                 u32x2 w; w.x = pk2(hq[0], hq[1]); w.y = pk2(hq[2], hq[3]);
;                 *(u32x2*)(ho + (size_t)q * DM + 4 * lane + 256 * j) = w;
;             }
;         }
	v_pk_add_f32 v[138:139], v[138:139], 1.0 op_sel_hi:[1,0]
	v_pk_add_f32 v[140:141], v[140:141], 1.0 op_sel_hi:[1,0]
	v_pk_mul_f32 v[134:135], v[134:135], v[138:139]
	v_pk_mul_f32 v[136:137], v[136:137], v[140:141]
	s_waitcnt vmcnt(0)
	v_pk_fma_f32 v[106:107], v[134:135], v[106:107], v[130:131]
	v_pk_fma_f32 v[108:109], v[136:137], v[108:109], v[132:133]
	v_cvt_pk_bf16_f32 v106, v106, v107
	s_nop 0
	v_cvt_pk_bf16_f32 v107, v108, v109
	global_store_dwordx2 v[166:167], v[106:107], off
	v_pk_mul_f32 v[106:107], v[114:115], v[160:161] op_sel_hi:[1,0]
	v_pk_mul_f32 v[108:109], v[116:117], v[160:161] op_sel_hi:[1,0]
	v_pk_fma_f32 v[106:107], v[134:135], v[106:107], v[130:131]
	v_pk_fma_f32 v[108:109], v[136:137], v[108:109], v[132:133]
	v_cvt_pk_bf16_f32 v114, v106, v107
	v_add_co_u32_e32 v106, vcc, s10, v166
	v_cvt_pk_bf16_f32 v115, v108, v109
	v_pk_mul_f32 v[116:117], v[120:121], v[162:163] op_sel_hi:[1,0]
	s_nop 0
	v_addc_co_u32_e32 v107, vcc, 0, v167, vcc
	v_add_co_u32_e32 v108, vcc, s0, v166
	v_pk_fma_f32 v[116:117], v[136:137], v[116:117], v[132:133]
	s_nop 0
	v_addc_co_u32_e32 v109, vcc, 0, v167, vcc
	global_store_dwordx2 v[108:109], v[114:115], off offset:-4096
	v_pk_mul_f32 v[114:115], v[118:119], v[162:163] op_sel_hi:[1,0]
	s_nop 0
	v_pk_fma_f32 v[114:115], v[134:135], v[114:115], v[130:131]
	s_nop 0
	v_cvt_pk_bf16_f32 v114, v114, v115
	v_cvt_pk_bf16_f32 v115, v116, v117
	global_store_dwordx2 v[108:109], v[114:115], off
	v_pk_mul_f32 v[114:115], v[126:127], v[164:165] op_sel_hi:[1,0]
	v_pk_mul_f32 v[116:117], v[128:129], v[164:165] op_sel_hi:[1,0]
	v_pk_fma_f32 v[114:115], v[134:135], v[114:115], v[130:131]
	v_pk_fma_f32 v[116:117], v[136:137], v[116:117], v[132:133]
	v_cvt_pk_bf16_f32 v118, v114, v115
	v_add_co_u32_e32 v114, vcc, s11, v166
	v_cvt_pk_bf16_f32 v119, v116, v117
	s_nop 1
	v_addc_co_u32_e32 v115, vcc, 0, v167, vcc
	global_store_dwordx2 v[114:115], v[118:119], off
	global_load_dwordx4 v[116:119], v[144:145], off offset:1024
	s_nop 0
	global_load_dwordx4 v[126:129], v[172:173], off offset:1024
	global_load_dwordx4 v[130:133], v[170:171], off offset:1024
	s_waitcnt vmcnt(1)
	v_pk_add_f32 v[126:127], v[126:127], 1.0 op_sel_hi:[1,0]
	v_pk_add_f32 v[120:121], v[128:129], 1.0 op_sel_hi:[1,0]
	v_pk_mul_f32 v[116:117], v[116:117], v[126:127]
	v_pk_mul_f32 v[118:119], v[118:119], v[120:121]
	s_waitcnt vmcnt(0)
	v_pk_fma_f32 v[90:91], v[90:91], v[116:117], v[130:131]
	v_pk_fma_f32 v[92:93], v[92:93], v[118:119], v[132:133]
	v_cvt_pk_bf16_f32 v90, v90, v91
	s_nop 0
	v_cvt_pk_bf16_f32 v91, v92, v93
	global_store_dwordx2 v[166:167], v[90:91], off offset:512
	v_pk_mul_f32 v[90:91], v[94:95], v[160:161] op_sel_hi:[1,0]
	v_pk_mul_f32 v[92:93], v[96:97], v[160:161] op_sel_hi:[1,0]
	v_pk_fma_f32 v[90:91], v[90:91], v[116:117], v[130:131]
	v_pk_fma_f32 v[92:93], v[92:93], v[118:119], v[132:133]
	v_cvt_pk_bf16_f32 v90, v90, v91
	s_nop 0
	v_cvt_pk_bf16_f32 v91, v92, v93
	global_store_dwordx2 v[106:107], v[90:91], off offset:512
	v_pk_mul_f32 v[90:91], v[102:103], v[162:163] op_sel_hi:[1,0]
	v_pk_mul_f32 v[92:93], v[104:105], v[162:163] op_sel_hi:[1,0]
	v_pk_fma_f32 v[90:91], v[90:91], v[116:117], v[130:131]
	v_pk_fma_f32 v[92:93], v[92:93], v[118:119], v[132:133]
	v_cvt_pk_bf16_f32 v90, v90, v91
	s_nop 0
	v_cvt_pk_bf16_f32 v91, v92, v93
	global_store_dwordx2 v[108:109], v[90:91], off offset:512
	v_pk_mul_f32 v[90:91], v[122:123], v[164:165] op_sel_hi:[1,0]
	v_pk_mul_f32 v[92:93], v[124:125], v[164:165] op_sel_hi:[1,0]
	v_pk_fma_f32 v[90:91], v[90:91], v[116:117], v[130:131]
	v_pk_fma_f32 v[92:93], v[92:93], v[118:119], v[132:133]
	v_cvt_pk_bf16_f32 v90, v90, v91
	s_nop 0
	v_cvt_pk_bf16_f32 v91, v92, v93
	global_store_dwordx2 v[114:115], v[90:91], off offset:512
	global_load_dwordx4 v[90:93], v[144:145], off offset:2048
	s_nop 0
	global_load_dwordx4 v[94:97], v[172:173], off offset:2048
	global_load_dwordx4 v[102:105], v[170:171], off offset:2048
	s_waitcnt vmcnt(1)
	v_pk_add_f32 v[94:95], v[94:95], 1.0 op_sel_hi:[1,0]
	v_pk_add_f32 v[96:97], v[96:97], 1.0 op_sel_hi:[1,0]
	v_pk_mul_f32 v[90:91], v[90:91], v[94:95]
	v_pk_mul_f32 v[92:93], v[92:93], v[96:97]
	s_waitcnt vmcnt(0)
	v_pk_fma_f32 v[74:75], v[74:75], v[90:91], v[102:103]
	v_pk_fma_f32 v[76:77], v[76:77], v[92:93], v[104:105]
	v_cvt_pk_bf16_f32 v74, v74, v75
	s_nop 0
	v_cvt_pk_bf16_f32 v75, v76, v77
	global_store_dwordx2 v[166:167], v[74:75], off offset:1024
	v_pk_mul_f32 v[74:75], v[78:79], v[160:161] op_sel_hi:[1,0]
	v_pk_mul_f32 v[76:77], v[80:81], v[160:161] op_sel_hi:[1,0]
	v_pk_fma_f32 v[74:75], v[74:75], v[90:91], v[102:103]
	v_pk_fma_f32 v[76:77], v[76:77], v[92:93], v[104:105]
	v_cvt_pk_bf16_f32 v74, v74, v75
	s_nop 0
	v_cvt_pk_bf16_f32 v75, v76, v77
	global_store_dwordx2 v[106:107], v[74:75], off offset:1024
	v_pk_mul_f32 v[74:75], v[86:87], v[162:163] op_sel_hi:[1,0]
	v_pk_mul_f32 v[76:77], v[88:89], v[162:163] op_sel_hi:[1,0]
	v_pk_fma_f32 v[74:75], v[74:75], v[90:91], v[102:103]
	v_pk_fma_f32 v[76:77], v[76:77], v[92:93], v[104:105]
	v_cvt_pk_bf16_f32 v74, v74, v75
	s_nop 0
	v_cvt_pk_bf16_f32 v75, v76, v77
	global_store_dwordx2 v[108:109], v[74:75], off offset:1024
	v_pk_mul_f32 v[74:75], v[110:111], v[164:165] op_sel_hi:[1,0]
	v_pk_mul_f32 v[76:77], v[112:113], v[164:165] op_sel_hi:[1,0]
	v_pk_fma_f32 v[74:75], v[74:75], v[90:91], v[102:103]
	v_pk_fma_f32 v[76:77], v[76:77], v[92:93], v[104:105]
	v_cvt_pk_bf16_f32 v74, v74, v75
	s_nop 0
	v_cvt_pk_bf16_f32 v75, v76, v77
	global_store_dwordx2 v[114:115], v[74:75], off offset:1024
	global_load_dwordx4 v[74:77], v[144:145], off offset:3072
	s_nop 0
	global_load_dwordx4 v[78:81], v[172:173], off offset:3072
	global_load_dwordx4 v[86:89], v[170:171], off offset:3072
	s_waitcnt vmcnt(1)
; __device__ __forceinline__ unsigned pk2(float lo, float hi) { unsigned r; asm("v_cvt_pk_bf16_f32 %0, %1, %2" : "=v"(r) : "v"(lo), "v"(hi)); return r; }
; __device__ __forceinline__ void ph_norm1_l0(const Params& p) {
;     ...
; #pragma unroll
;         for (int j = 0; j < 8; ++j) {
;             const f32x4 g = *(const f32x4*)(g1 + 4 * lane + 256 * j), s1 = *(const f32x4*)(sc + 4 * lane + 256 * j), s0 = *(const f32x4*)(sh + 4 * lane + 256 * j);
;             const f32x4 gg = g * (s1 + 1.f);
; #pragma unroll
;             for (int q = 0; q < 4; ++q) {
;                 const f32x4 hq = (v[q][j] * rq[q]) * gg + s0;
;                 u32x2 w; w.x = pk2(hq[0], hq[1]); w.y = pk2(hq[2], hq[3]);
;                 *(u32x2*)(ho + (size_t)q * DM + 4 * lane + 256 * j) = w;
;             }
;         }
	v_pk_add_f32 v[78:79], v[78:79], 1.0 op_sel_hi:[1,0]
	v_pk_add_f32 v[80:81], v[80:81], 1.0 op_sel_hi:[1,0]
	v_pk_mul_f32 v[74:75], v[74:75], v[78:79]
	v_pk_mul_f32 v[76:77], v[76:77], v[80:81]
	s_waitcnt vmcnt(0)
	v_pk_fma_f32 v[58:59], v[58:59], v[74:75], v[86:87]
	v_pk_fma_f32 v[60:61], v[60:61], v[76:77], v[88:89]
	v_cvt_pk_bf16_f32 v58, v58, v59
	s_nop 0
	v_cvt_pk_bf16_f32 v59, v60, v61
	global_store_dwordx2 v[166:167], v[58:59], off offset:1536
	v_pk_mul_f32 v[58:59], v[62:63], v[160:161] op_sel_hi:[1,0]
	v_pk_mul_f32 v[60:61], v[64:65], v[160:161] op_sel_hi:[1,0]
	v_pk_fma_f32 v[58:59], v[58:59], v[74:75], v[86:87]
	v_pk_fma_f32 v[60:61], v[60:61], v[76:77], v[88:89]
	v_cvt_pk_bf16_f32 v58, v58, v59
	s_nop 0
	v_cvt_pk_bf16_f32 v59, v60, v61
	global_store_dwordx2 v[106:107], v[58:59], off offset:1536
	v_pk_mul_f32 v[58:59], v[70:71], v[162:163] op_sel_hi:[1,0]
	v_pk_mul_f32 v[60:61], v[72:73], v[162:163] op_sel_hi:[1,0]
	v_pk_fma_f32 v[58:59], v[58:59], v[74:75], v[86:87]
	v_pk_fma_f32 v[60:61], v[60:61], v[76:77], v[88:89]
	v_cvt_pk_bf16_f32 v58, v58, v59
	s_nop 0
	v_cvt_pk_bf16_f32 v59, v60, v61
	global_store_dwordx2 v[108:109], v[58:59], off offset:1536
	v_pk_mul_f32 v[58:59], v[98:99], v[164:165] op_sel_hi:[1,0]
	v_pk_mul_f32 v[60:61], v[100:101], v[164:165] op_sel_hi:[1,0]
	v_pk_fma_f32 v[58:59], v[58:59], v[74:75], v[86:87]
	v_pk_fma_f32 v[60:61], v[60:61], v[76:77], v[88:89]
	v_cvt_pk_bf16_f32 v58, v58, v59
	s_nop 0
	v_cvt_pk_bf16_f32 v59, v60, v61
	global_store_dwordx2 v[114:115], v[58:59], off offset:1536
	global_load_dwordx4 v[60:63], v[146:147], off
	global_load_dwordx4 v[70:73], v[168:169], off
	v_add_co_u32_e32 v58, vcc, s10, v170
	s_waitcnt vmcnt(0)
	v_pk_add_f32 v[70:71], v[70:71], 1.0 op_sel_hi:[1,0]
	v_addc_co_u32_e32 v59, vcc, 0, v171, vcc
	global_load_dwordx4 v[74:77], v[58:59], off
	v_pk_add_f32 v[64:65], v[72:73], 1.0 op_sel_hi:[1,0]
	v_pk_mul_f32 v[60:61], v[60:61], v[70:71]
	v_pk_mul_f32 v[62:63], v[62:63], v[64:65]
	v_cmp_lt_i32_e32 vcc, s12, v142
	s_or_b64 s[38:39], vcc, s[38:39]
	s_waitcnt vmcnt(0)
	v_pk_fma_f32 v[46:47], v[46:47], v[60:61], v[74:75]
	v_pk_fma_f32 v[48:49], v[48:49], v[62:63], v[76:77]
	v_cvt_pk_bf16_f32 v46, v46, v47
	v_pk_fma_f32 v[50:51], v[50:51], v[60:61], v[74:75]
	v_cvt_pk_bf16_f32 v47, v48, v49
	global_store_dwordx2 v[106:107], v[46:47], off offset:2048
	v_pk_mul_f32 v[46:47], v[54:55], v[162:163] op_sel_hi:[1,0]
	v_pk_mul_f32 v[48:49], v[56:57], v[162:163] op_sel_hi:[1,0]
	v_pk_fma_f32 v[46:47], v[46:47], v[60:61], v[74:75]
	v_pk_fma_f32 v[48:49], v[48:49], v[62:63], v[76:77]
	v_cvt_pk_bf16_f32 v46, v46, v47
	v_pk_fma_f32 v[52:53], v[52:53], v[62:63], v[76:77]
	v_cvt_pk_bf16_f32 v47, v48, v49
	global_store_dwordx2 v[108:109], v[46:47], off offset:2048
	v_pk_mul_f32 v[46:47], v[82:83], v[164:165] op_sel_hi:[1,0]
	v_pk_mul_f32 v[48:49], v[84:85], v[164:165] op_sel_hi:[1,0]
	v_pk_fma_f32 v[46:47], v[46:47], v[60:61], v[74:75]
	v_cvt_pk_bf16_f32 v50, v50, v51
	v_cvt_pk_bf16_f32 v51, v52, v53
	global_store_dwordx2 v[166:167], v[50:51], off offset:2048
	v_pk_fma_f32 v[48:49], v[48:49], v[62:63], v[76:77]
	v_cvt_pk_bf16_f32 v46, v46, v47
	s_nop 0
	v_cvt_pk_bf16_f32 v47, v48, v49
	global_store_dwordx2 v[114:115], v[46:47], off offset:2048
	global_load_dwordx4 v[46:49], v[148:149], off
	s_nop 0
	global_load_dwordx4 v[50:53], v[168:169], off offset:1024
	global_load_dwordx4 v[54:57], v[58:59], off offset:1024
	s_waitcnt vmcnt(1)
	v_pk_add_f32 v[50:51], v[50:51], 1.0 op_sel_hi:[1,0]
	v_pk_add_f32 v[52:53], v[52:53], 1.0 op_sel_hi:[1,0]
	v_pk_mul_f32 v[46:47], v[46:47], v[50:51]
	v_pk_mul_f32 v[48:49], v[48:49], v[52:53]
	s_waitcnt vmcnt(0)
; __device__ __forceinline__ unsigned pk2(float lo, float hi) { unsigned r; asm("v_cvt_pk_bf16_f32 %0, %1, %2" : "=v"(r) : "v"(lo), "v"(hi)); return r; }
; __device__ __forceinline__ void ph_norm1_l0(const Params& p) {
;     ...
; #pragma unroll
;         for (int j = 0; j < 8; ++j) {
;             const f32x4 g = *(const f32x4*)(g1 + 4 * lane + 256 * j), s1 = *(const f32x4*)(sc + 4 * lane + 256 * j), s0 = *(const f32x4*)(sh + 4 * lane + 256 * j);
;             const f32x4 gg = g * (s1 + 1.f);
; #pragma unroll
;             for (int q = 0; q < 4; ++q) {
;                 const f32x4 hq = (v[q][j] * rq[q]) * gg + s0;
;                 u32x2 w; w.x = pk2(hq[0], hq[1]); w.y = pk2(hq[2], hq[3]);
;                 *(u32x2*)(ho + (size_t)q * DM + 4 * lane + 256 * j) = w;
;             }
;         }
	v_pk_fma_f32 v[34:35], v[34:35], v[46:47], v[54:55]
	v_pk_fma_f32 v[36:37], v[36:37], v[48:49], v[56:57]
	v_cvt_pk_bf16_f32 v34, v34, v35
	v_pk_fma_f32 v[38:39], v[38:39], v[46:47], v[54:55]
	v_cvt_pk_bf16_f32 v35, v36, v37
	global_store_dwordx2 v[106:107], v[34:35], off offset:2560
	v_pk_mul_f32 v[34:35], v[42:43], v[162:163] op_sel_hi:[1,0]
	v_pk_mul_f32 v[36:37], v[44:45], v[162:163] op_sel_hi:[1,0]
	v_pk_fma_f32 v[34:35], v[34:35], v[46:47], v[54:55]
	v_pk_fma_f32 v[36:37], v[36:37], v[48:49], v[56:57]
	v_cvt_pk_bf16_f32 v34, v34, v35
	v_pk_fma_f32 v[40:41], v[40:41], v[48:49], v[56:57]
	v_cvt_pk_bf16_f32 v35, v36, v37
	global_store_dwordx2 v[108:109], v[34:35], off offset:2560
	v_pk_mul_f32 v[34:35], v[66:67], v[164:165] op_sel_hi:[1,0]
	v_pk_mul_f32 v[36:37], v[68:69], v[164:165] op_sel_hi:[1,0]
	v_pk_fma_f32 v[34:35], v[34:35], v[46:47], v[54:55]
	v_cvt_pk_bf16_f32 v38, v38, v39
	v_cvt_pk_bf16_f32 v39, v40, v41
	global_store_dwordx2 v[166:167], v[38:39], off offset:2560
	v_pk_fma_f32 v[36:37], v[36:37], v[48:49], v[56:57]
	v_cvt_pk_bf16_f32 v34, v34, v35
	s_nop 0
	v_cvt_pk_bf16_f32 v35, v36, v37
	global_store_dwordx2 v[114:115], v[34:35], off offset:2560
	global_load_dwordx4 v[34:37], v[150:151], off
	s_nop 0
	global_load_dwordx4 v[38:41], v[168:169], off offset:2048
	global_load_dwordx4 v[42:45], v[58:59], off offset:2048
	s_waitcnt vmcnt(1)
	v_pk_add_f32 v[38:39], v[38:39], 1.0 op_sel_hi:[1,0]
	v_pk_add_f32 v[40:41], v[40:41], 1.0 op_sel_hi:[1,0]
	v_pk_mul_f32 v[34:35], v[34:35], v[38:39]
	v_pk_mul_f32 v[36:37], v[36:37], v[40:41]
	s_waitcnt vmcnt(0)
	v_pk_fma_f32 v[14:15], v[14:15], v[34:35], v[42:43]
	v_pk_fma_f32 v[16:17], v[16:17], v[36:37], v[44:45]
	v_cvt_pk_bf16_f32 v14, v14, v15
	v_pk_fma_f32 v[18:19], v[18:19], v[34:35], v[42:43]
	v_cvt_pk_bf16_f32 v15, v16, v17
	global_store_dwordx2 v[106:107], v[14:15], off offset:3072
	v_pk_mul_f32 v[14:15], v[22:23], v[162:163] op_sel_hi:[1,0]
	v_pk_mul_f32 v[16:17], v[24:25], v[162:163] op_sel_hi:[1,0]
	v_pk_fma_f32 v[14:15], v[14:15], v[34:35], v[42:43]
	v_pk_fma_f32 v[16:17], v[16:17], v[36:37], v[44:45]
	v_cvt_pk_bf16_f32 v14, v14, v15
	v_pk_fma_f32 v[20:21], v[20:21], v[36:37], v[44:45]
	v_cvt_pk_bf16_f32 v15, v16, v17
	global_store_dwordx2 v[108:109], v[14:15], off offset:3072
	v_pk_mul_f32 v[14:15], v[30:31], v[164:165] op_sel_hi:[1,0]
	v_pk_mul_f32 v[16:17], v[32:33], v[164:165] op_sel_hi:[1,0]
	v_pk_fma_f32 v[14:15], v[14:15], v[34:35], v[42:43]
	v_cvt_pk_bf16_f32 v18, v18, v19
	v_cvt_pk_bf16_f32 v19, v20, v21
	global_store_dwordx2 v[166:167], v[18:19], off offset:3072
	v_pk_fma_f32 v[16:17], v[16:17], v[36:37], v[44:45]
	v_cvt_pk_bf16_f32 v14, v14, v15
	s_nop 0
	v_cvt_pk_bf16_f32 v15, v16, v17
	global_store_dwordx2 v[114:115], v[14:15], off offset:3072
	global_load_dwordx4 v[14:17], v[152:153], off
	s_nop 0
	global_load_dwordx4 v[18:21], v[168:169], off offset:3072
	global_load_dwordx4 v[22:25], v[58:59], off offset:3072
	s_waitcnt vmcnt(1)
	v_pk_add_f32 v[18:19], v[18:19], 1.0 op_sel_hi:[1,0]
	v_pk_add_f32 v[20:21], v[20:21], 1.0 op_sel_hi:[1,0]
	v_pk_mul_f32 v[14:15], v[14:15], v[18:19]
	v_pk_mul_f32 v[16:17], v[16:17], v[20:21]
	s_waitcnt vmcnt(0)
	v_pk_fma_f32 v[2:3], v[2:3], v[14:15], v[22:23]
	v_pk_fma_f32 v[4:5], v[4:5], v[16:17], v[24:25]
	v_cvt_pk_bf16_f32 v2, v2, v3
	s_nop 0
	v_cvt_pk_bf16_f32 v3, v4, v5
	global_store_dwordx2 v[166:167], v[2:3], off offset:3584
	v_pk_mul_f32 v[2:3], v[6:7], v[160:161] op_sel_hi:[1,0]
	v_pk_mul_f32 v[4:5], v[8:9], v[160:161] op_sel_hi:[1,0]
	v_pk_fma_f32 v[2:3], v[2:3], v[14:15], v[22:23]
	v_pk_fma_f32 v[4:5], v[4:5], v[16:17], v[24:25]
	v_cvt_pk_bf16_f32 v2, v2, v3
	s_nop 0
	v_cvt_pk_bf16_f32 v3, v4, v5
	global_store_dwordx2 v[106:107], v[2:3], off offset:3584
	v_pk_mul_f32 v[2:3], v[10:11], v[162:163] op_sel_hi:[1,0]
	v_pk_mul_f32 v[4:5], v[12:13], v[162:163] op_sel_hi:[1,0]
	v_pk_fma_f32 v[2:3], v[2:3], v[14:15], v[22:23]
	v_pk_fma_f32 v[4:5], v[4:5], v[16:17], v[24:25]
	v_cvt_pk_bf16_f32 v2, v2, v3
	s_nop 0
	v_cvt_pk_bf16_f32 v3, v4, v5
	global_store_dwordx2 v[108:109], v[2:3], off offset:3584
	v_pk_mul_f32 v[2:3], v[26:27], v[164:165] op_sel_hi:[1,0]
	v_pk_mul_f32 v[4:5], v[28:29], v[164:165] op_sel_hi:[1,0]
	v_pk_fma_f32 v[2:3], v[2:3], v[14:15], v[22:23]
	v_pk_fma_f32 v[4:5], v[4:5], v[16:17], v[24:25]
	v_cvt_pk_bf16_f32 v2, v2, v3
	s_nop 0
	v_cvt_pk_bf16_f32 v3, v4, v5
	global_store_dwordx2 v[114:115], v[2:3], off offset:3584
	s_andn2_b64 exec, exec, s[38:39]
	s_cbranch_execnz .LBB0_363

;     __device__ __forceinline__ void fused(AccT& acc, const GUnit& u, int wr, int wc, int fr, int fq, LAS unsigned char* lds, int wid, int lane) const {
;     ...
; #pragma unroll
;         for (int bj = 0; bj < 2; ++bj)
; #pragma unroll
;             for (int n = 0; n < 2; ++n) { const int c = col0 + bj * 128 + n * 4; G[bj][n] = *(const f32x4*)(g2 + c) * (*(const f32x4*)(shf + (size_t)b * 12288 + 2048 + c) + 1.f); }
;     ...
;             for (int ai = 0; ai < 2; ++ai)
; #pragma unroll
;                 for (int m = 0; m < 4; ++m) {
;                     const int rowl = ai * 128 + wr * 64 + m * 16;
;                     float sq = 0.f; f32x4 lg = (f32x4){0.f, 0.f, 0.f, 0.f};
; #pragma unroll
;                     for (int bj = 0; bj < 2; ++bj) {
;                         const f32x4 x0 = acc[ai][bj][m][0], x1 = acc[ai][bj][m][1];
;                         sq += (x0[0] * x0[0] + x0[1] * x0[1]) + (x0[2] * x0[2] + x0[3] * x0[3]) + (x1[0] * x1[0] + x1[1] * x1[1]) + (x1[2] * x1[2] + x1[3] * x1[3]);
;                         const f32x4 h0 = x0 * G[bj][0], h1 = x1 * G[bj][1];
;                         lg = __builtin_amdgcn_mfma_f32_16x16x32_bf16(pack8(h0[0], h0[1], h0[2], h0[3], h1[0], h1[1], h1[2], h1[3]), wf[bj], lg, 0, 0, 0);
;                     }
;                     sq += __shfl_xor(sq, 16); sq += __shfl_xor(sq, 32);
;                     if (fq == 0) P[(rowl + fr) * 4 + wc] = sq;
; #pragma unroll
;                     for (int i = 0; i < 4; ++i) LP[((size_t)wc * 256 + rowl + 4 * fq + i) * 16 + fr] = lg[i];
.LBB0_1260:
	s_waitcnt vmcnt(0)
	v_pk_fma_f32 v[24:25], v[16:17], v[100:101], v[24:25]
	v_pk_fma_f32 v[22:23], v[14:15], v[98:99], v[22:23]
	v_pk_fma_f32 v[18:19], v[10:11], v[78:79], v[18:19]
	v_cvt_pk_bf16_f32 v10, v22, v23
	v_cvt_pk_bf16_f32 v11, v24, v25
	v_pk_fma_f32 v[20:21], v[12:13], v[80:81], v[20:21]
	v_cvt_pk_bf16_f32 v12, v18, v19
	v_pk_add_f32 v[120:121], v[120:121], 1.0 op_sel_hi:[1,0]
	v_cvt_pk_bf16_f32 v13, v20, v21
	global_store_dwordx4 v[130:131], v[10:13], off offset:256
	v_pk_add_f32 v[118:119], v[118:119], 1.0 op_sel_hi:[1,0]
	v_pk_mul_f32 v[116:117], v[116:117], v[120:121]
	v_mul_f32_e32 v10, v191, v191
	v_mul_f32_e32 v11, v193, v193
	v_fmac_f32_e32 v10, v190, v190
	v_fmac_f32_e32 v11, v192, v192
	v_add_f32_e32 v10, v10, v11
	v_mul_f32_e32 v11, v187, v187
	v_fmac_f32_e32 v11, v186, v186
	v_pk_mul_f32 v[114:115], v[114:115], v[118:119]
	v_pk_add_f32 v[118:119], v[106:107], 1.0 op_sel_hi:[1,0]
	v_pk_add_f32 v[106:107], v[108:109], 1.0 op_sel_hi:[1,0]
	v_add_f32_e32 v10, v11, v10
	v_mul_f32_e32 v11, v189, v189
	v_pk_mul_f32 v[106:107], v[96:97], v[106:107]
	v_pk_mul_f32 v[108:109], v[94:95], v[118:119]
	v_pk_add_f32 v[90:91], v[90:91], 1.0 op_sel_hi:[1,0]
	v_fmac_f32_e32 v11, v188, v188
	v_pk_mul_f32 v[14:15], v[116:117], v[192:193]
	v_pk_mul_f32 v[82:83], v[82:83], v[90:91]
	v_add_f32_e32 v90, v11, v10
	v_pk_mul_f32 v[16:17], v[114:115], v[190:191]
	v_pk_mul_f32 v[78:79], v[106:107], v[188:189]
	v_pk_mul_f32 v[80:81], v[108:109], v[186:187]
	v_cmp_lt_i32_e64 s[34:35], v216, v213
	v_cvt_pk_bf16_f32 v10, v16, v17
	v_cvt_pk_bf16_f32 v11, v14, v15
	v_cvt_pk_bf16_f32 v12, v80, v81
	v_cvt_pk_bf16_f32 v13, v78, v79
	s_nop 1
	v_mul_f32_e32 v14, v183, v183
	v_mul_f32_e32 v15, v185, v185
	v_fmac_f32_e32 v14, v182, v182
	v_fmac_f32_e32 v15, v184, v184
	v_add_f32_e32 v14, v14, v15
	v_mul_f32_e32 v15, v179, v179
	v_fmac_f32_e32 v15, v178, v178
	v_add_f32_e32 v14, v15, v14
	v_mul_f32_e32 v15, v181, v181
	v_fmac_f32_e32 v15, v180, v180
	v_add_f32_e32 v14, v15, v14
	v_add_f32_e32 v15, v90, v14
	v_cndmask_b32_e64 v14, v212, v216, s[34:35]
	v_pk_add_f32 v[94:95], v[112:113], 1.0 op_sel_hi:[1,0]
	v_lshlrev_b32_e32 v14, 2, v14
	v_pk_add_f32 v[96:97], v[110:111], 1.0 op_sel_hi:[1,0]
	v_pk_mul_f32 v[94:95], v[104:105], v[94:95]
	v_pk_add_f32 v[92:93], v[92:93], 1.0 op_sel_hi:[1,0]
	v_mov_b32_e32 v100, v15
	s_nop 1
	v_permlane16_swap_b32_e32 v15, v100
	v_pk_mul_f32 v[96:97], v[102:103], v[96:97]
	v_pk_mul_f32 v[84:85], v[84:85], v[92:93]
	v_pk_mul_f32 v[16:17], v[94:95], v[184:185]
	v_pk_mul_f32 v[90:91], v[96:97], v[182:183]
	v_pk_mul_f32 v[92:93], v[84:85], v[180:181]
	v_pk_mul_f32 v[98:99], v[82:83], v[178:179]
	v_mfma_f32_16x16x32_bf16 v[10:13], v[10:13], v[6:9], 0
	v_cvt_pk_bf16_f32 v78, v90, v91
	v_cvt_pk_bf16_f32 v79, v16, v17
	v_cvt_pk_bf16_f32 v80, v98, v99
	v_cvt_pk_bf16_f32 v81, v92, v93
	s_nop 1
	v_xor_b32_e32 v16, 32, v212
	v_cmp_lt_i32_e64 s[34:35], v16, v213
	s_waitcnt lgkmcnt(0)
	v_add_f32_e32 v15, v15, v100
	v_mfma_f32_16x16x32_bf16 v[10:13], v[78:81], v[2:5], v[10:13]
	v_cndmask_b32_e64 v16, v212, v16, s[34:35]
	v_lshlrev_b32_e32 v17, 2, v16
	ds_bpermute_b32 v16, v17, v15
	v_and_b32_e32 v132, 63, v207
	s_lshl_b32 s10, s59, 2
	s_add_i32 s10, s10, 0
	v_cmp_gt_u32_e32 vcc, 16, v132
	s_and_saveexec_b64 s[12:13], vcc
	s_cbranch_execz .LBB0_1262
	v_lshl_add_u32 v78, v1, 4, s10
	s_waitcnt lgkmcnt(0)
	v_add_f32_e32 v15, v15, v16
	ds_write_b32 v78, v15
.LBB0_1262:
	s_or_b64 exec, exec, s[12:13]
	v_lshlrev_b32_e32 v15, 2, v208
	v_lshl_or_b32 v15, s59, 8, v15
	s_waitcnt lgkmcnt(0)
	v_lshl_add_u32 v16, v206, 2, 0
	v_add_u32_e32 v78, s23, v15
	v_lshl_add_u32 v78, v78, 6, v16
	v_add_u32_e32 v78, 0x2000, v78
	ds_write2_b32 v78, v10, v11 offset1:16
	ds_write2_b32 v78, v12, v13 offset0:32 offset1:48
	v_mul_f32_e32 v10, v175, v175
	v_mul_f32_e32 v11, v177, v177
	v_fmac_f32_e32 v10, v174, v174
	v_fmac_f32_e32 v11, v176, v176
	v_add_f32_e32 v10, v10, v11
	v_mul_f32_e32 v11, v171, v171
	v_fmac_f32_e32 v11, v170, v170
	v_add_f32_e32 v10, v11, v10
	v_mul_f32_e32 v11, v173, v173
	v_fmac_f32_e32 v11, v172, v172
	v_pk_mul_f32 v[78:79], v[116:117], v[176:177]
	v_add_f32_e32 v98, v11, v10
	v_pk_mul_f32 v[80:81], v[114:115], v[174:175]
	v_pk_mul_f32 v[90:91], v[106:107], v[172:173]
	v_pk_mul_f32 v[92:93], v[108:109], v[170:171]
	v_pk_mul_f32 v[100:101], v[82:83], v[162:163]
	v_cvt_pk_bf16_f32 v10, v80, v81
	v_cvt_pk_bf16_f32 v11, v78, v79
	v_cvt_pk_bf16_f32 v12, v92, v93
	v_cvt_pk_bf16_f32 v13, v90, v91
	s_nop 1
	v_mul_f32_e32 v78, v167, v167
	v_mul_f32_e32 v79, v169, v169
	v_fmac_f32_e32 v78, v166, v166
	v_fmac_f32_e32 v79, v168, v168
	v_add_f32_e32 v78, v78, v79
	v_mul_f32_e32 v79, v163, v163
	v_fmac_f32_e32 v79, v162, v162
	v_mfma_f32_16x16x32_bf16 v[10:13], v[10:13], v[6:9], 0
	v_add_f32_e32 v78, v79, v78
	v_mul_f32_e32 v79, v165, v165
	v_fmac_f32_e32 v79, v164, v164
	v_add_f32_e32 v78, v79, v78
	v_add_f32_e32 v102, v98, v78
	v_pk_mul_f32 v[90:91], v[94:95], v[168:169]
	v_pk_mul_f32 v[92:93], v[96:97], v[166:167]
	v_pk_mul_f32 v[98:99], v[84:85], v[164:165]
	s_or_b32 s11, s23, 16
	v_cvt_pk_bf16_f32 v78, v92, v93
	v_cvt_pk_bf16_f32 v79, v90, v91
	v_cvt_pk_bf16_f32 v80, v100, v101
	v_cvt_pk_bf16_f32 v81, v98, v99
	s_nop 1
	s_nop 0
	v_mfma_f32_16x16x32_bf16 v[10:13], v[78:81], v[2:5], v[10:13]
	v_mov_b32_e32 v78, v102
	s_nop 1
	v_permlane16_swap_b32_e32 v102, v78
	s_waitcnt lgkmcnt(0)
	v_add_f32_e32 v78, v102, v78
	ds_bpermute_b32 v79, v17, v78
	s_and_saveexec_b64 s[12:13], vcc
	s_cbranch_execz .LBB0_1264
	v_or_b32_e32 v80, s11, v206
	v_lshl_add_u32 v80, v80, 4, s10
	s_waitcnt lgkmcnt(0)
	v_add_f32_e32 v78, v78, v79
	ds_write_b32 v80, v78
;     __device__ __forceinline__ void fused(AccT& acc, const GUnit& u, int wr, int wc, int fr, int fq, LAS unsigned char* lds, int wid, int lane) const {
;     ...
;             for (int ai = 0; ai < 2; ++ai)
; #pragma unroll
;                 for (int m = 0; m < 4; ++m) {
;                     const int rowl = ai * 128 + wr * 64 + m * 16;
;                     float sq = 0.f; f32x4 lg = (f32x4){0.f, 0.f, 0.f, 0.f};
; #pragma unroll
;                     for (int bj = 0; bj < 2; ++bj) {
;                         const f32x4 x0 = acc[ai][bj][m][0], x1 = acc[ai][bj][m][1];
;                         sq += (x0[0] * x0[0] + x0[1] * x0[1]) + (x0[2] * x0[2] + x0[3] * x0[3]) + (x1[0] * x1[0] + x1[1] * x1[1]) + (x1[2] * x1[2] + x1[3] * x1[3]);
;                         const f32x4 h0 = x0 * G[bj][0], h1 = x1 * G[bj][1];
;                         lg = __builtin_amdgcn_mfma_f32_16x16x32_bf16(pack8(h0[0], h0[1], h0[2], h0[3], h1[0], h1[1], h1[2], h1[3]), wf[bj], lg, 0, 0, 0);
;                     }
;                     sq += __shfl_xor(sq, 16); sq += __shfl_xor(sq, 32);
;                     if (fq == 0) P[(rowl + fr) * 4 + wc] = sq;
; #pragma unroll
;                     for (int i = 0; i < 4; ++i) LP[((size_t)wc * 256 + rowl + 4 * fq + i) * 16 + fr] = lg[i];
.LBB0_1264:
	s_or_b64 exec, exec, s[12:13]
	v_add_u32_e32 v78, s11, v15
	v_lshl_add_u32 v78, v78, 6, v16
	v_add_u32_e32 v78, 0x2000, v78
	ds_write2_b32 v78, v10, v11 offset1:16
	ds_write2_b32 v78, v12, v13 offset0:32 offset1:48
	v_mul_f32_e32 v10, v159, v159
	v_mul_f32_e32 v11, v161, v161
	v_fmac_f32_e32 v10, v158, v158
	v_fmac_f32_e32 v11, v160, v160
	v_add_f32_e32 v10, v10, v11
	v_mul_f32_e32 v11, v155, v155
	v_fmac_f32_e32 v11, v154, v154
	v_add_f32_e32 v10, v11, v10
	v_mul_f32_e32 v11, v157, v157
	v_fmac_f32_e32 v11, v156, v156
	s_waitcnt lgkmcnt(2)
	v_pk_mul_f32 v[78:79], v[116:117], v[160:161]
	v_add_f32_e32 v98, v11, v10
	v_pk_mul_f32 v[80:81], v[114:115], v[158:159]
	v_pk_mul_f32 v[90:91], v[106:107], v[156:157]
	v_pk_mul_f32 v[92:93], v[108:109], v[154:155]
	v_pk_mul_f32 v[100:101], v[82:83], v[146:147]
	v_cvt_pk_bf16_f32 v10, v80, v81
	v_cvt_pk_bf16_f32 v11, v78, v79
	v_cvt_pk_bf16_f32 v12, v92, v93
	v_cvt_pk_bf16_f32 v13, v90, v91
	s_nop 1
	v_mul_f32_e32 v78, v151, v151
	v_mul_f32_e32 v79, v153, v153
	v_fmac_f32_e32 v78, v150, v150
	v_fmac_f32_e32 v79, v152, v152
	v_add_f32_e32 v78, v78, v79
	v_mul_f32_e32 v79, v147, v147
	v_fmac_f32_e32 v79, v146, v146
	v_mfma_f32_16x16x32_bf16 v[10:13], v[10:13], v[6:9], 0
	v_add_f32_e32 v78, v79, v78
	v_mul_f32_e32 v79, v149, v149
	v_fmac_f32_e32 v79, v148, v148
	v_add_f32_e32 v78, v79, v78
	v_add_f32_e32 v102, v98, v78
	v_pk_mul_f32 v[90:91], v[94:95], v[152:153]
	v_pk_mul_f32 v[92:93], v[96:97], v[150:151]
	v_pk_mul_f32 v[98:99], v[84:85], v[148:149]
	s_or_b32 s11, s23, 32
	v_cvt_pk_bf16_f32 v78, v92, v93
	v_cvt_pk_bf16_f32 v79, v90, v91
	v_cvt_pk_bf16_f32 v80, v100, v101
	v_cvt_pk_bf16_f32 v81, v98, v99
	s_nop 1
	s_nop 0
	v_mfma_f32_16x16x32_bf16 v[10:13], v[78:81], v[2:5], v[10:13]
	v_mov_b32_e32 v78, v102
	s_nop 1
	v_permlane16_swap_b32_e32 v102, v78
	s_waitcnt lgkmcnt(0)
	v_add_f32_e32 v78, v102, v78
	ds_bpermute_b32 v79, v17, v78
	s_and_saveexec_b64 s[12:13], vcc
	s_cbranch_execz .LBB0_1266
	v_or_b32_e32 v80, s11, v206
	v_lshl_add_u32 v80, v80, 4, s10
	s_waitcnt lgkmcnt(0)
	v_add_f32_e32 v78, v78, v79
	ds_write_b32 v80, v78
.LBB0_1266:
	s_or_b64 exec, exec, s[12:13]
	v_add_u32_e32 v78, s11, v15
	v_lshl_add_u32 v78, v78, 6, v16
	v_add_u32_e32 v78, 0x2000, v78
	ds_write2_b32 v78, v10, v11 offset1:16
	ds_write2_b32 v78, v12, v13 offset0:32 offset1:48
	v_mul_f32_e32 v10, v143, v143
	v_mul_f32_e32 v11, v145, v145
	v_fmac_f32_e32 v10, v142, v142
	v_fmac_f32_e32 v11, v144, v144
	v_add_f32_e32 v10, v10, v11
	v_mul_f32_e32 v11, v139, v139
	v_fmac_f32_e32 v11, v138, v138
	v_add_f32_e32 v10, v11, v10
	v_mul_f32_e32 v11, v141, v141
	v_fmac_f32_e32 v11, v140, v140
	s_waitcnt lgkmcnt(2)
	v_pk_mul_f32 v[78:79], v[116:117], v[144:145]
	v_add_f32_e32 v98, v11, v10
	v_pk_mul_f32 v[80:81], v[114:115], v[142:143]
	v_pk_mul_f32 v[90:91], v[106:107], v[140:141]
	v_pk_mul_f32 v[92:93], v[108:109], v[138:139]
	v_pk_mul_f32 v[100:101], v[82:83], v[122:123]
	v_cvt_pk_bf16_f32 v10, v80, v81
	v_cvt_pk_bf16_f32 v11, v78, v79
	v_cvt_pk_bf16_f32 v12, v92, v93
	v_cvt_pk_bf16_f32 v13, v90, v91
	s_nop 1
	v_mul_f32_e32 v78, v127, v127
	v_mul_f32_e32 v79, v129, v129
	v_fmac_f32_e32 v78, v126, v126
	v_fmac_f32_e32 v79, v128, v128
	v_add_f32_e32 v78, v78, v79
	v_mul_f32_e32 v79, v123, v123
	v_fmac_f32_e32 v79, v122, v122
	v_mfma_f32_16x16x32_bf16 v[10:13], v[10:13], v[6:9], 0
	v_add_f32_e32 v78, v79, v78
	v_mul_f32_e32 v79, v125, v125
	v_fmac_f32_e32 v79, v124, v124
	v_add_f32_e32 v78, v79, v78
	v_add_f32_e32 v102, v98, v78
	v_pk_mul_f32 v[90:91], v[94:95], v[128:129]
	v_pk_mul_f32 v[92:93], v[96:97], v[126:127]
	v_pk_mul_f32 v[98:99], v[84:85], v[124:125]
	s_or_b32 s11, s23, 48
	v_cvt_pk_bf16_f32 v78, v92, v93
	v_cvt_pk_bf16_f32 v79, v90, v91
	v_cvt_pk_bf16_f32 v80, v100, v101
	v_cvt_pk_bf16_f32 v81, v98, v99
	s_nop 1
	s_nop 0
	v_mfma_f32_16x16x32_bf16 v[10:13], v[78:81], v[2:5], v[10:13]
	v_mov_b32_e32 v78, v102
	s_nop 1
	v_permlane16_swap_b32_e32 v102, v78
	s_waitcnt lgkmcnt(0)
	v_add_f32_e32 v78, v102, v78
	ds_bpermute_b32 v79, v17, v78
	s_and_saveexec_b64 s[12:13], vcc
	s_cbranch_execz .LBB0_1268
	v_or_b32_e32 v80, s11, v206
	v_lshl_add_u32 v80, v80, 4, s10
	s_waitcnt lgkmcnt(0)
	v_add_f32_e32 v78, v78, v79
	ds_write_b32 v80, v78
.LBB0_1268:
	s_or_b64 exec, exec, s[12:13]
	v_add_u32_e32 v78, s11, v15
	v_lshl_add_u32 v78, v78, 6, v16
	v_add_u32_e32 v78, 0x2000, v78
	ds_write2_b32 v78, v10, v11 offset1:16
	ds_write2_b32 v78, v12, v13 offset0:32 offset1:48
	v_mul_f32_e32 v10, v87, v87
	v_mul_f32_e32 v11, v89, v89
	v_fmac_f32_e32 v10, v86, v86
	v_fmac_f32_e32 v11, v88, v88
	v_add_f32_e32 v10, v10, v11
	v_mul_f32_e32 v11, v75, v75
	v_fmac_f32_e32 v11, v74, v74
	v_add_f32_e32 v10, v11, v10
	v_mul_f32_e32 v11, v77, v77
	v_fmac_f32_e32 v11, v76, v76
	s_waitcnt lgkmcnt(2)
	v_pk_mul_f32 v[78:79], v[116:117], v[88:89]
	v_add_f32_e32 v98, v11, v10
	v_pk_mul_f32 v[80:81], v[114:115], v[86:87]
	v_pk_mul_f32 v[90:91], v[106:107], v[76:77]
	v_pk_mul_f32 v[92:93], v[108:109], v[74:75]
	v_pk_mul_f32 v[100:101], v[82:83], v[66:67]
	v_cvt_pk_bf16_f32 v10, v80, v81
	v_cvt_pk_bf16_f32 v11, v78, v79
	v_cvt_pk_bf16_f32 v12, v92, v93
	v_cvt_pk_bf16_f32 v13, v90, v91
	s_nop 1
	v_mul_f32_e32 v78, v71, v71
	v_mul_f32_e32 v79, v73, v73
	v_fmac_f32_e32 v78, v70, v70
	v_fmac_f32_e32 v79, v72, v72
	v_add_f32_e32 v78, v78, v79
	v_mul_f32_e32 v79, v67, v67
	v_fmac_f32_e32 v79, v66, v66
	v_mfma_f32_16x16x32_bf16 v[10:13], v[10:13], v[6:9], 0
	v_add_f32_e32 v78, v79, v78
	v_mul_f32_e32 v79, v69, v69
	v_fmac_f32_e32 v79, v68, v68
	v_add_f32_e32 v78, v79, v78
	v_add_f32_e32 v102, v98, v78
	v_pk_mul_f32 v[90:91], v[94:95], v[72:73]
	v_pk_mul_f32 v[92:93], v[96:97], v[70:71]
	v_pk_mul_f32 v[98:99], v[84:85], v[68:69]
	s_add_i32 s11, s23, 0x80
	v_cvt_pk_bf16_f32 v78, v92, v93
	v_cvt_pk_bf16_f32 v79, v90, v91
	v_cvt_pk_bf16_f32 v80, v100, v101
	v_cvt_pk_bf16_f32 v81, v98, v99
	s_nop 1
	s_nop 0
	v_mfma_f32_16x16x32_bf16 v[10:13], v[78:81], v[2:5], v[10:13]
	v_mov_b32_e32 v78, v102
	s_nop 1
	v_permlane16_swap_b32_e32 v102, v78
	s_waitcnt lgkmcnt(0)
	v_add_f32_e32 v78, v102, v78
	ds_bpermute_b32 v79, v17, v78
	s_and_saveexec_b64 s[12:13], vcc
	s_cbranch_execz .LBB0_1270
	v_or_b32_e32 v80, s11, v206
	v_lshl_add_u32 v80, v80, 4, s10
	s_waitcnt lgkmcnt(0)
	v_add_f32_e32 v78, v78, v79
	ds_write_b32 v80, v78
;     __device__ __forceinline__ void fused(AccT& acc, const GUnit& u, int wr, int wc, int fr, int fq, LAS unsigned char* lds, int wid, int lane) const {
;     ...
;             for (int ai = 0; ai < 2; ++ai)
; #pragma unroll
;                 for (int m = 0; m < 4; ++m) {
;                     const int rowl = ai * 128 + wr * 64 + m * 16;
;                     float sq = 0.f; f32x4 lg = (f32x4){0.f, 0.f, 0.f, 0.f};
; #pragma unroll
;                     for (int bj = 0; bj < 2; ++bj) {
;                         const f32x4 x0 = acc[ai][bj][m][0], x1 = acc[ai][bj][m][1];
;                         sq += (x0[0] * x0[0] + x0[1] * x0[1]) + (x0[2] * x0[2] + x0[3] * x0[3]) + (x1[0] * x1[0] + x1[1] * x1[1]) + (x1[2] * x1[2] + x1[3] * x1[3]);
;                         const f32x4 h0 = x0 * G[bj][0], h1 = x1 * G[bj][1];
;                         lg = __builtin_amdgcn_mfma_f32_16x16x32_bf16(pack8(h0[0], h0[1], h0[2], h0[3], h1[0], h1[1], h1[2], h1[3]), wf[bj], lg, 0, 0, 0);
;                     }
;                     sq += __shfl_xor(sq, 16); sq += __shfl_xor(sq, 32);
;                     if (fq == 0) P[(rowl + fr) * 4 + wc] = sq;
; #pragma unroll
;                     for (int i = 0; i < 4; ++i) LP[((size_t)wc * 256 + rowl + 4 * fq + i) * 16 + fr] = lg[i];
.LBB0_1270:
	s_or_b64 exec, exec, s[12:13]
	v_add_u32_e32 v78, s11, v15
	v_lshl_add_u32 v78, v78, 6, v16
	v_add_u32_e32 v78, 0x2000, v78
	ds_write2_b32 v78, v10, v11 offset1:16
	ds_write2_b32 v78, v12, v13 offset0:32 offset1:48
	v_mul_f32_e32 v10, v63, v63
	v_mul_f32_e32 v11, v65, v65
	v_fmac_f32_e32 v10, v62, v62
	v_fmac_f32_e32 v11, v64, v64
	v_add_f32_e32 v10, v10, v11
	v_mul_f32_e32 v11, v59, v59
	v_fmac_f32_e32 v11, v58, v58
	v_add_f32_e32 v10, v11, v10
	v_mul_f32_e32 v11, v61, v61
	v_fmac_f32_e32 v11, v60, v60
	s_waitcnt lgkmcnt(2)
	v_pk_mul_f32 v[78:79], v[116:117], v[64:65]
	v_add_f32_e32 v98, v11, v10
	v_pk_mul_f32 v[80:81], v[114:115], v[62:63]
	v_pk_mul_f32 v[90:91], v[106:107], v[60:61]
	v_pk_mul_f32 v[92:93], v[108:109], v[58:59]
	v_pk_mul_f32 v[100:101], v[82:83], v[56:57]
	v_cvt_pk_bf16_f32 v10, v80, v81
	v_cvt_pk_bf16_f32 v11, v78, v79
	v_cvt_pk_bf16_f32 v12, v92, v93
	v_cvt_pk_bf16_f32 v13, v90, v91
	s_nop 1
	v_mul_f32_e32 v78, v51, v51
	v_mul_f32_e32 v79, v53, v53
	v_fmac_f32_e32 v78, v50, v50
	v_fmac_f32_e32 v79, v52, v52
	v_add_f32_e32 v78, v78, v79
	v_mul_f32_e32 v79, v57, v57
	v_fmac_f32_e32 v79, v56, v56
	v_mfma_f32_16x16x32_bf16 v[10:13], v[10:13], v[6:9], 0
	v_add_f32_e32 v78, v79, v78
	v_mul_f32_e32 v79, v55, v55
	v_fmac_f32_e32 v79, v54, v54
	v_add_f32_e32 v78, v79, v78
	v_add_f32_e32 v102, v98, v78
	v_pk_mul_f32 v[90:91], v[94:95], v[52:53]
	v_pk_mul_f32 v[92:93], v[96:97], v[50:51]
	v_pk_mul_f32 v[98:99], v[84:85], v[54:55]
	s_add_i32 s11, s23, 0x90
	v_cvt_pk_bf16_f32 v78, v92, v93
	v_cvt_pk_bf16_f32 v79, v90, v91
	v_cvt_pk_bf16_f32 v80, v100, v101
	v_cvt_pk_bf16_f32 v81, v98, v99
	s_nop 1
	s_nop 0
	v_mfma_f32_16x16x32_bf16 v[10:13], v[78:81], v[2:5], v[10:13]
	v_mov_b32_e32 v78, v102
	s_nop 1
	v_permlane16_swap_b32_e32 v102, v78
	s_waitcnt lgkmcnt(0)
	v_add_f32_e32 v78, v102, v78
	ds_bpermute_b32 v79, v17, v78
	s_and_saveexec_b64 s[12:13], vcc
	s_cbranch_execz .LBB0_1272
	v_or_b32_e32 v80, s11, v206
	v_lshl_add_u32 v80, v80, 4, s10
	s_waitcnt lgkmcnt(0)
	v_add_f32_e32 v78, v78, v79
	ds_write_b32 v80, v78
.LBB0_1272:
	s_or_b64 exec, exec, s[12:13]
	v_add_u32_e32 v78, s11, v15
	v_lshl_add_u32 v78, v78, 6, v16
	v_add_u32_e32 v78, 0x2000, v78
	ds_write2_b32 v78, v10, v11 offset1:16
	ds_write2_b32 v78, v12, v13 offset0:32 offset1:48
	v_mul_f32_e32 v10, v47, v47
	v_mul_f32_e32 v11, v49, v49
	v_fmac_f32_e32 v10, v46, v46
	v_fmac_f32_e32 v11, v48, v48
	v_add_f32_e32 v10, v10, v11
	v_mul_f32_e32 v11, v43, v43
	v_fmac_f32_e32 v11, v42, v42
	v_add_f32_e32 v10, v11, v10
	v_mul_f32_e32 v11, v45, v45
	v_fmac_f32_e32 v11, v44, v44
	s_waitcnt lgkmcnt(2)
	v_pk_mul_f32 v[78:79], v[116:117], v[48:49]
	v_add_f32_e32 v98, v11, v10
	v_pk_mul_f32 v[80:81], v[114:115], v[46:47]
	v_pk_mul_f32 v[90:91], v[106:107], v[44:45]
	v_pk_mul_f32 v[92:93], v[108:109], v[42:43]
	v_pk_mul_f32 v[100:101], v[82:83], v[40:41]
	v_cvt_pk_bf16_f32 v10, v80, v81
	v_cvt_pk_bf16_f32 v11, v78, v79
	v_cvt_pk_bf16_f32 v12, v92, v93
	v_cvt_pk_bf16_f32 v13, v90, v91
	s_nop 1
	v_mul_f32_e32 v78, v35, v35
	v_mul_f32_e32 v79, v37, v37
	v_fmac_f32_e32 v78, v34, v34
	v_fmac_f32_e32 v79, v36, v36
	v_add_f32_e32 v78, v78, v79
	v_mul_f32_e32 v79, v41, v41
	v_fmac_f32_e32 v79, v40, v40
	v_mfma_f32_16x16x32_bf16 v[10:13], v[10:13], v[6:9], 0
	v_add_f32_e32 v78, v79, v78
	v_mul_f32_e32 v79, v39, v39
	v_fmac_f32_e32 v79, v38, v38
	v_add_f32_e32 v78, v79, v78
	v_add_f32_e32 v102, v98, v78
	v_pk_mul_f32 v[90:91], v[94:95], v[36:37]
	v_pk_mul_f32 v[92:93], v[96:97], v[34:35]
	v_pk_mul_f32 v[98:99], v[84:85], v[38:39]
	s_add_i32 s11, s23, 0xa0
	v_cvt_pk_bf16_f32 v78, v92, v93
	v_cvt_pk_bf16_f32 v79, v90, v91
	v_cvt_pk_bf16_f32 v80, v100, v101
	v_cvt_pk_bf16_f32 v81, v98, v99
	s_nop 1
	s_nop 0
	v_mfma_f32_16x16x32_bf16 v[10:13], v[78:81], v[2:5], v[10:13]
	v_mov_b32_e32 v78, v102
	s_nop 1
	v_permlane16_swap_b32_e32 v102, v78
	s_waitcnt lgkmcnt(0)
	v_add_f32_e32 v78, v102, v78
	ds_bpermute_b32 v79, v17, v78
	s_and_saveexec_b64 s[12:13], vcc
	s_cbranch_execz .LBB0_1274
	v_or_b32_e32 v80, s11, v206
	v_lshl_add_u32 v80, v80, 4, s10
	s_waitcnt lgkmcnt(0)
	v_add_f32_e32 v78, v78, v79
	ds_write_b32 v80, v78
.LBB0_1274:
	s_or_b64 exec, exec, s[12:13]
	v_add_u32_e32 v78, s11, v15
	v_lshl_add_u32 v78, v78, 6, v16
	v_add_u32_e32 v78, 0x2000, v78
	ds_write2_b32 v78, v10, v11 offset1:16
	ds_write2_b32 v78, v12, v13 offset0:32 offset1:48
	v_mul_f32_e32 v10, v31, v31
	v_mul_f32_e32 v11, v33, v33
	v_fmac_f32_e32 v10, v30, v30
	v_fmac_f32_e32 v11, v32, v32
	v_add_f32_e32 v10, v10, v11
	v_mul_f32_e32 v11, v27, v27
	v_fmac_f32_e32 v11, v26, v26
	v_add_f32_e32 v10, v11, v10
	v_mul_f32_e32 v11, v29, v29
	v_fmac_f32_e32 v11, v28, v28
	v_add_f32_e32 v98, v11, v10
	s_waitcnt lgkmcnt(2)
	v_pk_mul_f32 v[78:79], v[116:117], v[32:33]
	v_pk_mul_f32 v[80:81], v[114:115], v[30:31]
	v_pk_mul_f32 v[90:91], v[106:107], v[28:29]
	v_pk_mul_f32 v[92:93], v[108:109], v[26:27]
	s_addk_i32 s23, 0xb0
	v_cvt_pk_bf16_f32 v10, v80, v81
	v_cvt_pk_bf16_f32 v11, v78, v79
	v_cvt_pk_bf16_f32 v12, v92, v93
	v_cvt_pk_bf16_f32 v13, v90, v91
	s_nop 1
	v_pk_mul_f32 v[90:91], v[84:85], v[20:21]
	v_mfma_f32_16x16x32_bf16 v[8:11], v[10:13], v[6:9], 0
	v_mul_f32_e32 v6, v23, v23
	v_mul_f32_e32 v7, v25, v25
	v_fmac_f32_e32 v6, v22, v22
	v_fmac_f32_e32 v7, v24, v24
	v_add_f32_e32 v6, v6, v7
	v_mul_f32_e32 v7, v19, v19
	v_fmac_f32_e32 v7, v18, v18
	v_add_f32_e32 v6, v7, v6
	v_mul_f32_e32 v7, v21, v21
	v_fmac_f32_e32 v7, v20, v20
	v_add_f32_e32 v6, v7, v6
	v_add_f32_e32 v98, v98, v6
	v_mov_b32_e32 v14, v98
	s_nop 1
	v_permlane16_swap_b32_e32 v98, v14
	v_pk_mul_f32 v[6:7], v[94:95], v[24:25]
	v_pk_mul_f32 v[12:13], v[96:97], v[22:23]
	v_pk_mul_f32 v[92:93], v[82:83], v[18:19]
	s_nop 0
	v_cvt_pk_bf16_f32 v78, v12, v13
	v_cvt_pk_bf16_f32 v79, v6, v7
	v_cvt_pk_bf16_f32 v80, v92, v93
	v_cvt_pk_bf16_f32 v81, v90, v91
	s_nop 1
	s_waitcnt lgkmcnt(0)
	v_add_f32_e32 v6, v98, v14
	ds_bpermute_b32 v7, v17, v6
	v_mfma_f32_16x16x32_bf16 v[2:5], v[78:81], v[2:5], v[8:11]
	s_and_saveexec_b64 s[12:13], vcc
	s_cbranch_execz .LBB0_1276
	s_nop 0
	v_or_b32_e32 v8, s23, v206
	v_lshl_add_u32 v8, v8, 4, s10
	s_waitcnt lgkmcnt(0)
	v_add_f32_e32 v6, v6, v7
	ds_write_b32 v8, v6

;     __device__ __forceinline__ void fused(AccT& acc, const GUnit& u, int wr, int wc, int fr, int fq, LAS unsigned char* lds, int wid, int lane) const {
;     ...
;             float sum = 0.f;
; #pragma unroll
;             for (int k = 0; k < 8; ++k) sum += t[k];
;             asm volatile("s_waitcnt lgkmcnt(0)" ::: "memory"); __builtin_amdgcn_s_barrier(); asm volatile("" ::: "memory");
;             const float lgt = S[rowl] * sum + rb_e;
;             float mx = lgt;
; #pragma unroll
;             for (int o = 1; o < 16; o <<= 1) mx = fmaxf(mx, __shfl_xor(mx, o));
;             const float ex = expf(lgt - mx); float den = ex;
; #pragma unroll
;             for (int o = 1; o < 16; o <<= 1) den += __shfl_xor(den, o);
;             __hip_atomic_store(aff + ((size_t)b * 16 + e) * 2048 + (u.pm & 7) * 256 + rowl, ex / den, __ATOMIC_RELAXED, __HIP_MEMORY_SCOPE_AGENT);
;             asm volatile("s_waitcnt vmcnt(0)" ::: "memory");
;             if (lane == 0) __hip_atomic_fetch_add(done + (b * 8 + wid) * 32, 1u, __ATOMIC_RELAXED, __HIP_MEMORY_SCOPE_AGENT);
.LBB0_1298:
	s_or_b64 exec, exec, s[42:43]
	s_waitcnt vmcnt(7)
	v_add_f32_e32 v78, 0, v91
	s_waitcnt vmcnt(6)
	v_add_f32_e32 v78, v78, v92
	s_waitcnt vmcnt(5)
	v_add_f32_e32 v78, v78, v93
	s_waitcnt lgkmcnt(0)
	s_barrier
	v_lshl_add_u32 v79, v80, 2, 0
	s_waitcnt vmcnt(4)
	v_add_f32_e32 v78, v78, v99
	ds_read_b32 v79, v79 offset:4096
	s_waitcnt vmcnt(3)
	v_add_f32_e32 v78, v78, v98
	s_waitcnt vmcnt(2)
	v_add_f32_e32 v78, v78, v100
	s_waitcnt vmcnt(1)
	v_add_f32_e32 v78, v78, v101
	s_waitcnt vmcnt(0)
	v_add_f32_e32 v78, v78, v102
	v_cmp_lt_i32_e32 vcc, v220, v213
	s_waitcnt lgkmcnt(0)
	v_fmac_f32_e32 v90, v78, v79
	v_xor_b32_e32 v91, 2, v212
	v_cndmask_b32_e32 v78, v212, v220, vcc
	v_lshlrev_b32_e32 v78, 2, v78
	ds_bpermute_b32 v79, v78, v90
	v_cmp_lt_i32_e32 vcc, v91, v213
	s_mov_b32 s0, 0x3fb8aa3b
	s_lshl_b64 s[10:11], s[44:45], 17
	v_cndmask_b32_e32 v91, v212, v91, vcc
	s_waitcnt lgkmcnt(0)
	v_max_f32_e32 v79, v79, v79
	v_max_f32_e32 v79, v90, v79
	v_lshlrev_b32_e32 v91, 2, v91
	ds_bpermute_b32 v92, v91, v79
	v_readlane_b32 s12, v254, 5
	v_readlane_b32 s13, v254, 6
	s_add_u32 s10, s12, s10
	s_addc_u32 s11, s13, s11
	s_waitcnt lgkmcnt(0)
	v_max_f32_e32 v92, v92, v92
	v_max_f32_e32 v79, v79, v92
	v_xor_b32_e32 v92, 4, v212
	v_cmp_lt_i32_e32 vcc, v92, v213
	s_and_b32 s8, s9, 0x700
	s_lshl_b32 s60, s8, 2
	v_cndmask_b32_e32 v92, v212, v92, vcc
	v_lshlrev_b32_e32 v92, 2, v92
	ds_bpermute_b32 v93, v92, v79
	s_waitcnt lgkmcnt(0)
	v_max_f32_e32 v93, v93, v93
	v_max_f32_e32 v79, v79, v93
	v_xor_b32_e32 v93, 8, v212
	v_cmp_lt_i32_e32 vcc, v93, v213
	s_nop 1
	v_cndmask_b32_e32 v93, v212, v93, vcc
	v_lshlrev_b32_e32 v93, 2, v93
	ds_bpermute_b32 v98, v93, v79
	s_waitcnt lgkmcnt(0)
	v_max_f32_e32 v98, v98, v98
	v_max_f32_e32 v79, v79, v98
	v_sub_f32_e32 v79, v90, v79
	v_mul_f32_e32 v90, 0x3fb8aa3b, v79
	v_fma_f32 v98, v79, s0, -v90
	v_rndne_f32_e32 v99, v90
	v_fmac_f32_e32 v98, 0x32a5705f, v79
	v_sub_f32_e32 v90, v90, v99
	v_add_f32_e32 v90, v90, v98
	v_exp_f32_e32 v90, v90
	v_cvt_i32_f32_e32 v98, v99
	s_mov_b32 s0, 0xc2ce8ed0
	v_cmp_ngt_f32_e32 vcc, s0, v79
	v_ldexp_f32 v90, v90, v98
	s_nop 0
	v_cndmask_b32_e32 v90, 0, v90, vcc
	v_cmp_nlt_f32_e32 vcc, s7, v79
	s_nop 1
	v_cndmask_b32_e32 v90, v227, v90, vcc
	s_waitcnt lgkmcnt(0)
	s_nop 1
	v_add_f32_dpp v78, v90, v90 quad_perm:[1,0,3,2] row_mask:0xf bank_mask:0xf
	v_lshlrev_b32_e32 v91, 11, v206
	v_lshlrev_b32_e32 v194, 2, v91
	s_waitcnt lgkmcnt(0)
	s_nop 1
	v_add_f32_dpp v78, v78, v78 quad_perm:[2,3,0,1] row_mask:0xf bank_mask:0xf
	s_waitcnt lgkmcnt(0)
	s_nop 1
	v_add_f32_dpp v91, v78, v78 row_half_mirror row_mask:0xf bank_mask:0xf
	v_lshl_add_u64 v[78:79], s[10:11], 0, v[194:195]
	v_lshl_add_u64 v[78:79], v[78:79], 0, s[60:61]
	v_lshl_add_u64 v[78:79], v[80:81], 2, v[78:79]
	s_waitcnt lgkmcnt(0)
	s_nop 1
	v_add_f32_dpp v91, v91, v91 row_mirror row_mask:0xf bank_mask:0xf
	v_div_scale_f32 v92, s[10:11], v91, v91, v90
	v_rcp_f32_e32 v93, v92
	v_div_scale_f32 v80, vcc, v90, v91, v90
	v_fma_f32 v81, -v92, v93, 1.0
	v_fmac_f32_e32 v93, v81, v93
	v_mul_f32_e32 v81, v80, v93
	v_fma_f32 v98, -v92, v81, v80
	v_fmac_f32_e32 v81, v98, v93
	v_fma_f32 v80, -v92, v81, v80
	v_div_fmas_f32 v80, v80, v93, v81
	v_div_fixup_f32 v80, v80, v91, v90
	global_store_dword v[78:79], v80, off sc1
	s_waitcnt vmcnt(0)
	s_and_saveexec_b64 s[12:13], s[36:37]
	s_cbranch_execz .LBB0_1301
	s_mov_b64 s[34:35], exec
	v_mbcnt_lo_u32_b32 v78, s34, 0
	v_mbcnt_hi_u32_b32 v78, s35, v78
	v_cmp_eq_u32_e32 vcc, 0, v78
	s_and_b64 s[10:11], exec, vcc
	s_mov_b64 exec, s[10:11]
	s_cbranch_execz .LBB0_1301
	v_readlane_b32 s10, v250, 59
	v_readlane_b32 s11, v250, 60
	s_lshl_b64 s[10:11], s[10:11], 12
	v_readlane_b32 s0, v254, 9
	s_add_u32 s8, s0, s10
	v_readlane_b32 s0, v254, 10
	s_addc_u32 s22, s0, s11
	v_readlane_b32 s10, v255, 18
	s_and_b32 s10, s10, 0x7fffff8
	s_add_i32 s10, s10, s4
	v_readlane_b32 s11, v255, 19
	s_lshl_b32 s10, s10, 5
	s_ashr_i32 s11, s10, 31
	s_lshl_b64 s[10:11], s[10:11], 2
	s_add_u32 s10, s8, s10
	s_addc_u32 s11, s22, s11
	s_bcnt1_i32_b64 s4, s[34:35]
	v_mov_b32_e32 v78, s4
	global_atomic_add v195, v78, s[10:11]

; __device__ __forceinline__ unsigned pk2(float lo, float hi) { unsigned r; asm("v_cvt_pk_bf16_f32 %0, %1, %2" : "=v"(r) : "v"(lo), "v"(hi)); return r; }
; __device__ __forceinline__ float bflo(unsigned u) { return __uint_as_float(u << 16); }
; __device__ __forceinline__ float bfhi(unsigned u) { return __uint_as_float(u & 0xffff0000u); }
; __device__ __forceinline__ void ph_norm1(const Params& p, int mode, LAS unsigned char* lds) {
;     ...
;             f32x4 v[8];
; #pragma unroll
;             for (int j = 0; j < 8; ++j) { const f32x4 g = gfv[j];
;                 v[j] = (f32x4){bflo(xw[q][j].x), bfhi(xw[q][j].x), bflo(xw[q][j].y), bfhi(xw[q][j].y)} + g * macc[j]; }
;             if (mode == 1) {
;                 bf16_t* xo = (bf16_t*)(p.ws + WS_X) + (size_t)t * DM;
; #pragma unroll
;                 for (int j = 0; j < 8; ++j) { u32x2 w; w.x = pk2(v[j][0], v[j][1]); w.y = pk2(v[j][2], v[j][3]); *(u32x2*)(xo + 4 * lane + 256 * j) = w;
;                     v[j] = (f32x4){bflo(w.x), bfhi(w.x), bflo(w.y), bfhi(w.y)}; }
;             }
;             float ss = 0.f;
; #pragma unroll
;             for (int j = 0; j < 8; ++j) ss += v[j][0] * v[j][0] + v[j][1] * v[j][1] + v[j][2] * v[j][2] + v[j][3] * v[j][3];
;             const float r = 1.0f / sqrtf(wave_sum(ss) * (1.f / DM) + EPS);
.LBB0_1789:
	v_lshlrev_b32_e32 v66, 16, v104
	v_and_b32_e32 v67, 0xffff0000, v104
	v_pk_fma_f32 v[60:61], v[60:61], v[132:133], v[66:67]
	v_lshlrev_b32_e32 v66, 16, v102
	v_and_b32_e32 v67, 0xffff0000, v102
	v_pk_fma_f32 v[56:57], v[56:57], v[128:129], v[66:67]
	v_lshlrev_b32_e32 v66, 16, v100
	v_and_b32_e32 v67, 0xffff0000, v100
	v_pk_fma_f32 v[52:53], v[52:53], v[124:125], v[66:67]
	v_lshlrev_b32_e32 v66, 16, v98
	v_and_b32_e32 v67, 0xffff0000, v98
	v_pk_fma_f32 v[48:49], v[48:49], v[120:121], v[66:67]
	v_lshlrev_b32_e32 v66, 16, v96
	v_and_b32_e32 v67, 0xffff0000, v96
	v_pk_fma_f32 v[44:45], v[44:45], v[116:117], v[66:67]
	v_lshlrev_b32_e32 v66, 16, v94
	v_and_b32_e32 v67, 0xffff0000, v94
	v_pk_fma_f32 v[40:41], v[40:41], v[112:113], v[66:67]
	v_lshlrev_b32_e32 v66, 16, v92
	v_and_b32_e32 v67, 0xffff0000, v92
	v_pk_fma_f32 v[36:37], v[36:37], v[108:109], v[66:67]
	v_lshlrev_b32_e32 v66, 16, v90
	v_and_b32_e32 v67, 0xffff0000, v90
	v_lshlrev_b32_e32 v90, 16, v91
	v_and_b32_e32 v91, 0xffff0000, v91
	v_lshlrev_b32_e32 v104, 16, v105
	v_and_b32_e32 v105, 0xffff0000, v105
	v_lshlrev_b32_e32 v102, 16, v103
	v_and_b32_e32 v103, 0xffff0000, v103
	v_pk_fma_f32 v[34:35], v[34:35], v[64:65], v[90:91]
	v_mul_f32_e32 v64, v61, v61
	v_mul_f32_e32 v65, v57, v57
	v_pk_fma_f32 v[62:63], v[62:63], v[134:135], v[104:105]
	v_pk_fma_f32 v[58:59], v[58:59], v[130:131], v[102:103]
	v_fmac_f32_e32 v64, v60, v60
	v_fmac_f32_e32 v65, v56, v56
	v_fmac_f32_e32 v64, v62, v62
	v_fmac_f32_e32 v65, v58, v58
	v_fmac_f32_e32 v64, v63, v63
	v_fmac_f32_e32 v65, v59, v59
	v_lshlrev_b32_e32 v100, 16, v101
	v_and_b32_e32 v101, 0xffff0000, v101
	v_add_f32_e32 v64, v64, v65
	v_mul_f32_e32 v65, v53, v53
	v_pk_fma_f32 v[54:55], v[54:55], v[126:127], v[100:101]
	v_fmac_f32_e32 v65, v52, v52
	v_fmac_f32_e32 v65, v54, v54
	v_fmac_f32_e32 v65, v55, v55
	v_lshlrev_b32_e32 v98, 16, v99
	v_and_b32_e32 v99, 0xffff0000, v99
	v_add_f32_e32 v64, v65, v64
	v_mul_f32_e32 v65, v49, v49
	v_pk_fma_f32 v[50:51], v[50:51], v[122:123], v[98:99]
	v_fmac_f32_e32 v65, v48, v48
	v_fmac_f32_e32 v65, v50, v50
	v_fmac_f32_e32 v65, v51, v51
	v_lshlrev_b32_e32 v96, 16, v97
	v_and_b32_e32 v97, 0xffff0000, v97
	v_add_f32_e32 v64, v65, v64
	v_mul_f32_e32 v65, v45, v45
	v_pk_fma_f32 v[46:47], v[46:47], v[118:119], v[96:97]
	v_fmac_f32_e32 v65, v44, v44
	v_fmac_f32_e32 v65, v46, v46
	v_fmac_f32_e32 v65, v47, v47
	v_lshlrev_b32_e32 v94, 16, v95
	v_and_b32_e32 v95, 0xffff0000, v95
	v_add_f32_e32 v64, v65, v64
	v_mul_f32_e32 v65, v41, v41
	v_pk_fma_f32 v[42:43], v[42:43], v[114:115], v[94:95]
	v_fmac_f32_e32 v65, v40, v40
	v_pk_fma_f32 v[32:33], v[32:33], v[106:107], v[66:67]
	v_fmac_f32_e32 v65, v42, v42
	v_lshlrev_b32_e32 v92, 16, v93
	v_and_b32_e32 v93, 0xffff0000, v93
	v_fmac_f32_e32 v65, v43, v43
	v_mov_b32_e32 v66, v33
	v_mov_b32_e32 v67, v37
	v_pk_fma_f32 v[38:39], v[38:39], v[110:111], v[92:93]
	v_add_f32_e32 v69, v65, v64
	v_mov_b32_e32 v64, v32
	v_mov_b32_e32 v65, v36
	v_pk_mul_f32 v[66:67], v[66:67], v[66:67]
	s_nop 0
	v_pk_fma_f32 v[64:65], v[64:65], v[64:65], v[66:67]
	v_mov_b32_e32 v66, v34
	v_mov_b32_e32 v67, v38
	v_pk_fma_f32 v[64:65], v[66:67], v[66:67], v[64:65]
	v_mov_b32_e32 v66, v35
	v_mov_b32_e32 v67, v39
	v_pk_fma_f32 v[64:65], v[66:67], v[66:67], v[64:65]
	s_nop 0
	v_add_f32_e32 v65, v65, v69
	v_add_f32_e32 v64, v64, v65
	s_waitcnt lgkmcnt(0)
	s_nop 1
	v_add_f32_dpp v64, v64, v64 quad_perm:[1,0,3,2] row_mask:0xf bank_mask:0xf
	s_waitcnt lgkmcnt(0)
	s_nop 1
	v_add_f32_dpp v64, v64, v64 quad_perm:[2,3,0,1] row_mask:0xf bank_mask:0xf
	s_waitcnt lgkmcnt(0)
	s_nop 1
	v_add_f32_dpp v64, v64, v64 row_half_mirror row_mask:0xf bank_mask:0xf
	s_waitcnt lgkmcnt(0)
; __device__ __forceinline__ void ph_norm1(const Params& p, int mode, LAS unsigned char* lds) {
;     ...
;             const float r = 1.0f / sqrtf(wave_sum(ss) * (1.f / DM) + EPS);
;             asm volatile("" ::: "memory");
;             if (mode == 2) {
;                 float* o = p.out + (size_t)t * DM;
; #pragma unroll
;                 for (int j = 0; j < 8; ++j) { const f32x4 g = fgv[j]; __builtin_nontemporal_store(v[j] * r * g, (f32x4*)(o + 4 * lane + 256 * j)); }
	s_nop 1
	v_add_f32_dpp v64, v64, v64 row_mirror row_mask:0xf bank_mask:0xf
	v_mov_b32_e32 v65, v64
	s_nop 1
	v_permlane16_swap_b32_e32 v64, v65
	s_waitcnt lgkmcnt(0)
	v_add_f32_e32 v64, v64, v65
	v_mov_b32_e32 v65, v64
	s_nop 1
	v_permlane32_swap_b32_e32 v64, v65
	s_waitcnt lgkmcnt(0)
	v_add_f32_e32 v64, v64, v65
	v_fmamk_f32 v64, v64, 0x3a000000, v192
	v_mul_f32_e32 v65, 0x4f800000, v64
	v_cmp_gt_f32_e32 vcc, s10, v64
	s_nop 1
	v_cndmask_b32_e32 v64, v64, v65, vcc
	v_sqrt_f32_e32 v65, v64
	s_nop 0
	v_add_u32_e32 v66, -1, v65
	v_fma_f32 v67, -v66, v65, v64
	v_cmp_ge_f32_e64 s[0:1], 0, v67
	v_add_u32_e32 v67, 1, v65
	s_nop 0
	v_cndmask_b32_e64 v66, v65, v66, s[0:1]
	v_fma_f32 v65, -v67, v65, v64
	v_cmp_lt_f32_e64 s[0:1], 0, v65
	s_nop 1
	v_cndmask_b32_e64 v65, v66, v67, s[0:1]
	v_mul_f32_e32 v66, 0x37800000, v65
	v_cndmask_b32_e32 v65, v65, v66, vcc
	v_cmp_class_f32_e32 vcc, v64, v193
	s_nop 1
	v_cndmask_b32_e32 v65, v65, v64, vcc
	v_div_scale_f32 v66, s[0:1], v65, v65, 1.0
	v_rcp_f32_e32 v67, v66
	v_or_b32_e32 v64, 3, v68
	v_add_u32_e32 v68, s20, v68
	v_fma_f32 v69, -v66, v67, 1.0
	v_fmac_f32_e32 v67, v69, v67
	v_div_scale_f32 v69, vcc, 1.0, v65, 1.0
	v_mul_f32_e32 v90, v69, v67
	v_fma_f32 v91, -v66, v90, v69
	v_fmac_f32_e32 v90, v91, v67
	v_fma_f32 v66, -v66, v90, v69
	v_div_fmas_f32 v66, v66, v67, v90
	v_div_fixup_f32 v66, v66, v65, 1.0
	v_ashrrev_i32_e32 v65, 31, v64
	v_lshlrev_b64 v[64:65], 13, v[64:65]
	v_pk_mul_f32 v[60:61], v[60:61], v[66:67] op_sel_hi:[1,0]
	v_pk_mul_f32 v[62:63], v[62:63], v[66:67] op_sel_hi:[1,0]
	v_lshl_add_u64 v[64:65], v[88:89], 0, v[64:65]
	v_pk_mul_f32 v[30:31], v[30:31], v[62:63]
	v_pk_mul_f32 v[28:29], v[28:29], v[60:61]
	global_store_dwordx4 v[64:65], v[28:31], off nt
	s_nop 1
	v_pk_mul_f32 v[28:29], v[56:57], v[66:67] op_sel_hi:[1,0]
	v_pk_mul_f32 v[30:31], v[58:59], v[66:67] op_sel_hi:[1,0]
	v_pk_mul_f32 v[24:25], v[24:25], v[28:29]
	v_pk_mul_f32 v[26:27], v[26:27], v[30:31]
	global_store_dwordx4 v[64:65], v[24:27], off offset:1024 nt
	s_nop 1
	v_pk_mul_f32 v[24:25], v[52:53], v[66:67] op_sel_hi:[1,0]
	v_pk_mul_f32 v[26:27], v[54:55], v[66:67] op_sel_hi:[1,0]
	v_pk_mul_f32 v[20:21], v[20:21], v[24:25]
	v_pk_mul_f32 v[22:23], v[22:23], v[26:27]
	global_store_dwordx4 v[64:65], v[20:23], off offset:2048 nt
	s_nop 1
	v_pk_mul_f32 v[20:21], v[48:49], v[66:67] op_sel_hi:[1,0]
	v_pk_mul_f32 v[22:23], v[50:51], v[66:67] op_sel_hi:[1,0]
	v_pk_mul_f32 v[16:17], v[16:17], v[20:21]
	v_pk_mul_f32 v[18:19], v[18:19], v[22:23]
	global_store_dwordx4 v[64:65], v[16:19], off offset:3072 nt
	s_nop 1
	v_pk_mul_f32 v[16:17], v[44:45], v[66:67] op_sel_hi:[1,0]
	v_pk_mul_f32 v[18:19], v[46:47], v[66:67] op_sel_hi:[1,0]
	v_pk_mul_f32 v[12:13], v[12:13], v[16:17]
	v_add_co_u32_e32 v16, vcc, s7, v64
	v_pk_mul_f32 v[14:15], v[14:15], v[18:19]
	s_nop 0
	v_addc_co_u32_e32 v17, vcc, 0, v65, vcc
	global_store_dwordx4 v[16:17], v[12:15], off nt
	v_cmp_lt_i32_e32 vcc, s11, v68
	s_or_b64 s[2:3], vcc, s[2:3]
	v_pk_mul_f32 v[12:13], v[40:41], v[66:67] op_sel_hi:[1,0]
	v_pk_mul_f32 v[14:15], v[42:43], v[66:67] op_sel_hi:[1,0]
	v_pk_mul_f32 v[8:9], v[8:9], v[12:13]
	v_pk_mul_f32 v[10:11], v[10:11], v[14:15]
	global_store_dwordx4 v[16:17], v[8:11], off offset:1024 nt
	s_nop 1
	v_pk_mul_f32 v[8:9], v[36:37], v[66:67] op_sel_hi:[1,0]
	v_pk_mul_f32 v[10:11], v[38:39], v[66:67] op_sel_hi:[1,0]
	v_pk_mul_f32 v[4:5], v[4:5], v[8:9]
	v_pk_mul_f32 v[6:7], v[6:7], v[10:11]
	global_store_dwordx4 v[16:17], v[4:7], off offset:2048 nt
	s_nop 1
	v_pk_mul_f32 v[4:5], v[32:33], v[66:67] op_sel_hi:[1,0]
	v_pk_mul_f32 v[6:7], v[34:35], v[66:67] op_sel_hi:[1,0]
	v_pk_mul_f32 v[0:1], v[0:1], v[4:5]
	v_pk_mul_f32 v[2:3], v[2:3], v[6:7]
	global_store_dwordx4 v[16:17], v[0:3], off offset:3072 nt
	s_andn2_b64 exec, exec, s[2:3]
	s_cbranch_execz .LBB0_1802

; __device__ __forceinline__ unsigned pk2(float lo, float hi) { unsigned r; asm("v_cvt_pk_bf16_f32 %0, %1, %2" : "=v"(r) : "v"(lo), "v"(hi)); return r; }
; __device__ __forceinline__ float bflo(unsigned u) { return __uint_as_float(u << 16); }
; __device__ __forceinline__ float bfhi(unsigned u) { return __uint_as_float(u & 0xffff0000u); }
; __device__ __forceinline__ void ph_norm1(const Params& p, int mode, LAS unsigned char* lds) {
;     ...
;             f32x4 v[8];
; #pragma unroll
;             for (int j = 0; j < 8; ++j) { const f32x4 g = gfv[j];
;                 v[j] = (f32x4){bflo(xw[q][j].x), bfhi(xw[q][j].x), bflo(xw[q][j].y), bfhi(xw[q][j].y)} + g * macc[j]; }
;             if (mode == 1) {
;                 bf16_t* xo = (bf16_t*)(p.ws + WS_X) + (size_t)t * DM;
; #pragma unroll
;                 for (int j = 0; j < 8; ++j) { u32x2 w; w.x = pk2(v[j][0], v[j][1]); w.y = pk2(v[j][2], v[j][3]); *(u32x2*)(xo + 4 * lane + 256 * j) = w;
;                     v[j] = (f32x4){bflo(w.x), bfhi(w.x), bflo(w.y), bfhi(w.y)}; }
;             }
;             float ss = 0.f;
; #pragma unroll
;             for (int j = 0; j < 8; ++j) ss += v[j][0] * v[j][0] + v[j][1] * v[j][1] + v[j][2] * v[j][2] + v[j][3] * v[j][3];
;             const float r = 1.0f / sqrtf(wave_sum(ss) * (1.f / DM) + EPS);
.LBB0_1793:
	v_lshlrev_b32_e32 v194, 16, v154
	v_and_b32_e32 v195, 0xffff0000, v154
	v_lshlrev_b32_e32 v154, 16, v155
	v_and_b32_e32 v155, 0xffff0000, v155
	v_pk_fma_f32 v[154:155], v[62:63], v[184:185], v[154:155]
	v_lshlrev_b32_e32 v184, 16, v152
	v_and_b32_e32 v185, 0xffff0000, v152
	v_lshlrev_b32_e32 v152, 16, v153
	v_and_b32_e32 v153, 0xffff0000, v153
	v_pk_fma_f32 v[152:153], v[58:59], v[180:181], v[152:153]
	v_lshlrev_b32_e32 v180, 16, v148
	v_and_b32_e32 v181, 0xffff0000, v148
	v_lshlrev_b32_e32 v148, 16, v149
	v_and_b32_e32 v149, 0xffff0000, v149
	v_pk_fma_f32 v[148:149], v[54:55], v[176:177], v[148:149]
	v_lshlrev_b32_e32 v176, 16, v146
	v_and_b32_e32 v177, 0xffff0000, v146
	v_lshlrev_b32_e32 v146, 16, v147
	v_and_b32_e32 v147, 0xffff0000, v147
	v_pk_fma_f32 v[146:147], v[50:51], v[172:173], v[146:147]
	v_lshlrev_b32_e32 v172, 16, v144
	v_and_b32_e32 v173, 0xffff0000, v144
	v_lshlrev_b32_e32 v144, 16, v145
	v_and_b32_e32 v145, 0xffff0000, v145
	v_pk_fma_f32 v[144:145], v[46:47], v[168:169], v[144:145]
	v_lshlrev_b32_e32 v168, 16, v142
	v_and_b32_e32 v169, 0xffff0000, v142
	v_lshlrev_b32_e32 v142, 16, v143
	v_and_b32_e32 v143, 0xffff0000, v143
	v_pk_fma_f32 v[164:165], v[42:43], v[164:165], v[142:143]
	v_lshlrev_b32_e32 v142, 16, v140
	v_and_b32_e32 v143, 0xffff0000, v140
	v_lshlrev_b32_e32 v140, 16, v141
	v_and_b32_e32 v141, 0xffff0000, v141
	v_pk_fma_f32 v[182:183], v[60:61], v[182:183], v[194:195]
	v_pk_fma_f32 v[178:179], v[56:57], v[178:179], v[184:185]
	v_pk_fma_f32 v[160:161], v[38:39], v[160:161], v[140:141]
	v_lshlrev_b32_e32 v140, 16, v138
	v_and_b32_e32 v141, 0xffff0000, v138
	v_lshlrev_b32_e32 v138, 16, v139
	v_and_b32_e32 v139, 0xffff0000, v139
	v_pk_fma_f32 v[150:151], v[34:35], v[150:151], v[138:139]
	v_mul_f32_e32 v64, v183, v183
	v_mul_f32_e32 v138, v179, v179
	v_fmac_f32_e32 v64, v182, v182
	v_fmac_f32_e32 v138, v178, v178
	v_fmac_f32_e32 v64, v154, v154
	v_fmac_f32_e32 v138, v152, v152
	v_pk_fma_f32 v[174:175], v[52:53], v[174:175], v[180:181]
	v_fmac_f32_e32 v64, v155, v155
	v_fmac_f32_e32 v138, v153, v153
	v_add_f32_e32 v64, v64, v138
	v_mul_f32_e32 v138, v175, v175
	v_fmac_f32_e32 v138, v174, v174
	v_fmac_f32_e32 v138, v148, v148
	v_pk_fma_f32 v[170:171], v[48:49], v[170:171], v[176:177]
	v_fmac_f32_e32 v138, v149, v149
	v_add_f32_e32 v64, v138, v64
	v_mul_f32_e32 v138, v171, v171
	v_fmac_f32_e32 v138, v170, v170
	v_fmac_f32_e32 v138, v146, v146
	v_pk_fma_f32 v[166:167], v[44:45], v[166:167], v[172:173]
	v_fmac_f32_e32 v138, v147, v147
	v_add_f32_e32 v64, v138, v64
	v_mul_f32_e32 v138, v167, v167
	v_fmac_f32_e32 v138, v166, v166
	v_fmac_f32_e32 v138, v144, v144
	v_pk_fma_f32 v[162:163], v[40:41], v[162:163], v[168:169]
	v_fmac_f32_e32 v138, v145, v145
	v_add_f32_e32 v64, v138, v64
	v_mul_f32_e32 v138, v163, v163
	v_fmac_f32_e32 v138, v162, v162
	v_pk_fma_f32 v[158:159], v[36:37], v[158:159], v[142:143]
	v_pk_fma_f32 v[156:157], v[32:33], v[156:157], v[140:141]
	v_fmac_f32_e32 v138, v164, v164
	v_fmac_f32_e32 v138, v165, v165
	v_mov_b32_e32 v140, v157
	v_mov_b32_e32 v141, v159
	v_add_f32_e32 v64, v138, v64
	v_mov_b32_e32 v138, v156
	v_mov_b32_e32 v139, v158
	v_pk_mul_f32 v[140:141], v[140:141], v[140:141]
	s_nop 0
	v_pk_fma_f32 v[138:139], v[138:139], v[138:139], v[140:141]
	v_mov_b32_e32 v140, v150
	v_mov_b32_e32 v141, v160
	v_pk_fma_f32 v[138:139], v[140:141], v[140:141], v[138:139]
	v_mov_b32_e32 v140, v151
	v_mov_b32_e32 v141, v161
	v_pk_fma_f32 v[138:139], v[140:141], v[140:141], v[138:139]
	s_nop 0
	v_add_f32_e32 v64, v139, v64
	v_add_f32_e32 v64, v138, v64
	s_waitcnt lgkmcnt(0)
	s_nop 1
	v_add_f32_dpp v64, v64, v64 quad_perm:[1,0,3,2] row_mask:0xf bank_mask:0xf
	s_waitcnt lgkmcnt(0)
	s_nop 1
	v_add_f32_dpp v64, v64, v64 quad_perm:[2,3,0,1] row_mask:0xf bank_mask:0xf
	s_waitcnt lgkmcnt(0)
	s_nop 1
	v_add_f32_dpp v64, v64, v64 row_half_mirror row_mask:0xf bank_mask:0xf
	s_waitcnt lgkmcnt(0)
	s_nop 1
	v_add_f32_dpp v64, v64, v64 row_mirror row_mask:0xf bank_mask:0xf
	v_mov_b32_e32 v138, v64
	s_nop 1
	v_permlane16_swap_b32_e32 v64, v138
	s_waitcnt lgkmcnt(0)
	v_add_f32_e32 v64, v64, v138
	v_mov_b32_e32 v138, v64
	s_nop 1
	v_permlane32_swap_b32_e32 v64, v138
	s_waitcnt lgkmcnt(0)
; __device__ __forceinline__ void ph_norm1(const Params& p, int mode, LAS unsigned char* lds) {
;     ...
;             f32x4 macc[8];
; #pragma unroll
;             for (int j = 0; j < 8; ++j) macc[j] = (f32x4){0.f, 0.f, 0.f, 0.f};
;             unsigned m = (unsigned)(__ballot(myslot[q] >= 0) & 0xffffull);
;             while (m) {
;     ...
;             const float r = 1.0f / sqrtf(wave_sum(ss) * (1.f / DM) + EPS);
;             asm volatile("" ::: "memory");
;             if (mode == 2) {
;                 float* o = p.out + (size_t)t * DM;
; #pragma unroll
;                 for (int j = 0; j < 8; ++j) { const f32x4 g = fgv[j]; __builtin_nontemporal_store(v[j] * r * g, (f32x4*)(o + 4 * lane + 256 * j)); }
	v_add_f32_e32 v64, v64, v138
	v_fmamk_f32 v64, v64, 0x3a000000, v192
	v_mul_f32_e32 v138, 0x4f800000, v64
	v_cmp_gt_f32_e32 vcc, s10, v64
	s_nop 1
	v_cndmask_b32_e32 v64, v64, v138, vcc
	v_sqrt_f32_e32 v138, v64
	s_nop 0
	v_add_u32_e32 v139, -1, v138
	v_fma_f32 v140, -v139, v138, v64
	v_cmp_ge_f32_e64 s[0:1], 0, v140
	v_add_u32_e32 v140, 1, v138
	s_nop 0
	v_cndmask_b32_e64 v139, v138, v139, s[0:1]
	v_fma_f32 v138, -v140, v138, v64
	v_cmp_lt_f32_e64 s[0:1], 0, v138
	s_nop 1
	v_cndmask_b32_e64 v138, v139, v140, s[0:1]
	v_mul_f32_e32 v139, 0x37800000, v138
	v_cndmask_b32_e32 v138, v138, v139, vcc
	v_cmp_class_f32_e32 vcc, v64, v193
	v_mov_b32_e32 v139, 0
	v_mov_b32_e32 v169, v139
	v_cndmask_b32_e32 v64, v138, v64, vcc
	v_div_scale_f32 v138, s[0:1], v64, v64, 1.0
	v_rcp_f32_e32 v140, v138
	v_mov_b32_e32 v168, v139
	v_fma_f32 v141, -v138, v140, 1.0
	v_fmac_f32_e32 v140, v141, v140
	v_div_scale_f32 v141, vcc, 1.0, v64, 1.0
	v_mul_f32_e32 v142, v141, v140
	v_fma_f32 v143, -v138, v142, v141
	v_fmac_f32_e32 v142, v143, v140
	v_fma_f32 v138, -v138, v142, v141
	v_div_fmas_f32 v138, v138, v140, v142
	v_div_fixup_f32 v64, v138, v64, 1.0
	v_pk_mul_f32 v[140:141], v[182:183], v[64:65] op_sel_hi:[1,0]
	v_pk_mul_f32 v[142:143], v[154:155], v[64:65] op_sel_hi:[1,0]
	v_lshlrev_b64 v[154:155], 13, v[68:69]
	v_lshl_add_u64 v[154:155], v[88:89], 0, v[154:155]
	v_pk_mul_f32 v[142:143], v[30:31], v[142:143]
	v_pk_mul_f32 v[140:141], v[28:29], v[140:141]
	global_store_dwordx4 v[154:155], v[140:143], off nt
	v_mov_b32_e32 v138, v139
	s_nop 0
	v_pk_mul_f32 v[140:141], v[178:179], v[64:65] op_sel_hi:[1,0]
	v_pk_mul_f32 v[142:143], v[152:153], v[64:65] op_sel_hi:[1,0]
	v_pk_mul_f32 v[140:141], v[24:25], v[140:141]
	v_pk_mul_f32 v[142:143], v[26:27], v[142:143]
	global_store_dwordx4 v[154:155], v[140:143], off offset:1024 nt
	v_mov_b32_e32 v153, v139
	v_mov_b32_e32 v152, v139
	v_pk_mul_f32 v[140:141], v[174:175], v[64:65] op_sel_hi:[1,0]
	v_pk_mul_f32 v[142:143], v[148:149], v[64:65] op_sel_hi:[1,0]
	v_pk_mul_f32 v[140:141], v[20:21], v[140:141]
	v_pk_mul_f32 v[142:143], v[22:23], v[142:143]
	global_store_dwordx4 v[154:155], v[140:143], off offset:2048 nt
	v_mov_b32_e32 v149, v139
	v_mov_b32_e32 v148, v139
	v_pk_mul_f32 v[140:141], v[170:171], v[64:65] op_sel_hi:[1,0]
	v_pk_mul_f32 v[142:143], v[146:147], v[64:65] op_sel_hi:[1,0]
	v_pk_mul_f32 v[140:141], v[16:17], v[140:141]
	v_pk_mul_f32 v[142:143], v[18:19], v[142:143]
	global_store_dwordx4 v[154:155], v[140:143], off offset:3072 nt
	v_mov_b32_e32 v147, v139
	v_mov_b32_e32 v146, v139
	v_pk_mul_f32 v[140:141], v[166:167], v[64:65] op_sel_hi:[1,0]
	v_pk_mul_f32 v[142:143], v[144:145], v[64:65] op_sel_hi:[1,0]
	v_add_co_u32_e32 v144, vcc, s7, v154
	v_pk_mul_f32 v[142:143], v[14:15], v[142:143]
	v_pk_mul_f32 v[140:141], v[12:13], v[140:141]
	v_addc_co_u32_e32 v145, vcc, 0, v155, vcc
	global_store_dwordx4 v[144:145], v[140:143], off nt
	v_cmp_lt_i32_e32 vcc, -1, v65
	s_and_b32 s0, vcc_lo, 0xffff
	v_pk_mul_f32 v[140:141], v[162:163], v[64:65] op_sel_hi:[1,0]
	v_pk_mul_f32 v[142:143], v[164:165], v[64:65] op_sel_hi:[1,0]
	v_pk_mul_f32 v[140:141], v[8:9], v[140:141]
	v_pk_mul_f32 v[142:143], v[10:11], v[142:143]
	global_store_dwordx4 v[144:145], v[140:143], off offset:1024 nt
	s_cmp_eq_u32 s0, 0
	v_mov_b32_e32 v155, v139
	v_pk_mul_f32 v[140:141], v[158:159], v[64:65] op_sel_hi:[1,0]
	v_pk_mul_f32 v[142:143], v[160:161], v[64:65] op_sel_hi:[1,0]
	v_pk_mul_f32 v[140:141], v[4:5], v[140:141]
	v_pk_mul_f32 v[142:143], v[6:7], v[142:143]
	global_store_dwordx4 v[144:145], v[140:143], off offset:2048 nt
	v_mov_b32_e32 v154, v139
	v_mov_b32_e32 v161, v139
	v_pk_mul_f32 v[140:141], v[156:157], v[64:65] op_sel_hi:[1,0]
	v_pk_mul_f32 v[142:143], v[150:151], v[64:65] op_sel_hi:[1,0]
	v_pk_mul_f32 v[140:141], v[0:1], v[140:141]
	v_pk_mul_f32 v[142:143], v[2:3], v[142:143]
	global_store_dwordx4 v[144:145], v[140:143], off offset:3072 nt
	v_mov_b32_e32 v145, v139
	v_mov_b32_e32 v144, v139
	v_mov_b32_e32 v141, v139
	v_mov_b32_e32 v140, v139
	v_mov_b32_e32 v143, v139
	v_mov_b32_e32 v142, v139
	v_mov_b32_e32 v151, v139
	v_mov_b32_e32 v150, v139
	v_mov_b32_e32 v157, v139
	v_mov_b32_e32 v156, v139
	v_mov_b32_e32 v160, v139
	v_mov_b32_e32 v159, v139
	v_mov_b32_e32 v158, v139
	v_mov_b32_e32 v165, v139
	v_mov_b32_e32 v164, v139
	v_mov_b32_e32 v163, v139
	v_mov_b32_e32 v162, v139
	v_mov_b32_e32 v167, v139
	v_mov_b32_e32 v166, v139
	s_cbranch_scc1 .LBB0_1796
	v_mov_b32_e32 v138, 0
	v_mov_b32_e32 v139, v138
	v_mov_b32_e32 v166, v138
	v_mov_b32_e32 v167, v138
	v_mov_b32_e32 v168, v138
	v_mov_b32_e32 v169, v138
	v_mov_b32_e32 v162, v138
	v_mov_b32_e32 v163, v138
	v_mov_b32_e32 v164, v138
	v_mov_b32_e32 v165, v138
	v_mov_b32_e32 v158, v138
	v_mov_b32_e32 v159, v138
	v_mov_b32_e32 v160, v138
	v_mov_b32_e32 v161, v138
	v_mov_b32_e32 v154, v138
	v_mov_b32_e32 v155, v138
	v_mov_b32_e32 v156, v138
	v_mov_b32_e32 v157, v138
	v_mov_b32_e32 v150, v138
	v_mov_b32_e32 v151, v138
	v_mov_b32_e32 v152, v138
	v_mov_b32_e32 v153, v138
	v_mov_b32_e32 v146, v138
	v_mov_b32_e32 v147, v138
	v_mov_b32_e32 v148, v138
	v_mov_b32_e32 v149, v138
	v_mov_b32_e32 v142, v138
	v_mov_b32_e32 v143, v138
	v_mov_b32_e32 v144, v138
	v_mov_b32_e32 v145, v138
	v_mov_b32_e32 v140, v138
	v_mov_b32_e32 v141, v138

; __device__ __forceinline__ unsigned pk2(float lo, float hi) { unsigned r; asm("v_cvt_pk_bf16_f32 %0, %1, %2" : "=v"(r) : "v"(lo), "v"(hi)); return r; }
; __device__ __forceinline__ float bflo(unsigned u) { return __uint_as_float(u << 16); }
; __device__ __forceinline__ float bfhi(unsigned u) { return __uint_as_float(u & 0xffff0000u); }
; __device__ __forceinline__ float wave_sum(float v) {
; #pragma unroll
;     for (int o = 1; o < 64; o <<= 1) v += __shfl_xor(v, o);
;     return v;
; __device__ __forceinline__ void ph_norm1(const Params& p, int mode, LAS unsigned char* lds) {
;     ...
;             f32x4 v[8];
; #pragma unroll
;             for (int j = 0; j < 8; ++j) { const f32x4 g = gfv[j];
;                 v[j] = (f32x4){bflo(xw[q][j].x), bfhi(xw[q][j].x), bflo(xw[q][j].y), bfhi(xw[q][j].y)} + g * macc[j]; }
;             if (mode == 1) {
;                 bf16_t* xo = (bf16_t*)(p.ws + WS_X) + (size_t)t * DM;
; #pragma unroll
;                 for (int j = 0; j < 8; ++j) { u32x2 w; w.x = pk2(v[j][0], v[j][1]); w.y = pk2(v[j][2], v[j][3]); *(u32x2*)(xo + 4 * lane + 256 * j) = w;
;                     v[j] = (f32x4){bflo(w.x), bfhi(w.x), bflo(w.y), bfhi(w.y)}; }
;             }
;             float ss = 0.f;
; #pragma unroll
;             for (int j = 0; j < 8; ++j) ss += v[j][0] * v[j][0] + v[j][1] * v[j][1] + v[j][2] * v[j][2] + v[j][3] * v[j][3];
;             const float r = 1.0f / sqrtf(wave_sum(ss) * (1.f / DM) + EPS);
.LBB0_1796:
	v_lshlrev_b32_e32 v64, 16, v136
	v_and_b32_e32 v65, 0xffff0000, v136
	v_pk_fma_f32 v[166:167], v[60:61], v[166:167], v[64:65]
	v_lshlrev_b32_e32 v64, 16, v134
	v_and_b32_e32 v65, 0xffff0000, v134
	v_pk_fma_f32 v[162:163], v[56:57], v[162:163], v[64:65]
	v_lshlrev_b32_e32 v64, 16, v132
	v_and_b32_e32 v65, 0xffff0000, v132
	v_pk_fma_f32 v[158:159], v[52:53], v[158:159], v[64:65]
	v_lshlrev_b32_e32 v64, 16, v130
	v_and_b32_e32 v65, 0xffff0000, v130
	v_pk_fma_f32 v[154:155], v[48:49], v[154:155], v[64:65]
	v_lshlrev_b32_e32 v64, 16, v128
	v_and_b32_e32 v65, 0xffff0000, v128
	v_pk_fma_f32 v[150:151], v[44:45], v[150:151], v[64:65]
	v_lshlrev_b32_e32 v64, 16, v126
	v_and_b32_e32 v65, 0xffff0000, v126
	v_pk_fma_f32 v[146:147], v[40:41], v[146:147], v[64:65]
	v_lshlrev_b32_e32 v64, 16, v124
	v_and_b32_e32 v65, 0xffff0000, v124
	v_pk_fma_f32 v[142:143], v[36:37], v[142:143], v[64:65]
	v_lshlrev_b32_e32 v64, 16, v122
	v_and_b32_e32 v65, 0xffff0000, v122
	v_lshlrev_b32_e32 v136, 16, v137
	v_and_b32_e32 v137, 0xffff0000, v137
	v_lshlrev_b32_e32 v134, 16, v135
	v_and_b32_e32 v135, 0xffff0000, v135
	v_pk_fma_f32 v[140:141], v[32:33], v[140:141], v[64:65]
	v_mul_f32_e32 v64, v167, v167
	v_mul_f32_e32 v65, v163, v163
	v_pk_fma_f32 v[136:137], v[62:63], v[168:169], v[136:137]
	v_pk_fma_f32 v[134:135], v[58:59], v[164:165], v[134:135]
	v_fmac_f32_e32 v64, v166, v166
	v_fmac_f32_e32 v65, v162, v162
	v_fmac_f32_e32 v64, v136, v136
	v_fmac_f32_e32 v65, v134, v134
	v_fmac_f32_e32 v64, v137, v137
	v_fmac_f32_e32 v65, v135, v135
	v_lshlrev_b32_e32 v132, 16, v133
	v_and_b32_e32 v133, 0xffff0000, v133
	v_add_f32_e32 v64, v64, v65
	v_mul_f32_e32 v65, v159, v159
	v_pk_fma_f32 v[132:133], v[54:55], v[160:161], v[132:133]
	v_fmac_f32_e32 v65, v158, v158
	v_fmac_f32_e32 v65, v132, v132
	v_fmac_f32_e32 v65, v133, v133
	v_lshlrev_b32_e32 v130, 16, v131
	v_and_b32_e32 v131, 0xffff0000, v131
	v_add_f32_e32 v64, v65, v64
	v_mul_f32_e32 v65, v155, v155
	v_pk_fma_f32 v[130:131], v[50:51], v[156:157], v[130:131]
	v_fmac_f32_e32 v65, v154, v154
	v_fmac_f32_e32 v65, v130, v130
	v_fmac_f32_e32 v65, v131, v131
	v_lshlrev_b32_e32 v128, 16, v129
	v_and_b32_e32 v129, 0xffff0000, v129
	v_add_f32_e32 v64, v65, v64
	v_mul_f32_e32 v65, v151, v151
	v_pk_fma_f32 v[128:129], v[46:47], v[152:153], v[128:129]
	v_fmac_f32_e32 v65, v150, v150
	v_fmac_f32_e32 v65, v128, v128
	v_fmac_f32_e32 v65, v129, v129
	v_lshlrev_b32_e32 v126, 16, v127
	v_and_b32_e32 v127, 0xffff0000, v127
	v_add_f32_e32 v64, v65, v64
	v_mul_f32_e32 v65, v147, v147
	v_pk_fma_f32 v[126:127], v[42:43], v[148:149], v[126:127]
	v_fmac_f32_e32 v65, v146, v146
	v_lshlrev_b32_e32 v122, 16, v123
	v_and_b32_e32 v123, 0xffff0000, v123
	v_fmac_f32_e32 v65, v126, v126
	v_lshlrev_b32_e32 v124, 16, v125
	v_and_b32_e32 v125, 0xffff0000, v125
	v_pk_fma_f32 v[138:139], v[34:35], v[138:139], v[122:123]
	v_fmac_f32_e32 v65, v127, v127
	v_mov_b32_e32 v122, v141
	v_mov_b32_e32 v123, v143
	v_pk_fma_f32 v[144:145], v[38:39], v[144:145], v[124:125]
	v_add_f32_e32 v69, v65, v64
	v_mov_b32_e32 v64, v140
	v_mov_b32_e32 v65, v142
	v_pk_mul_f32 v[122:123], v[122:123], v[122:123]
	s_nop 0
	v_pk_fma_f32 v[64:65], v[64:65], v[64:65], v[122:123]
	v_mov_b32_e32 v122, v138
	v_mov_b32_e32 v123, v144
	v_pk_fma_f32 v[64:65], v[122:123], v[122:123], v[64:65]
	v_mov_b32_e32 v122, v139
	v_mov_b32_e32 v123, v145
	v_pk_fma_f32 v[64:65], v[122:123], v[122:123], v[64:65]
	s_nop 0
	v_add_f32_e32 v65, v65, v69
	v_add_f32_e32 v64, v64, v65
	s_waitcnt lgkmcnt(0)
	s_nop 1
	v_add_f32_dpp v64, v64, v64 quad_perm:[1,0,3,2] row_mask:0xf bank_mask:0xf
	s_waitcnt lgkmcnt(0)
	s_nop 1
	v_add_f32_dpp v64, v64, v64 quad_perm:[2,3,0,1] row_mask:0xf bank_mask:0xf
	s_waitcnt lgkmcnt(0)
	s_nop 1
	v_add_f32_dpp v64, v64, v64 row_half_mirror row_mask:0xf bank_mask:0xf
	s_waitcnt lgkmcnt(0)
	s_nop 1
	v_add_f32_dpp v64, v64, v64 row_mirror row_mask:0xf bank_mask:0xf
	v_mov_b32_e32 v65, v64
	s_nop 1
	v_permlane16_swap_b32_e32 v64, v65
	s_waitcnt lgkmcnt(0)
	v_add_f32_e32 v64, v64, v65
	v_mov_b32_e32 v65, v64
	s_nop 1
	v_permlane32_swap_b32_e32 v64, v65
	s_waitcnt lgkmcnt(0)
; __device__ __forceinline__ void ph_norm1(const Params& p, int mode, LAS unsigned char* lds) {
;     ...
;             f32x4 macc[8];
; #pragma unroll
;             for (int j = 0; j < 8; ++j) macc[j] = (f32x4){0.f, 0.f, 0.f, 0.f};
;             unsigned m = (unsigned)(__ballot(myslot[q] >= 0) & 0xffffull);
;             while (m) {
;     ...
;             const float r = 1.0f / sqrtf(wave_sum(ss) * (1.f / DM) + EPS);
;             asm volatile("" ::: "memory");
;             if (mode == 2) {
;                 float* o = p.out + (size_t)t * DM;
; #pragma unroll
;                 for (int j = 0; j < 8; ++j) { const f32x4 g = fgv[j]; __builtin_nontemporal_store(v[j] * r * g, (f32x4*)(o + 4 * lane + 256 * j)); }
	v_add_f32_e32 v64, v64, v65
	v_fmamk_f32 v64, v64, 0x3a000000, v192
	v_mul_f32_e32 v65, 0x4f800000, v64
	v_cmp_gt_f32_e32 vcc, s10, v64
	s_nop 1
	v_cndmask_b32_e32 v64, v64, v65, vcc
	v_sqrt_f32_e32 v65, v64
	s_nop 0
	v_add_u32_e32 v69, -1, v65
	v_fma_f32 v122, -v69, v65, v64
	v_cmp_ge_f32_e64 s[0:1], 0, v122
	v_add_u32_e32 v122, 1, v65
	s_nop 0
	v_cndmask_b32_e64 v69, v65, v69, s[0:1]
	v_fma_f32 v65, -v122, v65, v64
	v_cmp_lt_f32_e64 s[0:1], 0, v65
	s_nop 1
	v_cndmask_b32_e64 v65, v69, v122, s[0:1]
	v_mul_f32_e32 v69, 0x37800000, v65
	v_cndmask_b32_e32 v65, v65, v69, vcc
	v_cmp_class_f32_e32 vcc, v64, v193
	v_or_b32_e32 v122, 1, v68
	s_nop 0
	v_cndmask_b32_e32 v64, v65, v64, vcc
	v_div_scale_f32 v69, s[0:1], v64, v64, 1.0
	v_rcp_f32_e32 v123, v69
	v_mov_b32_e32 v65, 0
	v_fma_f32 v124, -v69, v123, 1.0
	v_fmac_f32_e32 v123, v124, v123
	v_div_scale_f32 v124, vcc, 1.0, v64, 1.0
	v_mul_f32_e32 v125, v124, v123
	v_fma_f32 v148, -v69, v125, v124
	v_fmac_f32_e32 v125, v148, v123
	v_fma_f32 v69, -v69, v125, v124
	v_div_fmas_f32 v69, v69, v123, v125
	v_ashrrev_i32_e32 v123, 31, v122
	v_div_fixup_f32 v64, v69, v64, 1.0
	v_lshlrev_b64 v[122:123], 13, v[122:123]
	v_lshl_add_u64 v[148:149], v[88:89], 0, v[122:123]
	v_pk_mul_f32 v[122:123], v[166:167], v[64:65] op_sel_hi:[1,0]
	v_pk_mul_f32 v[124:125], v[136:137], v[64:65] op_sel_hi:[1,0]
	v_pk_mul_f32 v[122:123], v[28:29], v[122:123]
	v_pk_mul_f32 v[124:125], v[30:31], v[124:125]
	global_store_dwordx4 v[148:149], v[122:125], off nt
	v_mov_b32_e32 v137, v65
	v_mov_b32_e32 v136, v65
	v_pk_mul_f32 v[122:123], v[162:163], v[64:65] op_sel_hi:[1,0]
	v_pk_mul_f32 v[124:125], v[134:135], v[64:65] op_sel_hi:[1,0]
	v_pk_mul_f32 v[122:123], v[24:25], v[122:123]
	v_pk_mul_f32 v[124:125], v[26:27], v[124:125]
	global_store_dwordx4 v[148:149], v[122:125], off offset:1024 nt
	v_mov_b32_e32 v135, v65
	v_mov_b32_e32 v134, v65
	v_pk_mul_f32 v[122:123], v[158:159], v[64:65] op_sel_hi:[1,0]
	v_pk_mul_f32 v[124:125], v[132:133], v[64:65] op_sel_hi:[1,0]
	v_pk_mul_f32 v[122:123], v[20:21], v[122:123]
	v_pk_mul_f32 v[124:125], v[22:23], v[124:125]
	global_store_dwordx4 v[148:149], v[122:125], off offset:2048 nt
	v_mov_b32_e32 v133, v65
	v_mov_b32_e32 v132, v65
	v_pk_mul_f32 v[122:123], v[154:155], v[64:65] op_sel_hi:[1,0]
	v_pk_mul_f32 v[124:125], v[130:131], v[64:65] op_sel_hi:[1,0]
	v_pk_mul_f32 v[122:123], v[16:17], v[122:123]
	v_pk_mul_f32 v[124:125], v[18:19], v[124:125]
	global_store_dwordx4 v[148:149], v[122:125], off offset:3072 nt
	v_mov_b32_e32 v131, v65
	v_mov_b32_e32 v130, v65
	v_pk_mul_f32 v[122:123], v[150:151], v[64:65] op_sel_hi:[1,0]
	v_pk_mul_f32 v[124:125], v[128:129], v[64:65] op_sel_hi:[1,0]
	v_add_co_u32_e32 v128, vcc, s7, v148
	v_pk_mul_f32 v[124:125], v[14:15], v[124:125]
	v_pk_mul_f32 v[122:123], v[12:13], v[122:123]
	v_addc_co_u32_e32 v129, vcc, 0, v149, vcc
	global_store_dwordx4 v[128:129], v[122:125], off nt
	v_cmp_lt_i32_e32 vcc, -1, v66
	s_and_b32 s0, vcc_lo, 0xffff
	v_pk_mul_f32 v[122:123], v[146:147], v[64:65] op_sel_hi:[1,0]
	v_pk_mul_f32 v[124:125], v[126:127], v[64:65] op_sel_hi:[1,0]
	v_pk_mul_f32 v[122:123], v[8:9], v[122:123]
	v_pk_mul_f32 v[124:125], v[10:11], v[124:125]
	global_store_dwordx4 v[128:129], v[122:125], off offset:1024 nt
	s_cmp_eq_u32 s0, 0
	v_mov_b32_e32 v127, v65
	v_pk_mul_f32 v[122:123], v[142:143], v[64:65] op_sel_hi:[1,0]
	v_pk_mul_f32 v[124:125], v[144:145], v[64:65] op_sel_hi:[1,0]
	v_pk_mul_f32 v[122:123], v[4:5], v[122:123]
	v_pk_mul_f32 v[124:125], v[6:7], v[124:125]
	global_store_dwordx4 v[128:129], v[122:125], off offset:2048 nt
	v_mov_b32_e32 v126, v65
	v_mov_b32_e32 v143, v65
	v_pk_mul_f32 v[122:123], v[140:141], v[64:65] op_sel_hi:[1,0]
	v_pk_mul_f32 v[124:125], v[138:139], v[64:65] op_sel_hi:[1,0]
	v_pk_mul_f32 v[122:123], v[0:1], v[122:123]
	v_pk_mul_f32 v[124:125], v[2:3], v[124:125]
	global_store_dwordx4 v[128:129], v[122:125], off offset:3072 nt
	v_mov_b32_e32 v64, v65
	v_mov_b32_e32 v129, v65
	v_mov_b32_e32 v123, v65
	v_mov_b32_e32 v122, v65
	v_mov_b32_e32 v125, v65
	v_mov_b32_e32 v124, v65
	v_mov_b32_e32 v128, v65
	v_mov_b32_e32 v139, v65
	v_mov_b32_e32 v138, v65
	v_mov_b32_e32 v142, v65
	v_mov_b32_e32 v141, v65
	v_mov_b32_e32 v140, v65
	v_mov_b32_e32 v147, v65
	v_mov_b32_e32 v146, v65
	v_mov_b32_e32 v145, v65
	v_mov_b32_e32 v144, v65
	v_mov_b32_e32 v151, v65
	v_mov_b32_e32 v150, v65
	v_mov_b32_e32 v149, v65
	v_mov_b32_e32 v148, v65
	s_cbranch_scc1 .LBB0_1799
	v_mov_b32_e32 v64, 0
	v_mov_b32_e32 v65, v64
	v_mov_b32_e32 v148, v64
	v_mov_b32_e32 v149, v64
	v_mov_b32_e32 v150, v64
	v_mov_b32_e32 v151, v64
	v_mov_b32_e32 v144, v64
	v_mov_b32_e32 v145, v64
	v_mov_b32_e32 v146, v64
	v_mov_b32_e32 v147, v64
	v_mov_b32_e32 v140, v64
	v_mov_b32_e32 v141, v64
	v_mov_b32_e32 v142, v64
	v_mov_b32_e32 v143, v64
	v_mov_b32_e32 v136, v64
	v_mov_b32_e32 v137, v64
	v_mov_b32_e32 v138, v64
	v_mov_b32_e32 v139, v64
	v_mov_b32_e32 v132, v64
	v_mov_b32_e32 v133, v64
	v_mov_b32_e32 v134, v64
	v_mov_b32_e32 v135, v64
	v_mov_b32_e32 v128, v64
	v_mov_b32_e32 v129, v64
	v_mov_b32_e32 v130, v64
	v_mov_b32_e32 v131, v64
	v_mov_b32_e32 v124, v64
	v_mov_b32_e32 v125, v64
	v_mov_b32_e32 v126, v64
	v_mov_b32_e32 v127, v64
	v_mov_b32_e32 v122, v64
	v_mov_b32_e32 v123, v64

; __device__ __forceinline__ unsigned pk2(float lo, float hi) { unsigned r; asm("v_cvt_pk_bf16_f32 %0, %1, %2" : "=v"(r) : "v"(lo), "v"(hi)); return r; }
; __device__ __forceinline__ float bflo(unsigned u) { return __uint_as_float(u << 16); }
; __device__ __forceinline__ float bfhi(unsigned u) { return __uint_as_float(u & 0xffff0000u); }
; __device__ __forceinline__ float wave_sum(float v) {
; #pragma unroll
;     for (int o = 1; o < 64; o <<= 1) v += __shfl_xor(v, o);
;     return v;
; __device__ __forceinline__ void ph_norm1(const Params& p, int mode, LAS unsigned char* lds) {
;     ...
;             f32x4 v[8];
; #pragma unroll
;             for (int j = 0; j < 8; ++j) { const f32x4 g = gfv[j];
;                 v[j] = (f32x4){bflo(xw[q][j].x), bfhi(xw[q][j].x), bflo(xw[q][j].y), bfhi(xw[q][j].y)} + g * macc[j]; }
;             if (mode == 1) {
;                 bf16_t* xo = (bf16_t*)(p.ws + WS_X) + (size_t)t * DM;
; #pragma unroll
;                 for (int j = 0; j < 8; ++j) { u32x2 w; w.x = pk2(v[j][0], v[j][1]); w.y = pk2(v[j][2], v[j][3]); *(u32x2*)(xo + 4 * lane + 256 * j) = w;
;                     v[j] = (f32x4){bflo(w.x), bfhi(w.x), bflo(w.y), bfhi(w.y)}; }
;             }
;             float ss = 0.f;
; #pragma unroll
;             for (int j = 0; j < 8; ++j) ss += v[j][0] * v[j][0] + v[j][1] * v[j][1] + v[j][2] * v[j][2] + v[j][3] * v[j][3];
;             const float r = 1.0f / sqrtf(wave_sum(ss) * (1.f / DM) + EPS);
.LBB0_1799:
	v_lshlrev_b32_e32 v152, 16, v120
	v_and_b32_e32 v153, 0xffff0000, v120
	v_lshlrev_b32_e32 v120, 16, v121
	v_and_b32_e32 v121, 0xffff0000, v121
	v_pk_fma_f32 v[120:121], v[62:63], v[150:151], v[120:121]
	v_lshlrev_b32_e32 v150, 16, v118
	v_and_b32_e32 v151, 0xffff0000, v118
	v_lshlrev_b32_e32 v118, 16, v119
	v_and_b32_e32 v119, 0xffff0000, v119
	v_pk_fma_f32 v[118:119], v[58:59], v[146:147], v[118:119]
	v_lshlrev_b32_e32 v146, 16, v116
	v_and_b32_e32 v147, 0xffff0000, v116
	v_lshlrev_b32_e32 v116, 16, v117
	v_and_b32_e32 v117, 0xffff0000, v117
	v_pk_fma_f32 v[116:117], v[54:55], v[142:143], v[116:117]
	v_lshlrev_b32_e32 v142, 16, v114
	v_and_b32_e32 v143, 0xffff0000, v114
	v_lshlrev_b32_e32 v114, 16, v115
	v_and_b32_e32 v115, 0xffff0000, v115
	v_pk_fma_f32 v[114:115], v[50:51], v[138:139], v[114:115]
	v_lshlrev_b32_e32 v138, 16, v112
	v_and_b32_e32 v139, 0xffff0000, v112
	v_lshlrev_b32_e32 v112, 16, v113
	v_and_b32_e32 v113, 0xffff0000, v113
	v_pk_fma_f32 v[112:113], v[46:47], v[134:135], v[112:113]
	v_lshlrev_b32_e32 v134, 16, v110
	v_and_b32_e32 v135, 0xffff0000, v110
	v_lshlrev_b32_e32 v110, 16, v111
	v_and_b32_e32 v111, 0xffff0000, v111
	v_pk_fma_f32 v[110:111], v[42:43], v[130:131], v[110:111]
	v_lshlrev_b32_e32 v130, 16, v108
	v_and_b32_e32 v131, 0xffff0000, v108
	v_lshlrev_b32_e32 v108, 16, v109
	v_and_b32_e32 v109, 0xffff0000, v109
	v_pk_fma_f32 v[148:149], v[60:61], v[148:149], v[152:153]
	v_pk_fma_f32 v[144:145], v[56:57], v[144:145], v[150:151]
	v_pk_fma_f32 v[126:127], v[38:39], v[126:127], v[108:109]
	v_lshlrev_b32_e32 v108, 16, v106
	v_and_b32_e32 v109, 0xffff0000, v106
	v_lshlrev_b32_e32 v106, 16, v107
	v_and_b32_e32 v107, 0xffff0000, v107
	v_pk_fma_f32 v[124:125], v[36:37], v[124:125], v[130:131]
	v_pk_fma_f32 v[130:131], v[34:35], v[64:65], v[106:107]
	v_mul_f32_e32 v64, v149, v149
	v_mul_f32_e32 v65, v145, v145
	v_fmac_f32_e32 v64, v148, v148
	v_fmac_f32_e32 v65, v144, v144
	v_fmac_f32_e32 v64, v120, v120
	v_fmac_f32_e32 v65, v118, v118
	v_pk_fma_f32 v[140:141], v[52:53], v[140:141], v[146:147]
	v_fmac_f32_e32 v64, v121, v121
	v_fmac_f32_e32 v65, v119, v119
	v_add_f32_e32 v64, v64, v65
	v_mul_f32_e32 v65, v141, v141
	v_fmac_f32_e32 v65, v140, v140
	v_fmac_f32_e32 v65, v116, v116
	v_pk_fma_f32 v[136:137], v[48:49], v[136:137], v[142:143]
	v_fmac_f32_e32 v65, v117, v117
	v_add_f32_e32 v64, v65, v64
	v_mul_f32_e32 v65, v137, v137
	v_fmac_f32_e32 v65, v136, v136
	v_fmac_f32_e32 v65, v114, v114
	v_pk_fma_f32 v[132:133], v[44:45], v[132:133], v[138:139]
	v_fmac_f32_e32 v65, v115, v115
	v_add_f32_e32 v64, v65, v64
	v_mul_f32_e32 v65, v133, v133
	v_fmac_f32_e32 v65, v132, v132
	v_fmac_f32_e32 v65, v112, v112
	v_pk_fma_f32 v[128:129], v[40:41], v[128:129], v[134:135]
	v_fmac_f32_e32 v65, v113, v113
	v_add_f32_e32 v64, v65, v64
	v_mul_f32_e32 v65, v129, v129
	v_fmac_f32_e32 v65, v128, v128
	v_pk_fma_f32 v[122:123], v[32:33], v[122:123], v[108:109]
	v_fmac_f32_e32 v65, v110, v110
	v_fmac_f32_e32 v65, v111, v111
	v_mov_b32_e32 v106, v123
	v_mov_b32_e32 v107, v125
	v_add_f32_e32 v66, v65, v64
	v_mov_b32_e32 v64, v122
	v_mov_b32_e32 v65, v124
	v_pk_mul_f32 v[106:107], v[106:107], v[106:107]
	s_nop 0
	v_pk_fma_f32 v[64:65], v[64:65], v[64:65], v[106:107]
	v_mov_b32_e32 v106, v130
	v_mov_b32_e32 v107, v126
	v_pk_fma_f32 v[64:65], v[106:107], v[106:107], v[64:65]
	v_mov_b32_e32 v106, v131
	v_mov_b32_e32 v107, v127
	v_pk_fma_f32 v[64:65], v[106:107], v[106:107], v[64:65]
	v_or_b32_e32 v106, 2, v68
	v_add_f32_e32 v65, v65, v66
	v_add_f32_e32 v64, v64, v65
	s_waitcnt lgkmcnt(0)
	s_nop 1
	v_add_f32_dpp v64, v64, v64 quad_perm:[1,0,3,2] row_mask:0xf bank_mask:0xf
	s_waitcnt lgkmcnt(0)
	s_nop 1
	v_add_f32_dpp v64, v64, v64 quad_perm:[2,3,0,1] row_mask:0xf bank_mask:0xf
	s_waitcnt lgkmcnt(0)
	s_nop 1
	v_add_f32_dpp v64, v64, v64 row_half_mirror row_mask:0xf bank_mask:0xf
	s_waitcnt lgkmcnt(0)
	s_nop 1
	v_add_f32_dpp v64, v64, v64 row_mirror row_mask:0xf bank_mask:0xf
	v_mov_b32_e32 v65, v64
	s_nop 1
	v_permlane16_swap_b32_e32 v64, v65
	s_waitcnt lgkmcnt(0)
	v_add_f32_e32 v64, v64, v65
	v_mov_b32_e32 v65, v64
	s_nop 1
	v_permlane32_swap_b32_e32 v64, v65
	s_waitcnt lgkmcnt(0)
; __device__ __forceinline__ void ph_norm1(const Params& p, int mode, LAS unsigned char* lds) {
;     ...
;             f32x4 macc[8];
; #pragma unroll
;             for (int j = 0; j < 8; ++j) macc[j] = (f32x4){0.f, 0.f, 0.f, 0.f};
;             unsigned m = (unsigned)(__ballot(myslot[q] >= 0) & 0xffffull);
;             while (m) {
;     ...
;             const float r = 1.0f / sqrtf(wave_sum(ss) * (1.f / DM) + EPS);
;             asm volatile("" ::: "memory");
;             if (mode == 2) {
;                 float* o = p.out + (size_t)t * DM;
; #pragma unroll
;                 for (int j = 0; j < 8; ++j) { const f32x4 g = fgv[j]; __builtin_nontemporal_store(v[j] * r * g, (f32x4*)(o + 4 * lane + 256 * j)); }
	v_add_f32_e32 v64, v64, v65
	v_fmamk_f32 v64, v64, 0x3a000000, v192
	v_mul_f32_e32 v65, 0x4f800000, v64
	v_cmp_gt_f32_e32 vcc, s10, v64
	s_nop 1
	v_cndmask_b32_e32 v64, v64, v65, vcc
	v_sqrt_f32_e32 v65, v64
	s_nop 0
	v_add_u32_e32 v66, -1, v65
	v_fma_f32 v69, -v66, v65, v64
	v_cmp_ge_f32_e64 s[0:1], 0, v69
	v_add_u32_e32 v69, 1, v65
	s_nop 0
	v_cndmask_b32_e64 v66, v65, v66, s[0:1]
	v_fma_f32 v65, -v69, v65, v64
	v_cmp_lt_f32_e64 s[0:1], 0, v65
	s_nop 1
	v_cndmask_b32_e64 v65, v66, v69, s[0:1]
	v_mul_f32_e32 v66, 0x37800000, v65
	v_cndmask_b32_e32 v65, v65, v66, vcc
	v_cmp_class_f32_e32 vcc, v64, v193
	s_nop 1
	v_cndmask_b32_e32 v64, v65, v64, vcc
	v_div_scale_f32 v66, s[0:1], v64, v64, 1.0
	v_rcp_f32_e32 v69, v66
	v_mov_b32_e32 v65, 0
	v_fma_f32 v107, -v66, v69, 1.0
	v_fmac_f32_e32 v69, v107, v69
	v_div_scale_f32 v107, vcc, 1.0, v64, 1.0
	v_mul_f32_e32 v108, v107, v69
	v_fma_f32 v109, -v66, v108, v107
	v_fmac_f32_e32 v108, v109, v69
	v_fma_f32 v66, -v66, v108, v107
	v_div_fmas_f32 v66, v66, v69, v108
	v_ashrrev_i32_e32 v107, 31, v106
	v_div_fixup_f32 v64, v66, v64, 1.0
	v_lshlrev_b64 v[106:107], 13, v[106:107]
	v_lshl_add_u64 v[134:135], v[88:89], 0, v[106:107]
	v_pk_mul_f32 v[106:107], v[148:149], v[64:65] op_sel_hi:[1,0]
	v_pk_mul_f32 v[108:109], v[120:121], v[64:65] op_sel_hi:[1,0]
	v_pk_mul_f32 v[106:107], v[28:29], v[106:107]
	v_pk_mul_f32 v[108:109], v[30:31], v[108:109]
	global_store_dwordx4 v[134:135], v[106:109], off nt
	v_mov_b32_e32 v121, v65
	v_mov_b32_e32 v120, v65
	v_pk_mul_f32 v[106:107], v[144:145], v[64:65] op_sel_hi:[1,0]
	v_pk_mul_f32 v[108:109], v[118:119], v[64:65] op_sel_hi:[1,0]
	v_pk_mul_f32 v[106:107], v[24:25], v[106:107]
	v_pk_mul_f32 v[108:109], v[26:27], v[108:109]
	global_store_dwordx4 v[134:135], v[106:109], off offset:1024 nt
	v_mov_b32_e32 v119, v65
	v_mov_b32_e32 v118, v65
	v_pk_mul_f32 v[106:107], v[140:141], v[64:65] op_sel_hi:[1,0]
	v_pk_mul_f32 v[108:109], v[116:117], v[64:65] op_sel_hi:[1,0]
	v_pk_mul_f32 v[106:107], v[20:21], v[106:107]
	v_pk_mul_f32 v[108:109], v[22:23], v[108:109]
	global_store_dwordx4 v[134:135], v[106:109], off offset:2048 nt
	v_mov_b32_e32 v117, v65
	v_mov_b32_e32 v116, v65
	v_pk_mul_f32 v[106:107], v[136:137], v[64:65] op_sel_hi:[1,0]
	v_pk_mul_f32 v[108:109], v[114:115], v[64:65] op_sel_hi:[1,0]
	v_pk_mul_f32 v[106:107], v[16:17], v[106:107]
	v_pk_mul_f32 v[108:109], v[18:19], v[108:109]
	global_store_dwordx4 v[134:135], v[106:109], off offset:3072 nt
	v_mov_b32_e32 v115, v65
	v_mov_b32_e32 v114, v65
	v_pk_mul_f32 v[106:107], v[132:133], v[64:65] op_sel_hi:[1,0]
	v_pk_mul_f32 v[108:109], v[112:113], v[64:65] op_sel_hi:[1,0]
	v_add_co_u32_e32 v112, vcc, s7, v134
	v_pk_mul_f32 v[108:109], v[14:15], v[108:109]
	v_pk_mul_f32 v[106:107], v[12:13], v[106:107]
	v_addc_co_u32_e32 v113, vcc, 0, v135, vcc
	global_store_dwordx4 v[112:113], v[106:109], off nt
	v_cmp_lt_i32_e32 vcc, -1, v67
	s_and_b32 s0, vcc_lo, 0xffff
	v_pk_mul_f32 v[106:107], v[128:129], v[64:65] op_sel_hi:[1,0]
	v_pk_mul_f32 v[108:109], v[110:111], v[64:65] op_sel_hi:[1,0]
	v_pk_mul_f32 v[106:107], v[8:9], v[106:107]
	v_pk_mul_f32 v[108:109], v[10:11], v[108:109]
	global_store_dwordx4 v[112:113], v[106:109], off offset:1024 nt
	s_cmp_eq_u32 s0, 0
	v_mov_b32_e32 v111, v65
	v_pk_mul_f32 v[106:107], v[124:125], v[64:65] op_sel_hi:[1,0]
	v_pk_mul_f32 v[108:109], v[126:127], v[64:65] op_sel_hi:[1,0]
	v_pk_mul_f32 v[106:107], v[4:5], v[106:107]
	v_pk_mul_f32 v[108:109], v[6:7], v[108:109]
	global_store_dwordx4 v[112:113], v[106:109], off offset:2048 nt
	v_mov_b32_e32 v110, v65
	v_mov_b32_e32 v127, v65
	v_pk_mul_f32 v[106:107], v[122:123], v[64:65] op_sel_hi:[1,0]
	v_pk_mul_f32 v[108:109], v[130:131], v[64:65] op_sel_hi:[1,0]
	v_pk_mul_f32 v[106:107], v[0:1], v[106:107]
	v_pk_mul_f32 v[108:109], v[2:3], v[108:109]
	global_store_dwordx4 v[112:113], v[106:109], off offset:3072 nt
	v_mov_b32_e32 v64, v65
	v_mov_b32_e32 v113, v65
	v_mov_b32_e32 v107, v65
	v_mov_b32_e32 v106, v65
	v_mov_b32_e32 v109, v65
	v_mov_b32_e32 v108, v65
	v_mov_b32_e32 v112, v65
	v_mov_b32_e32 v123, v65
	v_mov_b32_e32 v122, v65
	v_mov_b32_e32 v126, v65
	v_mov_b32_e32 v125, v65
	v_mov_b32_e32 v124, v65
	v_mov_b32_e32 v131, v65
	v_mov_b32_e32 v130, v65
	v_mov_b32_e32 v129, v65
	v_mov_b32_e32 v128, v65
	v_mov_b32_e32 v135, v65
	v_mov_b32_e32 v134, v65
	v_mov_b32_e32 v133, v65
	v_mov_b32_e32 v132, v65
	s_cbranch_scc1 .LBB0_1789
	v_mov_b32_e32 v64, 0
	v_mov_b32_e32 v65, v64
	v_mov_b32_e32 v132, v64
	v_mov_b32_e32 v133, v64
	v_mov_b32_e32 v134, v64
	v_mov_b32_e32 v135, v64
	v_mov_b32_e32 v128, v64
	v_mov_b32_e32 v129, v64
	v_mov_b32_e32 v130, v64
	v_mov_b32_e32 v131, v64
	v_mov_b32_e32 v124, v64
	v_mov_b32_e32 v125, v64
	v_mov_b32_e32 v126, v64
	v_mov_b32_e32 v127, v64
	v_mov_b32_e32 v120, v64
	v_mov_b32_e32 v121, v64
	v_mov_b32_e32 v122, v64
	v_mov_b32_e32 v123, v64
	v_mov_b32_e32 v116, v64
	v_mov_b32_e32 v117, v64
	v_mov_b32_e32 v118, v64
	v_mov_b32_e32 v119, v64
	v_mov_b32_e32 v112, v64
	v_mov_b32_e32 v113, v64
	v_mov_b32_e32 v114, v64
	v_mov_b32_e32 v115, v64
	v_mov_b32_e32 v108, v64
	v_mov_b32_e32 v109, v64
	v_mov_b32_e32 v110, v64
	v_mov_b32_e32 v111, v64
	v_mov_b32_e32 v106, v64
	v_mov_b32_e32 v107, v64
